# GEMM mainloops: back-to-back s_setprio 0 / s_setprio 1 pairs between the two MFMA groups of a sub-phase removed
# speedup vs baseline: 1.0141x; 1.0055x over previous
; #define PG8_STAGE_B(bufoff, gbase) do { _Pragma("unroll") for (int _i = 0; _i < 2; ++_i) \
;         __builtin_amdgcn_global_load_lds((const unsigned*)((const char*)(gbase) + voffB[_i]), (LAS unsigned*)(lds + (bufoff) + ldsw + _i * 8192), 16, 0, 0); } while (0)
; #define PG8_STAGE_A(bufoff, gbase, UA) do { _Pragma("unroll") for (int _i = 0; _i < 2; ++_i) \
;         __builtin_amdgcn_global_load_lds((const unsigned*)((const char*)(gbase) + (UA)[_i]), (LAS unsigned*)(lds + (bufoff) + ldsw + _i * 8192), 16, 0, 0); } while (0)
; #define PG8_LDA(dst, b, h) do { _Pragma("unroll") for (int m = 0; m < 4; ++m) dst[m] = PG8_LD8(lds + PG8_SA(b, h) + aoff + m * 2048); } while (0)
; #define PG8_LDB(dst, b, h) do { _Pragma("unroll") for (int n = 0; n < 2; ++n) dst[n] = PG8_LD8(lds + PG8_SB(b, h) + boff + n * 2048); } while (0)
; #define PG8_WAIT_V(n) asm volatile("s_waitcnt vmcnt(" #n ")" ::: "memory")
; #define PG8_WAIT_L(n) asm volatile("s_waitcnt lgkmcnt(" #n ")" ::: "memory")
; #define PG8_BAR __builtin_amdgcn_s_barrier()
; #define PG8_SCHED __builtin_amdgcn_sched_barrier(0)
; template <class Epi, class Sched, bool GATHER, bool FP8 = false>
; __device__ __forceinline__ void gemm_phase(LAS unsigned char* lds, const Gemm g, const Sched& S, const Epi& E, const int wave_s) {
;     ...
;             PG8_LDB(B0, 0, 0); PG8_LDB(B1, 0, 1); PG8_SCHED; PG8_LDA(At, 0, 0); PG8_STAGE_A(PG8_SA(1, 1), a1, uAc[1]);
;             PG8_WAIT_V(8); PG8_WAIT_L(0); PG8_BAR; PG8_MMA(0, 0, At, B0); PG8_MMA(0, 1, At, B1); PG8_BAR; PG8_SCHED;
;             PG8_LDA(At, 0, 1); PG8_STAGE_B(PG8_SB(0, 0), b2); PG8_STAGE_B(PG8_SB(0, 1), b2 + hstepB); PG8_STAGE_A(PG8_SA(0, 0), a2, u2[0]);
;             PG8_WAIT_V(8); PG8_WAIT_L(0); PG8_BAR; PG8_MMA(1, 0, At, B0); PG8_MMA(1, 1, At, B1); PG8_BAR; PG8_SCHED;
.LBB0_204:
	s_add_u32 s2, s42, 0x80
	s_addc_u32 s3, s43, 0
	s_cmp_eq_u32 s60, 4
	s_cselect_b32 s47, s15, s3
	s_cselect_b32 s46, s59, s2
	s_cselect_b32 s45, s13, s1
	s_cselect_b32 s44, s58, s0
	s_add_i32 s61, 0, 0x10000
	s_add_i32 s62, 0, 0x14000
	v_add_u32_e32 v0, s61, v195
	v_add_u32_e32 v12, s62, v195
	ds_read_b128 v[16:19], v0
	ds_read_b128 v[20:23], v0 offset:1024
	ds_read_b128 v[24:27], v0 offset:2048
	ds_read_b128 v[28:31], v0 offset:3072
	ds_read_b128 v[0:3], v12
	ds_read_b128 v[4:7], v12 offset:1024
	ds_read_b128 v[8:11], v12 offset:2048
	ds_read_b128 v[12:15], v12 offset:3072
	v_lshl_add_u64 v[164:165], s[42:43], 0, v[184:185]
	s_add_i32 m0, s49, 0xc000
	ds_read_b128 v[186:189], v212
	ds_read_b128 v[190:193], v212 offset:1024
	ds_read_b128 v[214:217], v212 offset:2048
	ds_read_b128 v[218:221], v212 offset:3072
	ds_read_b128 v[222:225], v212 offset:4096
	ds_read_b128 v[226:229], v212 offset:5120
	ds_read_b128 v[230:233], v212 offset:6144
	ds_read_b128 v[234:237], v212 offset:7168
	global_load_lds_dwordx4 v[164:165], off
	v_lshl_add_u64 v[164:165], s[42:43], 0, v[182:183]
	s_add_i32 m0, s49, 0xe000
	s_nop 0
	global_load_lds_dwordx4 v[164:165], off
	s_waitcnt vmcnt(8)
	s_waitcnt lgkmcnt(0)
	s_barrier
	s_setprio 1
	s_waitcnt lgkmcnt(0)
	v_mfma_scale_f32_16x16x128_f8f6f4 v[158:161], v[16:23], v[186:193], v[158:161], v163, v196 op_sel_hi:[0,0,0]
	v_mfma_scale_f32_16x16x128_f8f6f4 v[154:157], v[24:31], v[186:193], v[154:157], v163, v196 op_sel_hi:[0,0,0]
	v_mfma_scale_f32_16x16x128_f8f6f4 v[148:151], v[16:23], v[214:221], v[148:151], v163, v196 op_sel_hi:[0,0,0]
	v_mfma_scale_f32_16x16x128_f8f6f4 v[140:143], v[24:31], v[214:221], v[140:143], v163, v196 op_sel_hi:[0,0,0]
	v_mfma_scale_f32_16x16x128_f8f6f4 v[132:135], v[16:23], v[222:229], v[132:135], v163, v196 op_sel_hi:[0,0,0]
	v_mfma_scale_f32_16x16x128_f8f6f4 v[124:127], v[24:31], v[222:229], v[124:127], v163, v196 op_sel_hi:[0,0,0]
	v_mfma_scale_f32_16x16x128_f8f6f4 v[116:119], v[16:23], v[230:237], v[116:119], v163, v196 op_sel_hi:[0,0,0]
	v_mfma_scale_f32_16x16x128_f8f6f4 v[108:111], v[24:31], v[230:237], v[108:111], v163, v196 op_sel_hi:[0,0,0]
	v_mfma_scale_f32_16x16x128_f8f6f4 v[144:147], v[0:7], v[186:193], v[144:147], v163, v196 op_sel_hi:[0,0,0]
	v_mfma_scale_f32_16x16x128_f8f6f4 v[136:139], v[8:15], v[186:193], v[136:139], v163, v196 op_sel_hi:[0,0,0]
	v_mfma_scale_f32_16x16x128_f8f6f4 v[128:131], v[0:7], v[214:221], v[128:131], v163, v196 op_sel_hi:[0,0,0]
	v_mfma_scale_f32_16x16x128_f8f6f4 v[120:123], v[8:15], v[214:221], v[120:123], v163, v196 op_sel_hi:[0,0,0]
	v_mfma_scale_f32_16x16x128_f8f6f4 v[112:115], v[0:7], v[222:229], v[112:115], v163, v196 op_sel_hi:[0,0,0]
	v_mfma_scale_f32_16x16x128_f8f6f4 v[104:107], v[8:15], v[222:229], v[104:107], v163, v196 op_sel_hi:[0,0,0]
	v_mfma_scale_f32_16x16x128_f8f6f4 v[100:103], v[0:7], v[230:237], v[100:103], v163, v196 op_sel_hi:[0,0,0]
	v_mfma_scale_f32_16x16x128_f8f6f4 v[96:99], v[8:15], v[230:237], v[96:99], v163, v196 op_sel_hi:[0,0,0]
	s_setprio 0
	s_barrier
	s_add_i32 s2, s61, s5
	v_lshl_add_u64 v[186:187], s[44:45], 0, v[152:153]
	s_mov_b32 m0, s2
	ds_read_b128 v[214:217], v212 offset:16384
	ds_read_b128 v[218:221], v212 offset:17408
	ds_read_b128 v[222:225], v212 offset:18432
	ds_read_b128 v[226:229], v212 offset:19456
	ds_read_b128 v[230:233], v212 offset:20480
	ds_read_b128 v[234:237], v212 offset:21504
	ds_read_b128 v[238:241], v212 offset:22528
	ds_read_b128 v[242:245], v212 offset:23552
	global_load_lds_dwordx4 v[186:187], off
	s_add_i32 m0, s2, 0x2000
	s_add_u32 s64, s44, 0x20000
	v_lshl_add_u64 v[188:189], s[44:45], 0, v[172:173]
	s_addc_u32 s65, s45, 0
	s_add_i32 s2, s62, s5
	global_load_lds_dwordx4 v[188:189], off
	v_lshl_add_u64 v[164:165], s[64:65], 0, v[152:153]
	s_mov_b32 m0, s2
	v_lshl_add_u64 v[190:191], s[46:47], 0, v[174:175]
	global_load_lds_dwordx4 v[164:165], off
	v_lshl_add_u64 v[164:165], s[64:65], 0, v[172:173]
	s_add_i32 m0, s2, 0x2000
	v_lshl_add_u64 v[192:193], s[46:47], 0, v[176:177]
	global_load_lds_dwordx4 v[164:165], off
	s_mov_b32 m0, s49
	s_nop 0
	global_load_lds_dwordx4 v[190:191], off
	s_mov_b32 m0, s50
	s_nop 0
	global_load_lds_dwordx4 v[192:193], off
	s_waitcnt vmcnt(8)
	s_waitcnt lgkmcnt(0)
	s_barrier
	s_setprio 1
	s_waitcnt lgkmcnt(0)
	v_mfma_scale_f32_16x16x128_f8f6f4 v[92:95], v[16:23], v[214:221], v[92:95], v163, v196 op_sel_hi:[0,0,0]
	v_mfma_scale_f32_16x16x128_f8f6f4 v[88:91], v[24:31], v[214:221], v[88:91], v163, v196 op_sel_hi:[0,0,0]
	v_mfma_scale_f32_16x16x128_f8f6f4 v[76:79], v[16:23], v[222:229], v[76:79], v163, v196 op_sel_hi:[0,0,0]
	v_mfma_scale_f32_16x16x128_f8f6f4 v[68:71], v[24:31], v[222:229], v[68:71], v163, v196 op_sel_hi:[0,0,0]
	v_mfma_scale_f32_16x16x128_f8f6f4 v[52:55], v[16:23], v[230:237], v[52:55], v163, v196 op_sel_hi:[0,0,0]
	v_mfma_scale_f32_16x16x128_f8f6f4 v[44:47], v[24:31], v[230:237], v[44:47], v163, v196 op_sel_hi:[0,0,0]
	v_mfma_scale_f32_16x16x128_f8f6f4 v[36:39], v[16:23], v[238:245], v[36:39], v163, v196 op_sel_hi:[0,0,0]
	v_mfma_scale_f32_16x16x128_f8f6f4 v[32:35], v[24:31], v[238:245], v[32:35], v163, v196 op_sel_hi:[0,0,0]
	v_mfma_scale_f32_16x16x128_f8f6f4 v[72:75], v[0:7], v[214:221], v[72:75], v163, v196 op_sel_hi:[0,0,0]
	v_mfma_scale_f32_16x16x128_f8f6f4 v[64:67], v[8:15], v[214:221], v[64:67], v163, v196 op_sel_hi:[0,0,0]
	v_mfma_scale_f32_16x16x128_f8f6f4 v[48:51], v[0:7], v[222:229], v[48:51], v163, v196 op_sel_hi:[0,0,0]
	v_mfma_scale_f32_16x16x128_f8f6f4 v[40:43], v[8:15], v[222:229], v[40:43], v163, v196 op_sel_hi:[0,0,0]
	v_mfma_scale_f32_16x16x128_f8f6f4 v[84:87], v[0:7], v[230:237], v[84:87], v163, v196 op_sel_hi:[0,0,0]
	v_mfma_scale_f32_16x16x128_f8f6f4 v[80:83], v[8:15], v[230:237], v[80:83], v163, v196 op_sel_hi:[0,0,0]
	v_mfma_scale_f32_16x16x128_f8f6f4 v[60:63], v[0:7], v[238:245], v[60:63], v163, v196 op_sel_hi:[0,0,0]
	v_mfma_scale_f32_16x16x128_f8f6f4 v[56:59], v[8:15], v[238:245], v[56:59], v163, v196 op_sel_hi:[0,0,0]
	s_setprio 0
	s_barrier
; #define PG8_STAGE_B(bufoff, gbase) do { _Pragma("unroll") for (int _i = 0; _i < 2; ++_i) \
;         __builtin_amdgcn_global_load_lds((const unsigned*)((const char*)(gbase) + voffB[_i]), (LAS unsigned*)(lds + (bufoff) + ldsw + _i * 8192), 16, 0, 0); } while (0)
; #define PG8_STAGE_A(bufoff, gbase, UA) do { _Pragma("unroll") for (int _i = 0; _i < 2; ++_i) \
;         __builtin_amdgcn_global_load_lds((const unsigned*)((const char*)(gbase) + (UA)[_i]), (LAS unsigned*)(lds + (bufoff) + ldsw + _i * 8192), 16, 0, 0); } while (0)
; #define PG8_LDA(dst, b, h) do { _Pragma("unroll") for (int m = 0; m < 4; ++m) dst[m] = PG8_LD8(lds + PG8_SA(b, h) + aoff + m * 2048); } while (0)
; #define PG8_LDB(dst, b, h) do { _Pragma("unroll") for (int n = 0; n < 2; ++n) dst[n] = PG8_LD8(lds + PG8_SB(b, h) + boff + n * 2048); } while (0)
; #define PG8_WAIT_V(n) asm volatile("s_waitcnt vmcnt(" #n ")" ::: "memory")
; #define PG8_WAIT_L(n) asm volatile("s_waitcnt lgkmcnt(" #n ")" ::: "memory")
; #define PG8_BAR __builtin_amdgcn_s_barrier()
; #define PG8_SCHED __builtin_amdgcn_sched_barrier(0)
; template <class Epi, class Sched, bool GATHER, bool FP8 = false>
; __device__ __forceinline__ void gemm_phase(LAS unsigned char* lds, const Gemm g, const Sched& S, const Epi& E, const int wave_s) {
;     ...
;             PG8_LDB(B0, 1, 0); PG8_LDB(B1, 1, 1); PG8_SCHED; PG8_LDA(At, 1, 0); PG8_STAGE_A(PG8_SA(0, 1), a2, u2[1]);
;             PG8_WAIT_V(8); PG8_WAIT_L(0); PG8_BAR; PG8_MMA(0, 0, At, B0); PG8_MMA(0, 1, At, B1); PG8_BAR; PG8_SCHED;
;             PG8_LDA(At, 1, 1); PG8_STAGE_B(PG8_SB(1, 0), b3); PG8_STAGE_B(PG8_SB(1, 1), b3 + hstepB); PG8_STAGE_A(PG8_SA(1, 0), a3, u2[0]);
;             PG8_WAIT_V(8); PG8_WAIT_L(0); PG8_BAR; PG8_MMA(1, 0, At, B0); PG8_MMA(1, 1, At, B1); PG8_BAR; PG8_SCHED;
;         }
;         if (wr == 0) PG8_BAR;
	s_add_i32 s2, 0, 0x18000
	s_add_i32 s3, 0, 0x1c000
	v_add_u32_e32 v12, s2, v195
	v_add_u32_e32 v28, s3, v195
	ds_read_b128 v[0:3], v12
	ds_read_b128 v[4:7], v12 offset:1024
	ds_read_b128 v[8:11], v12 offset:2048
	ds_read_b128 v[12:15], v12 offset:3072
	ds_read_b128 v[16:19], v28
	ds_read_b128 v[20:23], v28 offset:1024
	ds_read_b128 v[24:27], v28 offset:2048
	ds_read_b128 v[28:31], v28 offset:3072
	s_mov_b32 m0, s51
	v_lshl_add_u64 v[164:165], s[46:47], 0, v[178:179]
	ds_read_b128 v[214:217], v212 offset:32768
	ds_read_b128 v[218:221], v212 offset:33792
	ds_read_b128 v[222:225], v212 offset:34816
	ds_read_b128 v[226:229], v212 offset:35840
	ds_read_b128 v[230:233], v212 offset:36864
	ds_read_b128 v[234:237], v212 offset:37888
	ds_read_b128 v[238:241], v212 offset:38912
	ds_read_b128 v[242:245], v212 offset:39936
	global_load_lds_dwordx4 v[164:165], off
	v_lshl_add_u64 v[164:165], s[46:47], 0, v[180:181]
	s_mov_b32 m0, s52
	s_nop 0
	global_load_lds_dwordx4 v[164:165], off
	s_waitcnt vmcnt(8)
	s_waitcnt lgkmcnt(0)
	s_barrier
	s_setprio 1
	s_waitcnt lgkmcnt(0)
	v_mfma_scale_f32_16x16x128_f8f6f4 v[158:161], v[0:7], v[214:221], v[158:161], v163, v196 op_sel_hi:[0,0,0]
	v_mfma_scale_f32_16x16x128_f8f6f4 v[154:157], v[8:15], v[214:221], v[154:157], v163, v196 op_sel_hi:[0,0,0]
	v_mfma_scale_f32_16x16x128_f8f6f4 v[148:151], v[0:7], v[222:229], v[148:151], v163, v196 op_sel_hi:[0,0,0]
	v_mfma_scale_f32_16x16x128_f8f6f4 v[140:143], v[8:15], v[222:229], v[140:143], v163, v196 op_sel_hi:[0,0,0]
	v_mfma_scale_f32_16x16x128_f8f6f4 v[132:135], v[0:7], v[230:237], v[132:135], v163, v196 op_sel_hi:[0,0,0]
	v_mfma_scale_f32_16x16x128_f8f6f4 v[124:127], v[8:15], v[230:237], v[124:127], v163, v196 op_sel_hi:[0,0,0]
	v_mfma_scale_f32_16x16x128_f8f6f4 v[116:119], v[0:7], v[238:245], v[116:119], v163, v196 op_sel_hi:[0,0,0]
	v_mfma_scale_f32_16x16x128_f8f6f4 v[108:111], v[8:15], v[238:245], v[108:111], v163, v196 op_sel_hi:[0,0,0]
	v_mfma_scale_f32_16x16x128_f8f6f4 v[144:147], v[16:23], v[214:221], v[144:147], v163, v196 op_sel_hi:[0,0,0]
	v_mfma_scale_f32_16x16x128_f8f6f4 v[136:139], v[24:31], v[214:221], v[136:139], v163, v196 op_sel_hi:[0,0,0]
	v_mfma_scale_f32_16x16x128_f8f6f4 v[128:131], v[16:23], v[222:229], v[128:131], v163, v196 op_sel_hi:[0,0,0]
	v_mfma_scale_f32_16x16x128_f8f6f4 v[120:123], v[24:31], v[222:229], v[120:123], v163, v196 op_sel_hi:[0,0,0]
	v_mfma_scale_f32_16x16x128_f8f6f4 v[112:115], v[16:23], v[230:237], v[112:115], v163, v196 op_sel_hi:[0,0,0]
	v_mfma_scale_f32_16x16x128_f8f6f4 v[104:107], v[24:31], v[230:237], v[104:107], v163, v196 op_sel_hi:[0,0,0]
	v_mfma_scale_f32_16x16x128_f8f6f4 v[100:103], v[16:23], v[238:245], v[100:103], v163, v196 op_sel_hi:[0,0,0]
	v_mfma_scale_f32_16x16x128_f8f6f4 v[96:99], v[24:31], v[238:245], v[96:99], v163, v196 op_sel_hi:[0,0,0]
	s_setprio 0
	s_barrier
	s_add_i32 s2, s2, s5
	v_lshl_add_u64 v[164:165], v[186:187], 0, s[96:97]
	s_mov_b32 m0, s2
	ds_read_b128 v[214:217], v212 offset:49152
	ds_read_b128 v[218:221], v212 offset:50176
	ds_read_b128 v[222:225], v212 offset:51200
	ds_read_b128 v[226:229], v212 offset:52224
	ds_read_b128 v[230:233], v212 offset:53248
	ds_read_b128 v[234:237], v212 offset:54272
	ds_read_b128 v[238:241], v212 offset:55296
	ds_read_b128 v[242:245], v212 offset:56320
	global_load_lds_dwordx4 v[164:165], off
	s_add_i32 m0, s2, 0x2000
	s_add_u32 s44, s44, 0x20080
	v_lshl_add_u64 v[164:165], v[188:189], 0, s[96:97]
	s_addc_u32 s45, s45, 0
	s_add_i32 s2, s3, s5
	global_load_lds_dwordx4 v[164:165], off
	v_lshl_add_u64 v[164:165], s[44:45], 0, v[152:153]
	s_mov_b32 m0, s2
	s_nop 0
	global_load_lds_dwordx4 v[164:165], off
	v_lshl_add_u64 v[164:165], s[44:45], 0, v[172:173]
	s_add_i32 m0, s2, 0x2000
	s_nop 0
	global_load_lds_dwordx4 v[164:165], off
	v_lshl_add_u64 v[164:165], v[190:191], 0, s[96:97]
	s_mov_b32 m0, s53
	s_nop 0
	global_load_lds_dwordx4 v[164:165], off
	v_lshl_add_u64 v[164:165], v[192:193], 0, s[96:97]
	s_mov_b32 m0, s54
	s_nop 0
	global_load_lds_dwordx4 v[164:165], off
	s_waitcnt vmcnt(8)
	s_waitcnt lgkmcnt(0)
	s_barrier
	s_setprio 1
	s_waitcnt lgkmcnt(0)
	v_mfma_scale_f32_16x16x128_f8f6f4 v[92:95], v[0:7], v[214:221], v[92:95], v163, v196 op_sel_hi:[0,0,0]
	v_mfma_scale_f32_16x16x128_f8f6f4 v[88:91], v[8:15], v[214:221], v[88:91], v163, v196 op_sel_hi:[0,0,0]
	v_mfma_scale_f32_16x16x128_f8f6f4 v[76:79], v[0:7], v[222:229], v[76:79], v163, v196 op_sel_hi:[0,0,0]
	v_mfma_scale_f32_16x16x128_f8f6f4 v[68:71], v[8:15], v[222:229], v[68:71], v163, v196 op_sel_hi:[0,0,0]
	v_mfma_scale_f32_16x16x128_f8f6f4 v[52:55], v[0:7], v[230:237], v[52:55], v163, v196 op_sel_hi:[0,0,0]
	v_mfma_scale_f32_16x16x128_f8f6f4 v[44:47], v[8:15], v[230:237], v[44:47], v163, v196 op_sel_hi:[0,0,0]
	v_mfma_scale_f32_16x16x128_f8f6f4 v[36:39], v[0:7], v[238:245], v[36:39], v163, v196 op_sel_hi:[0,0,0]
	v_mfma_scale_f32_16x16x128_f8f6f4 v[32:35], v[8:15], v[238:245], v[32:35], v163, v196 op_sel_hi:[0,0,0]
	v_mfma_scale_f32_16x16x128_f8f6f4 v[72:75], v[16:23], v[214:221], v[72:75], v163, v196 op_sel_hi:[0,0,0]
	v_mfma_scale_f32_16x16x128_f8f6f4 v[64:67], v[24:31], v[214:221], v[64:67], v163, v196 op_sel_hi:[0,0,0]
	v_mfma_scale_f32_16x16x128_f8f6f4 v[48:51], v[16:23], v[222:229], v[48:51], v163, v196 op_sel_hi:[0,0,0]
	v_mfma_scale_f32_16x16x128_f8f6f4 v[40:43], v[24:31], v[222:229], v[40:43], v163, v196 op_sel_hi:[0,0,0]
	v_mfma_scale_f32_16x16x128_f8f6f4 v[84:87], v[16:23], v[230:237], v[84:87], v163, v196 op_sel_hi:[0,0,0]
	v_mfma_scale_f32_16x16x128_f8f6f4 v[80:83], v[24:31], v[230:237], v[80:83], v163, v196 op_sel_hi:[0,0,0]
	v_mfma_scale_f32_16x16x128_f8f6f4 v[60:63], v[16:23], v[238:245], v[60:63], v163, v196 op_sel_hi:[0,0,0]
	v_mfma_scale_f32_16x16x128_f8f6f4 v[56:59], v[24:31], v[238:245], v[56:59], v163, v196 op_sel_hi:[0,0,0]
	s_setprio 0
	s_barrier
	s_add_i32 s60, s60, 2
	s_add_u32 s42, s42, 0x100
	s_addc_u32 s43, s43, 0
	s_add_u32 s0, s0, 0x100
	s_addc_u32 s1, s1, 0
	s_cmp_gt_u32 s60, 5
	s_cbranch_scc0 .LBB0_204
	s_and_b64 vcc, exec, s[10:11]
	s_cbranch_vccz .LBB0_207
	s_barrier

; #define PG8_STAGE_B(bufoff, gbase) do { _Pragma("unroll") for (int _i = 0; _i < 2; ++_i) \
;         __builtin_amdgcn_global_load_lds((const unsigned*)((const char*)(gbase) + voffB[_i]), (LAS unsigned*)(lds + (bufoff) + ldsw + _i * 8192), 16, 0, 0); } while (0)
; #define PG8_STAGE_A(bufoff, gbase, UA) do { _Pragma("unroll") for (int _i = 0; _i < 2; ++_i) \
;         __builtin_amdgcn_global_load_lds((const unsigned*)((const char*)(gbase) + (UA)[_i]), (LAS unsigned*)(lds + (bufoff) + ldsw + _i * 8192), 16, 0, 0); } while (0)
; #define PG8_LDA(dst, b, h) do { _Pragma("unroll") for (int m = 0; m < 4; ++m) dst[m] = PG8_LD8(lds + PG8_SA(b, h) + aoff + m * 2048); } while (0)
; #define PG8_LDB(dst, b, h) do { _Pragma("unroll") for (int n = 0; n < 2; ++n) dst[n] = PG8_LD8(lds + PG8_SB(b, h) + boff + n * 2048); } while (0)
; #define PG8_WAIT_V(n) asm volatile("s_waitcnt vmcnt(" #n ")" ::: "memory")
; #define PG8_WAIT_L(n) asm volatile("s_waitcnt lgkmcnt(" #n ")" ::: "memory")
; #define PG8_BAR __builtin_amdgcn_s_barrier()
; #define PG8_SCHED __builtin_amdgcn_sched_barrier(0)
; template <class Epi, class Sched, bool GATHER, bool FP8 = false>
; __device__ __forceinline__ void gemm_phase(LAS unsigned char* lds, const Gemm g, const Sched& S, const Epi& E, const int wave_s) {
;     ...
;         for (int t = 0; t < nt; t += 2) {
;             const bool last = (t == nt - 2);
;             const char* a1 = cA + (size_t)(t + 1) * kstep;
;             const char* a2 = last ? nA : cA + (size_t)(t + 2) * kstep; const char* b2 = last ? nB : cB + (size_t)(t + 2) * kstep;
;             const char* a3 = a2 + kstep; const char* b3 = b2 + kstep;
;             unsigned u2[2][2];
; #pragma unroll
;             for (int h = 0; h < 2; ++h)
; #pragma unroll
;                 for (int i = 0; i < 2; ++i) u2[h][i] = (GATHER && last) ? uAn[h][i] : uAc[h][i];
;             PG8_LDB(B0, 0, 0); PG8_LDB(B1, 0, 1); PG8_SCHED; PG8_LDA(At, 0, 0); PG8_STAGE_A(PG8_SA(1, 1), a1, uAc[1]);
;             PG8_WAIT_V(8); PG8_WAIT_L(0); PG8_BAR; PG8_MMA(0, 0, At, B0); PG8_MMA(0, 1, At, B1); PG8_BAR; PG8_SCHED;
;             PG8_LDA(At, 0, 1); PG8_STAGE_B(PG8_SB(0, 0), b2); PG8_STAGE_B(PG8_SB(0, 1), b2 + hstepB); PG8_STAGE_A(PG8_SA(0, 0), a2, u2[0]);
;             PG8_WAIT_V(8); PG8_WAIT_L(0); PG8_BAR; PG8_MMA(1, 0, At, B0); PG8_MMA(1, 1, At, B1); PG8_BAR; PG8_SCHED;
.LBB0_437:
	s_add_u32 s0, s16, 0x80
	s_addc_u32 s1, s17, 0
	s_cmp_eq_u32 s59, 2
	s_cselect_b32 s1, s15, s1
	s_cselect_b32 s0, s14, s0
	s_cselect_b32 s19, s13, s45
	s_cselect_b32 s18, s12, s44
	s_add_i32 s2, 0, 0x10000
	v_add_u32_e32 v150, s2, v147
	s_add_i32 s3, 0, 0x14000
	ds_read_b128 v[142:145], v150
	ds_read_b128 v[154:157], v150 offset:1024
	ds_read_b128 v[158:161], v150 offset:2048
	ds_read_b128 v[164:167], v150 offset:3072
	v_add_u32_e32 v150, s3, v147
	ds_read_b128 v[168:171], v150
	ds_read_b128 v[172:175], v150 offset:1024
	ds_read_b128 v[176:179], v150 offset:2048
	ds_read_b128 v[180:183], v150 offset:3072
	v_lshl_add_u64 v[150:151], s[16:17], 0, v[138:139]
	s_add_i32 m0, s48, 0xc000
	ds_read_b128 v[184:187], v149
	ds_read_b128 v[188:191], v149 offset:1024
	ds_read_b128 v[192:195], v149 offset:2048
	ds_read_b128 v[212:215], v149 offset:3072
	ds_read_b128 v[216:219], v149 offset:4096
	ds_read_b128 v[220:223], v149 offset:5120
	ds_read_b128 v[224:227], v149 offset:6144
	ds_read_b128 v[228:231], v149 offset:7168
	global_load_lds_dwordx4 v[150:151], off
	v_lshl_add_u64 v[150:151], s[16:17], 0, v[140:141]
	s_add_i32 m0, s48, 0xe000
	s_nop 0
	global_load_lds_dwordx4 v[150:151], off
	s_waitcnt vmcnt(8)
	s_waitcnt lgkmcnt(0)
	s_barrier
	s_setprio 1
	s_waitcnt lgkmcnt(0)
	v_mfma_f32_16x16x32_bf16 v[124:127], v[142:145], v[184:187], v[124:127]
	v_mfma_f32_16x16x32_bf16 v[120:123], v[158:161], v[184:187], v[120:123]
	v_mfma_f32_16x16x32_bf16 v[116:119], v[142:145], v[192:195], v[116:119]
	v_mfma_f32_16x16x32_bf16 v[108:111], v[158:161], v[192:195], v[108:111]
	v_mfma_f32_16x16x32_bf16 v[100:103], v[142:145], v[216:219], v[100:103]
	v_mfma_f32_16x16x32_bf16 v[92:95], v[158:161], v[216:219], v[92:95]
	v_mfma_f32_16x16x32_bf16 v[84:87], v[142:145], v[224:227], v[84:87]
	v_mfma_f32_16x16x32_bf16 v[76:79], v[158:161], v[224:227], v[76:79]
	v_mfma_f32_16x16x32_bf16 v[124:127], v[154:157], v[188:191], v[124:127]
	v_mfma_f32_16x16x32_bf16 v[120:123], v[164:167], v[188:191], v[120:123]
	v_mfma_f32_16x16x32_bf16 v[116:119], v[154:157], v[212:215], v[116:119]
	v_mfma_f32_16x16x32_bf16 v[108:111], v[164:167], v[212:215], v[108:111]
	v_mfma_f32_16x16x32_bf16 v[100:103], v[154:157], v[220:223], v[100:103]
	v_mfma_f32_16x16x32_bf16 v[92:95], v[164:167], v[220:223], v[92:95]
	v_mfma_f32_16x16x32_bf16 v[84:87], v[154:157], v[228:231], v[84:87]
	v_mfma_f32_16x16x32_bf16 v[76:79], v[164:167], v[228:231], v[76:79]
	v_mfma_f32_16x16x32_bf16 v[112:115], v[168:171], v[184:187], v[112:115]
	v_mfma_f32_16x16x32_bf16 v[104:107], v[176:179], v[184:187], v[104:107]
	v_mfma_f32_16x16x32_bf16 v[96:99], v[168:171], v[192:195], v[96:99]
	v_mfma_f32_16x16x32_bf16 v[88:91], v[176:179], v[192:195], v[88:91]
	v_mfma_f32_16x16x32_bf16 v[80:83], v[168:171], v[216:219], v[80:83]
	v_mfma_f32_16x16x32_bf16 v[72:75], v[176:179], v[216:219], v[72:75]
	v_mfma_f32_16x16x32_bf16 v[68:71], v[168:171], v[224:227], v[68:71]
	v_mfma_f32_16x16x32_bf16 v[64:67], v[176:179], v[224:227], v[64:67]
	v_mfma_f32_16x16x32_bf16 v[112:115], v[172:175], v[188:191], v[112:115]
	v_mfma_f32_16x16x32_bf16 v[104:107], v[180:183], v[188:191], v[104:107]
	v_mfma_f32_16x16x32_bf16 v[96:99], v[172:175], v[212:215], v[96:99]
	v_mfma_f32_16x16x32_bf16 v[88:91], v[180:183], v[212:215], v[88:91]
	v_mfma_f32_16x16x32_bf16 v[80:83], v[172:175], v[220:223], v[80:83]
	v_mfma_f32_16x16x32_bf16 v[72:75], v[180:183], v[220:223], v[72:75]
	v_mfma_f32_16x16x32_bf16 v[68:71], v[172:175], v[228:231], v[68:71]
	v_mfma_f32_16x16x32_bf16 v[64:67], v[180:183], v[228:231], v[64:67]
	s_setprio 0
	s_barrier
	s_add_i32 s2, s2, s5
	v_lshl_add_u64 v[150:151], s[18:19], 0, v[152:153]
	s_mov_b32 m0, s2
	ds_read_b128 v[184:187], v149 offset:16384
	ds_read_b128 v[188:191], v149 offset:17408
	ds_read_b128 v[192:195], v149 offset:18432
	ds_read_b128 v[212:215], v149 offset:19456
	ds_read_b128 v[216:219], v149 offset:20480
	ds_read_b128 v[220:223], v149 offset:21504
	ds_read_b128 v[224:227], v149 offset:22528
	ds_read_b128 v[228:231], v149 offset:23552
	global_load_lds_dwordx4 v[150:151], off
	s_add_i32 m0, s2, 0x2000
	s_add_u32 s40, s18, 0x18000
	v_lshl_add_u64 v[232:233], s[18:19], 0, v[128:129]
	s_addc_u32 s41, s19, 0
	s_add_i32 s2, s3, s5
	global_load_lds_dwordx4 v[232:233], off
	v_lshl_add_u64 v[234:235], s[40:41], 0, v[152:153]
	s_mov_b32 m0, s2
	v_lshl_add_u64 v[236:237], s[0:1], 0, v[132:133]
	global_load_lds_dwordx4 v[234:235], off
	v_lshl_add_u64 v[234:235], s[40:41], 0, v[128:129]
	s_add_i32 m0, s2, 0x2000
	s_nop 0
	global_load_lds_dwordx4 v[234:235], off
	v_lshl_add_u64 v[234:235], s[0:1], 0, v[130:131]
	s_mov_b32 m0, s48
	s_nop 0
	global_load_lds_dwordx4 v[234:235], off
	s_mov_b32 m0, s49
	s_nop 0
	global_load_lds_dwordx4 v[236:237], off
	s_waitcnt vmcnt(8)
	s_waitcnt lgkmcnt(0)
	s_barrier
; #define PG8_STAGE_B(bufoff, gbase) do { _Pragma("unroll") for (int _i = 0; _i < 2; ++_i) \
;         __builtin_amdgcn_global_load_lds((const unsigned*)((const char*)(gbase) + voffB[_i]), (LAS unsigned*)(lds + (bufoff) + ldsw + _i * 8192), 16, 0, 0); } while (0)
; #define PG8_STAGE_A(bufoff, gbase, UA) do { _Pragma("unroll") for (int _i = 0; _i < 2; ++_i) \
;         __builtin_amdgcn_global_load_lds((const unsigned*)((const char*)(gbase) + (UA)[_i]), (LAS unsigned*)(lds + (bufoff) + ldsw + _i * 8192), 16, 0, 0); } while (0)
; #define PG8_LDA(dst, b, h) do { _Pragma("unroll") for (int m = 0; m < 4; ++m) dst[m] = PG8_LD8(lds + PG8_SA(b, h) + aoff + m * 2048); } while (0)
; #define PG8_LDB(dst, b, h) do { _Pragma("unroll") for (int n = 0; n < 2; ++n) dst[n] = PG8_LD8(lds + PG8_SB(b, h) + boff + n * 2048); } while (0)
; #define PG8_WAIT_V(n) asm volatile("s_waitcnt vmcnt(" #n ")" ::: "memory")
; #define PG8_WAIT_L(n) asm volatile("s_waitcnt lgkmcnt(" #n ")" ::: "memory")
; #define PG8_BAR __builtin_amdgcn_s_barrier()
; #define PG8_SCHED __builtin_amdgcn_sched_barrier(0)
; template <class Epi, class Sched, bool GATHER, bool FP8 = false>
; __device__ __forceinline__ void gemm_phase(LAS unsigned char* lds, const Gemm g, const Sched& S, const Epi& E, const int wave_s) {
;     ...
;             PG8_WAIT_V(8); PG8_WAIT_L(0); PG8_BAR; PG8_MMA(1, 0, At, B0); PG8_MMA(1, 1, At, B1); PG8_BAR; PG8_SCHED;
;             PG8_LDB(B0, 1, 0); PG8_LDB(B1, 1, 1); PG8_SCHED; PG8_LDA(At, 1, 0); PG8_STAGE_A(PG8_SA(0, 1), a2, u2[1]);
;             PG8_WAIT_V(8); PG8_WAIT_L(0); PG8_BAR; PG8_MMA(0, 0, At, B0); PG8_MMA(0, 1, At, B1); PG8_BAR; PG8_SCHED;
;             PG8_LDA(At, 1, 1); PG8_STAGE_B(PG8_SB(1, 0), b3); PG8_STAGE_B(PG8_SB(1, 1), b3 + hstepB); PG8_STAGE_A(PG8_SA(1, 0), a3, u2[0]);
;             PG8_WAIT_V(8); PG8_WAIT_L(0); PG8_BAR; PG8_MMA(1, 0, At, B0); PG8_MMA(1, 1, At, B1); PG8_BAR; PG8_SCHED;
	s_setprio 1
	s_waitcnt lgkmcnt(0)
	v_mfma_f32_16x16x32_bf16 v[60:63], v[142:145], v[184:187], v[60:63]
	v_mfma_f32_16x16x32_bf16 v[56:59], v[158:161], v[184:187], v[56:59]
	v_mfma_f32_16x16x32_bf16 v[44:47], v[142:145], v[192:195], v[44:47]
	v_mfma_f32_16x16x32_bf16 v[28:31], v[158:161], v[192:195], v[28:31]
	v_mfma_f32_16x16x32_bf16 v[20:23], v[142:145], v[216:219], v[20:23]
	v_mfma_f32_16x16x32_bf16 v[12:15], v[158:161], v[216:219], v[12:15]
	v_mfma_f32_16x16x32_bf16 v[4:7], v[142:145], v[224:227], v[4:7]
	v_mfma_f32_16x16x32_bf16 v[0:3], v[158:161], v[224:227], v[0:3]
	v_mfma_f32_16x16x32_bf16 v[60:63], v[154:157], v[188:191], v[60:63]
	v_mfma_f32_16x16x32_bf16 v[56:59], v[164:167], v[188:191], v[56:59]
	v_mfma_f32_16x16x32_bf16 v[44:47], v[154:157], v[212:215], v[44:47]
	v_mfma_f32_16x16x32_bf16 v[28:31], v[164:167], v[212:215], v[28:31]
	v_mfma_f32_16x16x32_bf16 v[20:23], v[154:157], v[220:223], v[20:23]
	v_mfma_f32_16x16x32_bf16 v[12:15], v[164:167], v[220:223], v[12:15]
	v_mfma_f32_16x16x32_bf16 v[4:7], v[154:157], v[228:231], v[4:7]
	v_mfma_f32_16x16x32_bf16 v[0:3], v[164:167], v[228:231], v[0:3]
	v_mfma_f32_16x16x32_bf16 v[40:43], v[168:171], v[184:187], v[40:43]
	v_mfma_f32_16x16x32_bf16 v[24:27], v[176:179], v[184:187], v[24:27]
	v_mfma_f32_16x16x32_bf16 v[16:19], v[168:171], v[192:195], v[16:19]
	v_mfma_f32_16x16x32_bf16 v[8:11], v[176:179], v[192:195], v[8:11]
	v_mfma_f32_16x16x32_bf16 v[52:55], v[168:171], v[216:219], v[52:55]
	v_mfma_f32_16x16x32_bf16 v[48:51], v[176:179], v[216:219], v[48:51]
	v_mfma_f32_16x16x32_bf16 v[36:39], v[168:171], v[224:227], v[36:39]
	v_mfma_f32_16x16x32_bf16 v[32:35], v[176:179], v[224:227], v[32:35]
	v_mfma_f32_16x16x32_bf16 v[40:43], v[172:175], v[188:191], v[40:43]
	v_mfma_f32_16x16x32_bf16 v[24:27], v[180:183], v[188:191], v[24:27]
	v_mfma_f32_16x16x32_bf16 v[16:19], v[172:175], v[212:215], v[16:19]
	v_mfma_f32_16x16x32_bf16 v[8:11], v[180:183], v[212:215], v[8:11]
	v_mfma_f32_16x16x32_bf16 v[52:55], v[172:175], v[220:223], v[52:55]
	v_mfma_f32_16x16x32_bf16 v[48:51], v[180:183], v[220:223], v[48:51]
	v_mfma_f32_16x16x32_bf16 v[36:39], v[172:175], v[228:231], v[36:39]
	v_mfma_f32_16x16x32_bf16 v[32:35], v[180:183], v[228:231], v[32:35]
	s_setprio 0
	s_barrier
	s_add_i32 s2, 0, 0x18000
	s_add_i32 s3, 0, 0x1c000
	v_add_u32_e32 v164, s2, v147
	v_add_u32_e32 v180, s3, v147
	ds_read_b128 v[142:145], v164
	ds_read_b128 v[154:157], v164 offset:1024
	ds_read_b128 v[158:161], v164 offset:2048
	ds_read_b128 v[164:167], v164 offset:3072
	ds_read_b128 v[168:171], v180
	ds_read_b128 v[172:175], v180 offset:1024
	ds_read_b128 v[176:179], v180 offset:2048
	ds_read_b128 v[180:183], v180 offset:3072
	s_mov_b32 m0, s50
	v_lshl_add_u64 v[238:239], s[0:1], 0, v[134:135]
	ds_read_b128 v[184:187], v149 offset:32768
	ds_read_b128 v[188:191], v149 offset:33792
	ds_read_b128 v[192:195], v149 offset:34816
	ds_read_b128 v[212:215], v149 offset:35840
	ds_read_b128 v[216:219], v149 offset:36864
	ds_read_b128 v[220:223], v149 offset:37888
	ds_read_b128 v[224:227], v149 offset:38912
	ds_read_b128 v[228:231], v149 offset:39936
	global_load_lds_dwordx4 v[238:239], off
	v_lshl_add_u64 v[238:239], s[0:1], 0, v[136:137]
	s_mov_b32 m0, s51
	s_nop 0
	global_load_lds_dwordx4 v[238:239], off
	s_waitcnt vmcnt(8)
	s_waitcnt lgkmcnt(0)
	s_barrier
	s_setprio 1
	s_waitcnt lgkmcnt(0)
	v_mfma_f32_16x16x32_bf16 v[124:127], v[142:145], v[184:187], v[124:127]
	v_mfma_f32_16x16x32_bf16 v[120:123], v[158:161], v[184:187], v[120:123]
	v_mfma_f32_16x16x32_bf16 v[116:119], v[142:145], v[192:195], v[116:119]
	v_mfma_f32_16x16x32_bf16 v[108:111], v[158:161], v[192:195], v[108:111]
	v_mfma_f32_16x16x32_bf16 v[100:103], v[142:145], v[216:219], v[100:103]
	v_mfma_f32_16x16x32_bf16 v[92:95], v[158:161], v[216:219], v[92:95]
	v_mfma_f32_16x16x32_bf16 v[84:87], v[142:145], v[224:227], v[84:87]
	v_mfma_f32_16x16x32_bf16 v[76:79], v[158:161], v[224:227], v[76:79]
	v_mfma_f32_16x16x32_bf16 v[124:127], v[154:157], v[188:191], v[124:127]
	v_mfma_f32_16x16x32_bf16 v[120:123], v[164:167], v[188:191], v[120:123]
	v_mfma_f32_16x16x32_bf16 v[116:119], v[154:157], v[212:215], v[116:119]
	v_mfma_f32_16x16x32_bf16 v[108:111], v[164:167], v[212:215], v[108:111]
	v_mfma_f32_16x16x32_bf16 v[100:103], v[154:157], v[220:223], v[100:103]
	v_mfma_f32_16x16x32_bf16 v[92:95], v[164:167], v[220:223], v[92:95]
	v_mfma_f32_16x16x32_bf16 v[84:87], v[154:157], v[228:231], v[84:87]
	v_mfma_f32_16x16x32_bf16 v[76:79], v[164:167], v[228:231], v[76:79]
	v_mfma_f32_16x16x32_bf16 v[112:115], v[168:171], v[184:187], v[112:115]
	v_mfma_f32_16x16x32_bf16 v[104:107], v[176:179], v[184:187], v[104:107]
	v_mfma_f32_16x16x32_bf16 v[96:99], v[168:171], v[192:195], v[96:99]
	v_mfma_f32_16x16x32_bf16 v[88:91], v[176:179], v[192:195], v[88:91]
	v_mfma_f32_16x16x32_bf16 v[80:83], v[168:171], v[216:219], v[80:83]
	v_mfma_f32_16x16x32_bf16 v[72:75], v[176:179], v[216:219], v[72:75]
	v_mfma_f32_16x16x32_bf16 v[68:71], v[168:171], v[224:227], v[68:71]
	v_mfma_f32_16x16x32_bf16 v[64:67], v[176:179], v[224:227], v[64:67]
	v_mfma_f32_16x16x32_bf16 v[112:115], v[172:175], v[188:191], v[112:115]
	v_mfma_f32_16x16x32_bf16 v[104:107], v[180:183], v[188:191], v[104:107]
	v_mfma_f32_16x16x32_bf16 v[96:99], v[172:175], v[212:215], v[96:99]
	v_mfma_f32_16x16x32_bf16 v[88:91], v[180:183], v[212:215], v[88:91]
	v_mfma_f32_16x16x32_bf16 v[80:83], v[172:175], v[220:223], v[80:83]
	v_mfma_f32_16x16x32_bf16 v[72:75], v[180:183], v[220:223], v[72:75]
	v_mfma_f32_16x16x32_bf16 v[68:71], v[172:175], v[228:231], v[68:71]
	v_mfma_f32_16x16x32_bf16 v[64:67], v[180:183], v[228:231], v[64:67]
	s_setprio 0
	s_barrier
; #define PG8_STAGE_B(bufoff, gbase) do { _Pragma("unroll") for (int _i = 0; _i < 2; ++_i) \
;         __builtin_amdgcn_global_load_lds((const unsigned*)((const char*)(gbase) + voffB[_i]), (LAS unsigned*)(lds + (bufoff) + ldsw + _i * 8192), 16, 0, 0); } while (0)
; #define PG8_STAGE_A(bufoff, gbase, UA) do { _Pragma("unroll") for (int _i = 0; _i < 2; ++_i) \
;         __builtin_amdgcn_global_load_lds((const unsigned*)((const char*)(gbase) + (UA)[_i]), (LAS unsigned*)(lds + (bufoff) + ldsw + _i * 8192), 16, 0, 0); } while (0)
; #define PG8_LDA(dst, b, h) do { _Pragma("unroll") for (int m = 0; m < 4; ++m) dst[m] = PG8_LD8(lds + PG8_SA(b, h) + aoff + m * 2048); } while (0)
; #define PG8_WAIT_V(n) asm volatile("s_waitcnt vmcnt(" #n ")" ::: "memory")
; #define PG8_WAIT_L(n) asm volatile("s_waitcnt lgkmcnt(" #n ")" ::: "memory")
; #define PG8_BAR __builtin_amdgcn_s_barrier()
; #define PG8_SCHED __builtin_amdgcn_sched_barrier(0)
; template <class Epi, class Sched, bool GATHER, bool FP8 = false>
; __device__ __forceinline__ void gemm_phase(LAS unsigned char* lds, const Gemm g, const Sched& S, const Epi& E, const int wave_s) {
;     ...
;             PG8_LDA(At, 1, 1); PG8_STAGE_B(PG8_SB(1, 0), b3); PG8_STAGE_B(PG8_SB(1, 1), b3 + hstepB); PG8_STAGE_A(PG8_SA(1, 0), a3, u2[0]);
;             PG8_WAIT_V(8); PG8_WAIT_L(0); PG8_BAR; PG8_MMA(1, 0, At, B0); PG8_MMA(1, 1, At, B1); PG8_BAR; PG8_SCHED;
;         }
;         if (wr == 0) PG8_BAR;
	s_add_i32 s0, s2, s5
	v_lshl_add_u64 v[150:151], v[150:151], 0, s[96:97]
	s_mov_b32 m0, s0
	ds_read_b128 v[184:187], v149 offset:49152
	ds_read_b128 v[188:191], v149 offset:50176
	ds_read_b128 v[192:195], v149 offset:51200
	ds_read_b128 v[212:215], v149 offset:52224
	ds_read_b128 v[216:219], v149 offset:53248
	ds_read_b128 v[220:223], v149 offset:54272
	ds_read_b128 v[224:227], v149 offset:55296
	ds_read_b128 v[228:231], v149 offset:56320
	global_load_lds_dwordx4 v[150:151], off
	s_add_i32 m0, s0, 0x2000
	s_add_u32 s0, s18, 0x18080
	v_lshl_add_u64 v[150:151], v[232:233], 0, s[96:97]
	s_addc_u32 s1, s19, 0
	s_add_i32 s2, s3, s5
	global_load_lds_dwordx4 v[150:151], off
	v_lshl_add_u64 v[150:151], s[0:1], 0, v[152:153]
	s_mov_b32 m0, s2
	s_nop 0
	global_load_lds_dwordx4 v[150:151], off
	v_lshl_add_u64 v[150:151], s[0:1], 0, v[128:129]
	s_add_i32 m0, s2, 0x2000
	s_nop 0
	global_load_lds_dwordx4 v[150:151], off
	v_lshl_add_u64 v[150:151], v[234:235], 0, s[96:97]
	s_mov_b32 m0, s52
	s_nop 0
	global_load_lds_dwordx4 v[150:151], off
	v_lshl_add_u64 v[150:151], v[236:237], 0, s[96:97]
	s_mov_b32 m0, s53
	s_nop 0
	global_load_lds_dwordx4 v[150:151], off
	s_waitcnt vmcnt(8)
	s_waitcnt lgkmcnt(0)
	s_barrier
	s_setprio 1
	s_waitcnt lgkmcnt(0)
	v_mfma_f32_16x16x32_bf16 v[60:63], v[142:145], v[184:187], v[60:63]
	v_mfma_f32_16x16x32_bf16 v[56:59], v[158:161], v[184:187], v[56:59]
	v_mfma_f32_16x16x32_bf16 v[44:47], v[142:145], v[192:195], v[44:47]
	v_mfma_f32_16x16x32_bf16 v[28:31], v[158:161], v[192:195], v[28:31]
	v_mfma_f32_16x16x32_bf16 v[20:23], v[142:145], v[216:219], v[20:23]
	v_mfma_f32_16x16x32_bf16 v[12:15], v[158:161], v[216:219], v[12:15]
	v_mfma_f32_16x16x32_bf16 v[4:7], v[142:145], v[224:227], v[4:7]
	v_mfma_f32_16x16x32_bf16 v[0:3], v[158:161], v[224:227], v[0:3]
	v_mfma_f32_16x16x32_bf16 v[60:63], v[154:157], v[188:191], v[60:63]
	v_mfma_f32_16x16x32_bf16 v[56:59], v[164:167], v[188:191], v[56:59]
	v_mfma_f32_16x16x32_bf16 v[44:47], v[154:157], v[212:215], v[44:47]
	v_mfma_f32_16x16x32_bf16 v[28:31], v[164:167], v[212:215], v[28:31]
	v_mfma_f32_16x16x32_bf16 v[20:23], v[154:157], v[220:223], v[20:23]
	v_mfma_f32_16x16x32_bf16 v[12:15], v[164:167], v[220:223], v[12:15]
	v_mfma_f32_16x16x32_bf16 v[4:7], v[154:157], v[228:231], v[4:7]
	v_mfma_f32_16x16x32_bf16 v[0:3], v[164:167], v[228:231], v[0:3]
	v_mfma_f32_16x16x32_bf16 v[40:43], v[168:171], v[184:187], v[40:43]
	v_mfma_f32_16x16x32_bf16 v[24:27], v[176:179], v[184:187], v[24:27]
	v_mfma_f32_16x16x32_bf16 v[16:19], v[168:171], v[192:195], v[16:19]
	v_mfma_f32_16x16x32_bf16 v[8:11], v[176:179], v[192:195], v[8:11]
	v_mfma_f32_16x16x32_bf16 v[52:55], v[168:171], v[216:219], v[52:55]
	v_mfma_f32_16x16x32_bf16 v[48:51], v[176:179], v[216:219], v[48:51]
	v_mfma_f32_16x16x32_bf16 v[36:39], v[168:171], v[224:227], v[36:39]
	v_mfma_f32_16x16x32_bf16 v[32:35], v[176:179], v[224:227], v[32:35]
	v_mfma_f32_16x16x32_bf16 v[40:43], v[172:175], v[188:191], v[40:43]
	v_mfma_f32_16x16x32_bf16 v[24:27], v[180:183], v[188:191], v[24:27]
	v_mfma_f32_16x16x32_bf16 v[16:19], v[172:175], v[212:215], v[16:19]
	v_mfma_f32_16x16x32_bf16 v[8:11], v[180:183], v[212:215], v[8:11]
	v_mfma_f32_16x16x32_bf16 v[52:55], v[172:175], v[220:223], v[52:55]
	v_mfma_f32_16x16x32_bf16 v[48:51], v[180:183], v[220:223], v[48:51]
	v_mfma_f32_16x16x32_bf16 v[36:39], v[172:175], v[228:231], v[36:39]
	v_mfma_f32_16x16x32_bf16 v[32:35], v[180:183], v[228:231], v[32:35]
	s_setprio 0
	s_barrier
	s_add_i32 s59, s59, 2
	s_add_u32 s16, s16, 0x100
	s_addc_u32 s17, s17, 0
	s_add_u32 s44, s44, 0x100
	s_addc_u32 s45, s45, 0
	s_cmp_gt_u32 s59, 3
	s_cbranch_scc0 .LBB0_437
	s_and_b64 vcc, exec, s[10:11]
	s_cbranch_vccz .LBB0_440
	s_barrier

; #define PG8_STAGE_B(bufoff, gbase) do { _Pragma("unroll") for (int _i = 0; _i < 2; ++_i) \
;         __builtin_amdgcn_global_load_lds((const unsigned*)((const char*)(gbase) + voffB[_i]), (LAS unsigned*)(lds + (bufoff) + ldsw + _i * 8192), 16, 0, 0); } while (0)
; #define PG8_STAGE_A(bufoff, gbase, UA) do { _Pragma("unroll") for (int _i = 0; _i < 2; ++_i) \
;         __builtin_amdgcn_global_load_lds((const unsigned*)((const char*)(gbase) + (UA)[_i]), (LAS unsigned*)(lds + (bufoff) + ldsw + _i * 8192), 16, 0, 0); } while (0)
; #define PG8_LDA(dst, b, h) do { _Pragma("unroll") for (int m = 0; m < 4; ++m) dst[m] = PG8_LD8(lds + PG8_SA(b, h) + aoff + m * 2048); } while (0)
; #define PG8_LDB(dst, b, h) do { _Pragma("unroll") for (int n = 0; n < 2; ++n) dst[n] = PG8_LD8(lds + PG8_SB(b, h) + boff + n * 2048); } while (0)
; #define PG8_WAIT_V(n) asm volatile("s_waitcnt vmcnt(" #n ")" ::: "memory")
; #define PG8_WAIT_L(n) asm volatile("s_waitcnt lgkmcnt(" #n ")" ::: "memory")
; #define PG8_BAR __builtin_amdgcn_s_barrier()
; #define PG8_SCHED __builtin_amdgcn_sched_barrier(0)
; template <class Epi, class Sched, bool GATHER, bool FP8 = false>
; __device__ __forceinline__ void gemm_phase(LAS unsigned char* lds, const Gemm g, const Sched& S, const Epi& E, const int wave_s) {
;     ...
;         for (int t = 0; t < nt; t += 2) {
;             const bool last = (t == nt - 2);
;             const char* a1 = cA + (size_t)(t + 1) * kstep;
;             const char* a2 = last ? nA : cA + (size_t)(t + 2) * kstep; const char* b2 = last ? nB : cB + (size_t)(t + 2) * kstep;
;             const char* a3 = a2 + kstep; const char* b3 = b2 + kstep;
;             unsigned u2[2][2];
; #pragma unroll
;             for (int h = 0; h < 2; ++h)
; #pragma unroll
;                 for (int i = 0; i < 2; ++i) u2[h][i] = (GATHER && last) ? uAn[h][i] : uAc[h][i];
;             PG8_LDB(B0, 0, 0); PG8_LDB(B1, 0, 1); PG8_SCHED; PG8_LDA(At, 0, 0); PG8_STAGE_A(PG8_SA(1, 1), a1, uAc[1]);
;             PG8_WAIT_V(8); PG8_WAIT_L(0); PG8_BAR; PG8_MMA(0, 0, At, B0); PG8_MMA(0, 1, At, B1); PG8_BAR; PG8_SCHED;
;             PG8_LDA(At, 0, 1); PG8_STAGE_B(PG8_SB(0, 0), b2); PG8_STAGE_B(PG8_SB(0, 1), b2 + hstepB); PG8_STAGE_A(PG8_SA(0, 0), a2, u2[0]);
;             PG8_WAIT_V(8); PG8_WAIT_L(0); PG8_BAR; PG8_MMA(1, 0, At, B0); PG8_MMA(1, 1, At, B1); PG8_BAR; PG8_SCHED;
.LBB0_453:
	s_add_u32 s58, s46, s52
	s_addc_u32 s59, s47, s53
	s_add_u32 s2, s58, 0x100
	s_addc_u32 s3, s59, 0
	s_and_b64 s[40:41], s[50:51], exec
	s_cselect_b32 s54, s15, s2
	s_cselect_b32 s55, s13, s3
	s_add_u32 s2, s44, s52
	s_addc_u32 s3, s45, s53
	s_add_u32 s2, s2, 0x100
	s_addc_u32 s3, s3, 0
	s_and_b64 s[40:41], s[50:51], exec
	s_cselect_b32 s53, s0, s3
	s_cselect_b32 s52, s1, s2
	s_add_i32 s2, 0, 0x10000
	s_add_i32 s3, 0, 0x14000
	v_add_u32_e32 v140, s2, v143
	s_add_i32 s91, s2, s5
	ds_read_b128 v[146:149], v140
	ds_read_b128 v[154:157], v140 offset:1024
	ds_read_b128 v[158:161], v140 offset:2048
	ds_read_b128 v[164:167], v140 offset:3072
	v_add_u32_e32 v140, s3, v143
	s_add_i32 m0, s62, 0xc000
	s_add_i32 s4, s62, 0xe000
	s_add_i32 s76, s91, 0x2000
	ds_read_b128 v[168:171], v140
	ds_read_b128 v[172:175], v140 offset:1024
	ds_read_b128 v[176:179], v140 offset:2048
	ds_read_b128 v[180:183], v140 offset:3072
	s_add_u32 s56, s52, 0x10000
	s_addc_u32 s57, s53, 0
	s_add_i32 s74, 0, 0x18000
	s_add_i32 s90, s3, s5
	s_add_i32 s72, s74, s5
	s_add_i32 s77, s90, 0x2000
	s_add_i32 s73, 0, 0x1c000
	s_add_i32 s71, s72, 0x2000
	s_add_u32 s50, s52, 0x10080
	s_addc_u32 s51, s53, 0
	s_add_i32 vcc_hi, s73, s5
	s_add_i32 vcc_lo, vcc_hi, 0x2000
	v_lshl_add_u64 v[140:141], s[58:59], 0, v[134:135]
	v_lshl_add_u64 v[140:141], v[140:141], 0, s[96:97]
	ds_read_b128 v[184:187], v144
	ds_read_b128 v[188:191], v144 offset:1024
	ds_read_b128 v[192:195], v144 offset:2048
	ds_read_b128 v[212:215], v144 offset:3072
	ds_read_b128 v[216:219], v144 offset:4096
	ds_read_b128 v[220:223], v144 offset:5120
	ds_read_b128 v[224:227], v144 offset:6144
	ds_read_b128 v[228:231], v144 offset:7168
	global_load_lds_dwordx4 v[140:141], off
	v_lshl_add_u64 v[140:141], s[58:59], 0, v[136:137]
	v_lshl_add_u64 v[140:141], v[140:141], 0, s[96:97]
	s_mov_b32 m0, s4
	s_nop 0
	global_load_lds_dwordx4 v[140:141], off
	s_waitcnt vmcnt(8)
	s_waitcnt lgkmcnt(0)
	s_barrier
	s_setprio 1
	s_waitcnt lgkmcnt(0)
	v_mfma_f32_16x16x32_bf16 v[124:127], v[146:149], v[184:187], v[124:127]
	v_mfma_f32_16x16x32_bf16 v[120:123], v[158:161], v[184:187], v[120:123]
	v_mfma_f32_16x16x32_bf16 v[112:115], v[146:149], v[192:195], v[112:115]
	v_mfma_f32_16x16x32_bf16 v[104:107], v[158:161], v[192:195], v[104:107]
	v_mfma_f32_16x16x32_bf16 v[96:99], v[146:149], v[216:219], v[96:99]
	v_mfma_f32_16x16x32_bf16 v[88:91], v[158:161], v[216:219], v[88:91]
	v_mfma_f32_16x16x32_bf16 v[80:83], v[146:149], v[224:227], v[80:83]
	v_mfma_f32_16x16x32_bf16 v[72:75], v[158:161], v[224:227], v[72:75]
	v_mfma_f32_16x16x32_bf16 v[124:127], v[154:157], v[188:191], v[124:127]
	v_mfma_f32_16x16x32_bf16 v[120:123], v[164:167], v[188:191], v[120:123]
	v_mfma_f32_16x16x32_bf16 v[112:115], v[154:157], v[212:215], v[112:115]
	v_mfma_f32_16x16x32_bf16 v[104:107], v[164:167], v[212:215], v[104:107]
	v_mfma_f32_16x16x32_bf16 v[96:99], v[154:157], v[220:223], v[96:99]
	v_mfma_f32_16x16x32_bf16 v[88:91], v[164:167], v[220:223], v[88:91]
	v_mfma_f32_16x16x32_bf16 v[80:83], v[154:157], v[228:231], v[80:83]
	v_mfma_f32_16x16x32_bf16 v[72:75], v[164:167], v[228:231], v[72:75]
	v_mfma_f32_16x16x32_bf16 v[116:119], v[168:171], v[184:187], v[116:119]
	v_mfma_f32_16x16x32_bf16 v[108:111], v[176:179], v[184:187], v[108:111]
	v_mfma_f32_16x16x32_bf16 v[100:103], v[168:171], v[192:195], v[100:103]
	v_mfma_f32_16x16x32_bf16 v[92:95], v[176:179], v[192:195], v[92:95]
	v_mfma_f32_16x16x32_bf16 v[84:87], v[168:171], v[216:219], v[84:87]
	v_mfma_f32_16x16x32_bf16 v[76:79], v[176:179], v[216:219], v[76:79]
	v_mfma_f32_16x16x32_bf16 v[68:71], v[168:171], v[224:227], v[68:71]
	v_mfma_f32_16x16x32_bf16 v[64:67], v[176:179], v[224:227], v[64:67]
	v_mfma_f32_16x16x32_bf16 v[116:119], v[172:175], v[188:191], v[116:119]
	v_mfma_f32_16x16x32_bf16 v[108:111], v[180:183], v[188:191], v[108:111]
	v_mfma_f32_16x16x32_bf16 v[100:103], v[172:175], v[212:215], v[100:103]
	v_mfma_f32_16x16x32_bf16 v[92:95], v[180:183], v[212:215], v[92:95]
	v_mfma_f32_16x16x32_bf16 v[84:87], v[172:175], v[220:223], v[84:87]
	v_mfma_f32_16x16x32_bf16 v[76:79], v[180:183], v[220:223], v[76:79]
	v_mfma_f32_16x16x32_bf16 v[68:71], v[172:175], v[228:231], v[68:71]
	v_mfma_f32_16x16x32_bf16 v[64:67], v[180:183], v[228:231], v[64:67]
	s_setprio 0
	s_barrier
	s_mov_b32 m0, s91
	v_lshl_add_u64 v[140:141], s[52:53], 0, v[152:153]
	ds_read_b128 v[184:187], v144 offset:16384
	ds_read_b128 v[188:191], v144 offset:17408
	ds_read_b128 v[192:195], v144 offset:18432
	ds_read_b128 v[212:215], v144 offset:19456
	ds_read_b128 v[216:219], v144 offset:20480
	ds_read_b128 v[220:223], v144 offset:21504
	ds_read_b128 v[224:227], v144 offset:22528
	ds_read_b128 v[228:231], v144 offset:23552
	global_load_lds_dwordx4 v[140:141], off
	v_lshl_add_u64 v[150:151], s[52:53], 0, v[128:129]
	s_mov_b32 m0, s76
	v_lshl_add_u64 v[232:233], s[56:57], 0, v[152:153]
	global_load_lds_dwordx4 v[150:151], off
	s_mov_b32 m0, s90
	v_lshl_add_u64 v[234:235], s[54:55], 0, v[132:133]
	global_load_lds_dwordx4 v[232:233], off
	v_lshl_add_u64 v[232:233], s[56:57], 0, v[128:129]
	s_mov_b32 m0, s77
	s_nop 0
	global_load_lds_dwordx4 v[232:233], off
	v_lshl_add_u64 v[232:233], s[54:55], 0, v[130:131]
	s_mov_b32 m0, s62
	s_nop 0
	global_load_lds_dwordx4 v[232:233], off
	s_mov_b32 m0, s63
	s_nop 0
	global_load_lds_dwordx4 v[234:235], off
	s_waitcnt vmcnt(8)
	s_waitcnt lgkmcnt(0)
	s_barrier
; #define PG8_STAGE_B(bufoff, gbase) do { _Pragma("unroll") for (int _i = 0; _i < 2; ++_i) \
;         __builtin_amdgcn_global_load_lds((const unsigned*)((const char*)(gbase) + voffB[_i]), (LAS unsigned*)(lds + (bufoff) + ldsw + _i * 8192), 16, 0, 0); } while (0)
; #define PG8_STAGE_A(bufoff, gbase, UA) do { _Pragma("unroll") for (int _i = 0; _i < 2; ++_i) \
;         __builtin_amdgcn_global_load_lds((const unsigned*)((const char*)(gbase) + (UA)[_i]), (LAS unsigned*)(lds + (bufoff) + ldsw + _i * 8192), 16, 0, 0); } while (0)
; #define PG8_LDA(dst, b, h) do { _Pragma("unroll") for (int m = 0; m < 4; ++m) dst[m] = PG8_LD8(lds + PG8_SA(b, h) + aoff + m * 2048); } while (0)
; #define PG8_LDB(dst, b, h) do { _Pragma("unroll") for (int n = 0; n < 2; ++n) dst[n] = PG8_LD8(lds + PG8_SB(b, h) + boff + n * 2048); } while (0)
; #define PG8_WAIT_V(n) asm volatile("s_waitcnt vmcnt(" #n ")" ::: "memory")
; #define PG8_WAIT_L(n) asm volatile("s_waitcnt lgkmcnt(" #n ")" ::: "memory")
; #define PG8_BAR __builtin_amdgcn_s_barrier()
; #define PG8_SCHED __builtin_amdgcn_sched_barrier(0)
; template <class Epi, class Sched, bool GATHER, bool FP8 = false>
; __device__ __forceinline__ void gemm_phase(LAS unsigned char* lds, const Gemm g, const Sched& S, const Epi& E, const int wave_s) {
;     ...
;             PG8_WAIT_V(8); PG8_WAIT_L(0); PG8_BAR; PG8_MMA(1, 0, At, B0); PG8_MMA(1, 1, At, B1); PG8_BAR; PG8_SCHED;
;             PG8_LDB(B0, 1, 0); PG8_LDB(B1, 1, 1); PG8_SCHED; PG8_LDA(At, 1, 0); PG8_STAGE_A(PG8_SA(0, 1), a2, u2[1]);
;             PG8_WAIT_V(8); PG8_WAIT_L(0); PG8_BAR; PG8_MMA(0, 0, At, B0); PG8_MMA(0, 1, At, B1); PG8_BAR; PG8_SCHED;
;             PG8_LDA(At, 1, 1); PG8_STAGE_B(PG8_SB(1, 0), b3); PG8_STAGE_B(PG8_SB(1, 1), b3 + hstepB); PG8_STAGE_A(PG8_SA(1, 0), a3, u2[0]);
;             PG8_WAIT_V(8); PG8_WAIT_L(0); PG8_BAR; PG8_MMA(1, 0, At, B0); PG8_MMA(1, 1, At, B1); PG8_BAR; PG8_SCHED;
	s_setprio 1
	s_waitcnt lgkmcnt(0)
	v_mfma_f32_16x16x32_bf16 v[60:63], v[146:149], v[184:187], v[60:63]
	v_mfma_f32_16x16x32_bf16 v[56:59], v[158:161], v[184:187], v[56:59]
	v_mfma_f32_16x16x32_bf16 v[40:43], v[146:149], v[192:195], v[40:43]
	v_mfma_f32_16x16x32_bf16 v[32:35], v[158:161], v[192:195], v[32:35]
	v_mfma_f32_16x16x32_bf16 v[16:19], v[146:149], v[216:219], v[16:19]
	v_mfma_f32_16x16x32_bf16 v[12:15], v[158:161], v[216:219], v[12:15]
	v_mfma_f32_16x16x32_bf16 v[4:7], v[146:149], v[224:227], v[4:7]
	v_mfma_f32_16x16x32_bf16 v[0:3], v[158:161], v[224:227], v[0:3]
	v_mfma_f32_16x16x32_bf16 v[60:63], v[154:157], v[188:191], v[60:63]
	v_mfma_f32_16x16x32_bf16 v[56:59], v[164:167], v[188:191], v[56:59]
	v_mfma_f32_16x16x32_bf16 v[40:43], v[154:157], v[212:215], v[40:43]
	v_mfma_f32_16x16x32_bf16 v[32:35], v[164:167], v[212:215], v[32:35]
	v_mfma_f32_16x16x32_bf16 v[16:19], v[154:157], v[220:223], v[16:19]
	v_mfma_f32_16x16x32_bf16 v[12:15], v[164:167], v[220:223], v[12:15]
	v_mfma_f32_16x16x32_bf16 v[4:7], v[154:157], v[228:231], v[4:7]
	v_mfma_f32_16x16x32_bf16 v[0:3], v[164:167], v[228:231], v[0:3]
	v_mfma_f32_16x16x32_bf16 v[44:47], v[168:171], v[184:187], v[44:47]
	v_mfma_f32_16x16x32_bf16 v[36:39], v[176:179], v[184:187], v[36:39]
	v_mfma_f32_16x16x32_bf16 v[20:23], v[168:171], v[192:195], v[20:23]
	v_mfma_f32_16x16x32_bf16 v[8:11], v[176:179], v[192:195], v[8:11]
	v_mfma_f32_16x16x32_bf16 v[48:51], v[168:171], v[216:219], v[48:51]
	v_mfma_f32_16x16x32_bf16 v[52:55], v[176:179], v[216:219], v[52:55]
	v_mfma_f32_16x16x32_bf16 v[24:27], v[168:171], v[224:227], v[24:27]
	v_mfma_f32_16x16x32_bf16 v[28:31], v[176:179], v[224:227], v[28:31]
	v_mfma_f32_16x16x32_bf16 v[44:47], v[172:175], v[188:191], v[44:47]
	v_mfma_f32_16x16x32_bf16 v[36:39], v[180:183], v[188:191], v[36:39]
	v_mfma_f32_16x16x32_bf16 v[20:23], v[172:175], v[212:215], v[20:23]
	v_mfma_f32_16x16x32_bf16 v[8:11], v[180:183], v[212:215], v[8:11]
	v_mfma_f32_16x16x32_bf16 v[48:51], v[172:175], v[220:223], v[48:51]
	v_mfma_f32_16x16x32_bf16 v[52:55], v[180:183], v[220:223], v[52:55]
	v_mfma_f32_16x16x32_bf16 v[24:27], v[172:175], v[228:231], v[24:27]
	v_mfma_f32_16x16x32_bf16 v[28:31], v[180:183], v[228:231], v[28:31]
	s_setprio 0
	s_barrier
	v_add_u32_e32 v145, s74, v143
	ds_read_b128 v[146:149], v145
	ds_read_b128 v[154:157], v145 offset:1024
	ds_read_b128 v[158:161], v145 offset:2048
	ds_read_b128 v[164:167], v145 offset:3072
	v_add_u32_e32 v145, s73, v143
	ds_read_b128 v[168:171], v145
	ds_read_b128 v[172:175], v145 offset:1024
	ds_read_b128 v[176:179], v145 offset:2048
	ds_read_b128 v[180:183], v145 offset:3072
	s_mov_b32 m0, s64
	v_lshl_add_u64 v[236:237], s[54:55], 0, v[134:135]
	ds_read_b128 v[184:187], v144 offset:32768
	ds_read_b128 v[188:191], v144 offset:33792
	ds_read_b128 v[192:195], v144 offset:34816
	ds_read_b128 v[212:215], v144 offset:35840
	ds_read_b128 v[216:219], v144 offset:36864
	ds_read_b128 v[220:223], v144 offset:37888
	ds_read_b128 v[224:227], v144 offset:38912
	ds_read_b128 v[228:231], v144 offset:39936
	global_load_lds_dwordx4 v[236:237], off
	v_lshl_add_u64 v[236:237], s[54:55], 0, v[136:137]
	s_mov_b32 m0, s65
	s_nop 0
	global_load_lds_dwordx4 v[236:237], off
	s_waitcnt vmcnt(8)
	s_waitcnt lgkmcnt(0)
	s_barrier
	s_setprio 1
	s_waitcnt lgkmcnt(0)
	v_mfma_f32_16x16x32_bf16 v[124:127], v[146:149], v[184:187], v[124:127]
	v_mfma_f32_16x16x32_bf16 v[120:123], v[158:161], v[184:187], v[120:123]
	v_mfma_f32_16x16x32_bf16 v[112:115], v[146:149], v[192:195], v[112:115]
	v_mfma_f32_16x16x32_bf16 v[104:107], v[158:161], v[192:195], v[104:107]
	v_mfma_f32_16x16x32_bf16 v[96:99], v[146:149], v[216:219], v[96:99]
	v_mfma_f32_16x16x32_bf16 v[88:91], v[158:161], v[216:219], v[88:91]
	v_mfma_f32_16x16x32_bf16 v[80:83], v[146:149], v[224:227], v[80:83]
	v_mfma_f32_16x16x32_bf16 v[72:75], v[158:161], v[224:227], v[72:75]
	v_mfma_f32_16x16x32_bf16 v[124:127], v[154:157], v[188:191], v[124:127]
	v_mfma_f32_16x16x32_bf16 v[120:123], v[164:167], v[188:191], v[120:123]
	v_mfma_f32_16x16x32_bf16 v[112:115], v[154:157], v[212:215], v[112:115]
	v_mfma_f32_16x16x32_bf16 v[104:107], v[164:167], v[212:215], v[104:107]
	v_mfma_f32_16x16x32_bf16 v[96:99], v[154:157], v[220:223], v[96:99]
	v_mfma_f32_16x16x32_bf16 v[88:91], v[164:167], v[220:223], v[88:91]
	v_mfma_f32_16x16x32_bf16 v[80:83], v[154:157], v[228:231], v[80:83]
	v_mfma_f32_16x16x32_bf16 v[72:75], v[164:167], v[228:231], v[72:75]
	v_mfma_f32_16x16x32_bf16 v[116:119], v[168:171], v[184:187], v[116:119]
	v_mfma_f32_16x16x32_bf16 v[108:111], v[176:179], v[184:187], v[108:111]
	v_mfma_f32_16x16x32_bf16 v[100:103], v[168:171], v[192:195], v[100:103]
	v_mfma_f32_16x16x32_bf16 v[92:95], v[176:179], v[192:195], v[92:95]
	v_mfma_f32_16x16x32_bf16 v[84:87], v[168:171], v[216:219], v[84:87]
	v_mfma_f32_16x16x32_bf16 v[76:79], v[176:179], v[216:219], v[76:79]
	v_mfma_f32_16x16x32_bf16 v[68:71], v[168:171], v[224:227], v[68:71]
	v_mfma_f32_16x16x32_bf16 v[64:67], v[176:179], v[224:227], v[64:67]
	v_mfma_f32_16x16x32_bf16 v[116:119], v[172:175], v[188:191], v[116:119]
	v_mfma_f32_16x16x32_bf16 v[108:111], v[180:183], v[188:191], v[108:111]
	v_mfma_f32_16x16x32_bf16 v[100:103], v[172:175], v[212:215], v[100:103]
	v_mfma_f32_16x16x32_bf16 v[92:95], v[180:183], v[212:215], v[92:95]
	v_mfma_f32_16x16x32_bf16 v[84:87], v[172:175], v[220:223], v[84:87]
	v_mfma_f32_16x16x32_bf16 v[76:79], v[180:183], v[220:223], v[76:79]
	v_mfma_f32_16x16x32_bf16 v[68:71], v[172:175], v[228:231], v[68:71]
	v_mfma_f32_16x16x32_bf16 v[64:67], v[180:183], v[228:231], v[64:67]
	s_setprio 0
	s_barrier
; #define PG8_STAGE_B(bufoff, gbase) do { _Pragma("unroll") for (int _i = 0; _i < 2; ++_i) \
;         __builtin_amdgcn_global_load_lds((const unsigned*)((const char*)(gbase) + voffB[_i]), (LAS unsigned*)(lds + (bufoff) + ldsw + _i * 8192), 16, 0, 0); } while (0)
; #define PG8_STAGE_A(bufoff, gbase, UA) do { _Pragma("unroll") for (int _i = 0; _i < 2; ++_i) \
;         __builtin_amdgcn_global_load_lds((const unsigned*)((const char*)(gbase) + (UA)[_i]), (LAS unsigned*)(lds + (bufoff) + ldsw + _i * 8192), 16, 0, 0); } while (0)
; #define PG8_LDA(dst, b, h) do { _Pragma("unroll") for (int m = 0; m < 4; ++m) dst[m] = PG8_LD8(lds + PG8_SA(b, h) + aoff + m * 2048); } while (0)
; #define PG8_WAIT_V(n) asm volatile("s_waitcnt vmcnt(" #n ")" ::: "memory")
; #define PG8_WAIT_L(n) asm volatile("s_waitcnt lgkmcnt(" #n ")" ::: "memory")
; #define PG8_BAR __builtin_amdgcn_s_barrier()
; #define PG8_SCHED __builtin_amdgcn_sched_barrier(0)
; template <class Epi, class Sched, bool GATHER, bool FP8 = false>
; __device__ __forceinline__ void gemm_phase(LAS unsigned char* lds, const Gemm g, const Sched& S, const Epi& E, const int wave_s) {
;     ...
;             PG8_LDA(At, 1, 1); PG8_STAGE_B(PG8_SB(1, 0), b3); PG8_STAGE_B(PG8_SB(1, 1), b3 + hstepB); PG8_STAGE_A(PG8_SA(1, 0), a3, u2[0]);
;             PG8_WAIT_V(8); PG8_WAIT_L(0); PG8_BAR; PG8_MMA(1, 0, At, B0); PG8_MMA(1, 1, At, B1); PG8_BAR; PG8_SCHED;
;         }
;         if (wr == 0) PG8_BAR;
	s_mov_b32 m0, s72
	v_lshl_add_u64 v[140:141], v[140:141], 0, s[96:97]
	ds_read_b128 v[184:187], v144 offset:49152
	ds_read_b128 v[188:191], v144 offset:50176
	ds_read_b128 v[192:195], v144 offset:51200
	ds_read_b128 v[212:215], v144 offset:52224
	ds_read_b128 v[216:219], v144 offset:53248
	ds_read_b128 v[220:223], v144 offset:54272
	ds_read_b128 v[224:227], v144 offset:55296
	ds_read_b128 v[228:231], v144 offset:56320
	global_load_lds_dwordx4 v[140:141], off
	v_lshl_add_u64 v[140:141], v[150:151], 0, s[96:97]
	s_mov_b32 m0, s71
	s_nop 0
	global_load_lds_dwordx4 v[140:141], off
	v_lshl_add_u64 v[140:141], s[50:51], 0, v[152:153]
	s_mov_b32 m0, vcc_hi
	s_nop 0
	global_load_lds_dwordx4 v[140:141], off
	v_lshl_add_u64 v[140:141], s[50:51], 0, v[128:129]
	s_mov_b32 m0, vcc_lo
	s_nop 0
	global_load_lds_dwordx4 v[140:141], off
	v_lshl_add_u64 v[140:141], v[232:233], 0, s[96:97]
	s_mov_b32 m0, s66
	s_nop 0
	global_load_lds_dwordx4 v[140:141], off
	v_lshl_add_u64 v[140:141], v[234:235], 0, s[96:97]
	s_mov_b32 m0, s67
	s_nop 0
	global_load_lds_dwordx4 v[140:141], off
	s_waitcnt vmcnt(8)
	s_waitcnt lgkmcnt(0)
	s_barrier
	s_setprio 1
	s_waitcnt lgkmcnt(0)
	v_mfma_f32_16x16x32_bf16 v[60:63], v[146:149], v[184:187], v[60:63]
	v_mfma_f32_16x16x32_bf16 v[56:59], v[158:161], v[184:187], v[56:59]
	v_mfma_f32_16x16x32_bf16 v[40:43], v[146:149], v[192:195], v[40:43]
	v_mfma_f32_16x16x32_bf16 v[32:35], v[158:161], v[192:195], v[32:35]
	v_mfma_f32_16x16x32_bf16 v[16:19], v[146:149], v[216:219], v[16:19]
	v_mfma_f32_16x16x32_bf16 v[12:15], v[158:161], v[216:219], v[12:15]
	v_mfma_f32_16x16x32_bf16 v[4:7], v[146:149], v[224:227], v[4:7]
	v_mfma_f32_16x16x32_bf16 v[0:3], v[158:161], v[224:227], v[0:3]
	v_mfma_f32_16x16x32_bf16 v[60:63], v[154:157], v[188:191], v[60:63]
	v_mfma_f32_16x16x32_bf16 v[56:59], v[164:167], v[188:191], v[56:59]
	v_mfma_f32_16x16x32_bf16 v[40:43], v[154:157], v[212:215], v[40:43]
	v_mfma_f32_16x16x32_bf16 v[32:35], v[164:167], v[212:215], v[32:35]
	v_mfma_f32_16x16x32_bf16 v[16:19], v[154:157], v[220:223], v[16:19]
	v_mfma_f32_16x16x32_bf16 v[12:15], v[164:167], v[220:223], v[12:15]
	v_mfma_f32_16x16x32_bf16 v[4:7], v[154:157], v[228:231], v[4:7]
	v_mfma_f32_16x16x32_bf16 v[0:3], v[164:167], v[228:231], v[0:3]
	v_mfma_f32_16x16x32_bf16 v[44:47], v[168:171], v[184:187], v[44:47]
	v_mfma_f32_16x16x32_bf16 v[36:39], v[176:179], v[184:187], v[36:39]
	v_mfma_f32_16x16x32_bf16 v[20:23], v[168:171], v[192:195], v[20:23]
	v_mfma_f32_16x16x32_bf16 v[8:11], v[176:179], v[192:195], v[8:11]
	v_mfma_f32_16x16x32_bf16 v[48:51], v[168:171], v[216:219], v[48:51]
	v_mfma_f32_16x16x32_bf16 v[52:55], v[176:179], v[216:219], v[52:55]
	v_mfma_f32_16x16x32_bf16 v[24:27], v[168:171], v[224:227], v[24:27]
	v_mfma_f32_16x16x32_bf16 v[28:31], v[176:179], v[224:227], v[28:31]
	v_mfma_f32_16x16x32_bf16 v[44:47], v[172:175], v[188:191], v[44:47]
	v_mfma_f32_16x16x32_bf16 v[36:39], v[180:183], v[188:191], v[36:39]
	v_mfma_f32_16x16x32_bf16 v[20:23], v[172:175], v[212:215], v[20:23]
	v_mfma_f32_16x16x32_bf16 v[8:11], v[180:183], v[212:215], v[8:11]
	v_mfma_f32_16x16x32_bf16 v[48:51], v[172:175], v[220:223], v[48:51]
	v_mfma_f32_16x16x32_bf16 v[52:55], v[180:183], v[220:223], v[52:55]
	v_mfma_f32_16x16x32_bf16 v[24:27], v[172:175], v[228:231], v[24:27]
	v_mfma_f32_16x16x32_bf16 v[28:31], v[180:183], v[228:231], v[28:31]
	s_setprio 0
	s_barrier
	s_andn2_b64 vcc, exec, s[48:49]
	s_mov_b64 s[50:51], -1
	s_mov_b64 s[48:49], 0
	s_mov_b64 s[52:53], 0x100
	s_cbranch_vccz .LBB0_453
	s_and_b64 vcc, exec, s[10:11]
	s_cbranch_vccz .LBB0_456
	s_barrier

; #define PG8_STAGE_B(bufoff, gbase) do { _Pragma("unroll") for (int _i = 0; _i < 2; ++_i) \
;         __builtin_amdgcn_global_load_lds((const unsigned*)((const char*)(gbase) + voffB[_i]), (LAS unsigned*)(lds + (bufoff) + ldsw + _i * 8192), 16, 0, 0); } while (0)
; #define PG8_STAGE_A(bufoff, gbase, UA) do { _Pragma("unroll") for (int _i = 0; _i < 2; ++_i) \
;         __builtin_amdgcn_global_load_lds((const unsigned*)((const char*)(gbase) + (UA)[_i]), (LAS unsigned*)(lds + (bufoff) + ldsw + _i * 8192), 16, 0, 0); } while (0)
; #define PG8_LDA(dst, b, h) do { _Pragma("unroll") for (int m = 0; m < 4; ++m) dst[m] = PG8_LD8(lds + PG8_SA(b, h) + aoff + m * 2048); } while (0)
; #define PG8_LDB(dst, b, h) do { _Pragma("unroll") for (int n = 0; n < 2; ++n) dst[n] = PG8_LD8(lds + PG8_SB(b, h) + boff + n * 2048); } while (0)
; #define PG8_WAIT_V(n) asm volatile("s_waitcnt vmcnt(" #n ")" ::: "memory")
; #define PG8_WAIT_L(n) asm volatile("s_waitcnt lgkmcnt(" #n ")" ::: "memory")
; #define PG8_BAR __builtin_amdgcn_s_barrier()
; #define PG8_SCHED __builtin_amdgcn_sched_barrier(0)
; template <class Epi, class Sched, bool GATHER, bool FP8 = false>
; __device__ __forceinline__ void gemm_phase(LAS unsigned char* lds, const Gemm g, const Sched& S, const Epi& E, const int wave_s) {
;     ...
;         for (int t = 0; t < nt; t += 2) {
;             const bool last = (t == nt - 2);
;             const char* a1 = cA + (size_t)(t + 1) * kstep;
;             const char* a2 = last ? nA : cA + (size_t)(t + 2) * kstep; const char* b2 = last ? nB : cB + (size_t)(t + 2) * kstep;
;             const char* a3 = a2 + kstep; const char* b3 = b2 + kstep;
;             unsigned u2[2][2];
; #pragma unroll
;             for (int h = 0; h < 2; ++h)
; #pragma unroll
;                 for (int i = 0; i < 2; ++i) u2[h][i] = (GATHER && last) ? uAn[h][i] : uAc[h][i];
;             PG8_LDB(B0, 0, 0); PG8_LDB(B1, 0, 1); PG8_SCHED; PG8_LDA(At, 0, 0); PG8_STAGE_A(PG8_SA(1, 1), a1, uAc[1]);
;             PG8_WAIT_V(8); PG8_WAIT_L(0); PG8_BAR; PG8_MMA(0, 0, At, B0); PG8_MMA(0, 1, At, B1); PG8_BAR; PG8_SCHED;
;             PG8_LDA(At, 0, 1); PG8_STAGE_B(PG8_SB(0, 0), b2); PG8_STAGE_B(PG8_SB(0, 1), b2 + hstepB); PG8_STAGE_A(PG8_SA(0, 0), a2, u2[0]);
;             PG8_WAIT_V(8); PG8_WAIT_L(0); PG8_BAR; PG8_MMA(1, 0, At, B0); PG8_MMA(1, 1, At, B1); PG8_BAR; PG8_SCHED;
.LBB0_469:
	s_add_u32 s58, s44, s52
	s_addc_u32 s59, s45, s53
	s_add_u32 s2, s58, 0x100
	s_addc_u32 s3, s59, 0
	s_and_b64 s[40:41], s[50:51], exec
	s_cselect_b32 s54, s15, s2
	s_cselect_b32 s55, s13, s3
	s_add_u32 s2, s46, s52
	s_addc_u32 s3, s47, s53
	s_add_u32 s2, s2, 0x100
	s_addc_u32 s3, s3, 0
	s_and_b64 s[40:41], s[50:51], exec
	s_cselect_b32 s53, s0, s3
	s_cselect_b32 s52, s1, s2
	s_add_i32 s2, 0, 0x10000
	s_add_i32 s3, 0, 0x14000
	v_add_u32_e32 v145, s2, v142
	s_add_i32 vcc_lo, s2, s5
	ds_read_b128 v[146:149], v145
	ds_read_b128 v[154:157], v145 offset:1024
	ds_read_b128 v[158:161], v145 offset:2048
	ds_read_b128 v[164:167], v145 offset:3072
	v_add_u32_e32 v145, s3, v142
	s_add_i32 m0, s62, 0xc000
	s_add_i32 s4, s62, 0xe000
	s_add_i32 s77, vcc_lo, 0x2000
	ds_read_b128 v[168:171], v145
	ds_read_b128 v[172:175], v145 offset:1024
	ds_read_b128 v[176:179], v145 offset:2048
	ds_read_b128 v[180:183], v145 offset:3072
	s_add_u32 s56, s52, 0x10000
	s_addc_u32 s57, s53, 0
	s_add_i32 s76, 0, 0x18000
	s_add_i32 s91, s3, s5
	s_add_i32 s73, s76, s5
	s_add_i32 s90, s91, 0x2000
	s_add_i32 s74, 0, 0x1c000
	s_add_i32 s72, s73, 0x2000
	s_add_u32 s50, s52, 0x10080
	s_addc_u32 s51, s53, 0
	s_add_i32 vcc_hi, s74, s5
	s_add_i32 s40, vcc_hi, 0x2000
	v_lshl_add_u64 v[150:151], s[58:59], 0, v[136:137]
	v_lshl_add_u64 v[150:151], v[150:151], 0, s[96:97]
	ds_read_b128 v[184:187], v144
	ds_read_b128 v[188:191], v144 offset:1024
	ds_read_b128 v[192:195], v144 offset:2048
	ds_read_b128 v[212:215], v144 offset:3072
	ds_read_b128 v[216:219], v144 offset:4096
	ds_read_b128 v[220:223], v144 offset:5120
	ds_read_b128 v[224:227], v144 offset:6144
	ds_read_b128 v[228:231], v144 offset:7168
	global_load_lds_dwordx4 v[150:151], off
	v_lshl_add_u64 v[150:151], s[58:59], 0, v[138:139]
	v_lshl_add_u64 v[150:151], v[150:151], 0, s[96:97]
	s_mov_b32 m0, s4
	s_nop 0
	global_load_lds_dwordx4 v[150:151], off
	s_waitcnt vmcnt(8)
	s_waitcnt lgkmcnt(0)
	s_barrier
	s_setprio 1
	s_waitcnt lgkmcnt(0)
	v_mfma_f32_16x16x32_bf16 v[124:127], v[146:149], v[184:187], v[124:127]
	v_mfma_f32_16x16x32_bf16 v[120:123], v[158:161], v[184:187], v[120:123]
	v_mfma_f32_16x16x32_bf16 v[116:119], v[146:149], v[192:195], v[116:119]
	v_mfma_f32_16x16x32_bf16 v[112:115], v[158:161], v[192:195], v[112:115]
	v_mfma_f32_16x16x32_bf16 v[108:111], v[146:149], v[216:219], v[108:111]
	v_mfma_f32_16x16x32_bf16 v[104:107], v[158:161], v[216:219], v[104:107]
	v_mfma_f32_16x16x32_bf16 v[100:103], v[146:149], v[224:227], v[100:103]
	v_mfma_f32_16x16x32_bf16 v[96:99], v[158:161], v[224:227], v[96:99]
	v_mfma_f32_16x16x32_bf16 v[124:127], v[154:157], v[188:191], v[124:127]
	v_mfma_f32_16x16x32_bf16 v[120:123], v[164:167], v[188:191], v[120:123]
	v_mfma_f32_16x16x32_bf16 v[116:119], v[154:157], v[212:215], v[116:119]
	v_mfma_f32_16x16x32_bf16 v[112:115], v[164:167], v[212:215], v[112:115]
	v_mfma_f32_16x16x32_bf16 v[108:111], v[154:157], v[220:223], v[108:111]
	v_mfma_f32_16x16x32_bf16 v[104:107], v[164:167], v[220:223], v[104:107]
	v_mfma_f32_16x16x32_bf16 v[100:103], v[154:157], v[228:231], v[100:103]
	v_mfma_f32_16x16x32_bf16 v[96:99], v[164:167], v[228:231], v[96:99]
	v_mfma_f32_16x16x32_bf16 v[68:71], v[168:171], v[184:187], v[68:71]
	v_mfma_f32_16x16x32_bf16 v[64:67], v[176:179], v[184:187], v[64:67]
	v_mfma_f32_16x16x32_bf16 v[52:55], v[168:171], v[192:195], v[52:55]
	v_mfma_f32_16x16x32_bf16 v[48:51], v[176:179], v[192:195], v[48:51]
	v_mfma_f32_16x16x32_bf16 v[44:47], v[168:171], v[216:219], v[44:47]
	v_mfma_f32_16x16x32_bf16 v[40:43], v[176:179], v[216:219], v[40:43]
	v_mfma_f32_16x16x32_bf16 v[36:39], v[168:171], v[224:227], v[36:39]
	v_mfma_f32_16x16x32_bf16 v[32:35], v[176:179], v[224:227], v[32:35]
	v_mfma_f32_16x16x32_bf16 v[68:71], v[172:175], v[188:191], v[68:71]
	v_mfma_f32_16x16x32_bf16 v[64:67], v[180:183], v[188:191], v[64:67]
	v_mfma_f32_16x16x32_bf16 v[52:55], v[172:175], v[212:215], v[52:55]
	v_mfma_f32_16x16x32_bf16 v[48:51], v[180:183], v[212:215], v[48:51]
	v_mfma_f32_16x16x32_bf16 v[44:47], v[172:175], v[220:223], v[44:47]
	v_mfma_f32_16x16x32_bf16 v[40:43], v[180:183], v[220:223], v[40:43]
	v_mfma_f32_16x16x32_bf16 v[36:39], v[172:175], v[228:231], v[36:39]
	v_mfma_f32_16x16x32_bf16 v[32:35], v[180:183], v[228:231], v[32:35]
	s_setprio 0
	s_barrier
	s_mov_b32 m0, vcc_lo
	v_lshl_add_u64 v[150:151], s[52:53], 0, v[130:131]
	ds_read_b128 v[184:187], v144 offset:16384
	ds_read_b128 v[188:191], v144 offset:17408
	ds_read_b128 v[192:195], v144 offset:18432
	ds_read_b128 v[212:215], v144 offset:19456
	ds_read_b128 v[216:219], v144 offset:20480
	ds_read_b128 v[220:223], v144 offset:21504
	ds_read_b128 v[224:227], v144 offset:22528
	ds_read_b128 v[228:231], v144 offset:23552
	global_load_lds_dwordx4 v[150:151], off
	v_lshl_add_u64 v[232:233], s[52:53], 0, v[128:129]
	s_mov_b32 m0, s77
	v_lshl_add_u64 v[234:235], s[56:57], 0, v[130:131]
	global_load_lds_dwordx4 v[232:233], off
	s_mov_b32 m0, s91
	v_lshl_add_u64 v[236:237], s[54:55], 0, v[134:135]
	global_load_lds_dwordx4 v[234:235], off
	v_lshl_add_u64 v[234:235], s[56:57], 0, v[128:129]
	s_mov_b32 m0, s90
	s_nop 0
	global_load_lds_dwordx4 v[234:235], off
	v_lshl_add_u64 v[234:235], s[54:55], 0, v[132:133]
	s_mov_b32 m0, s62
	s_nop 0
	global_load_lds_dwordx4 v[234:235], off
	s_mov_b32 m0, s63
	s_nop 0
	global_load_lds_dwordx4 v[236:237], off
	s_waitcnt vmcnt(8)
	s_waitcnt lgkmcnt(0)
	s_barrier
; #define PG8_STAGE_B(bufoff, gbase) do { _Pragma("unroll") for (int _i = 0; _i < 2; ++_i) \
;         __builtin_amdgcn_global_load_lds((const unsigned*)((const char*)(gbase) + voffB[_i]), (LAS unsigned*)(lds + (bufoff) + ldsw + _i * 8192), 16, 0, 0); } while (0)
; #define PG8_STAGE_A(bufoff, gbase, UA) do { _Pragma("unroll") for (int _i = 0; _i < 2; ++_i) \
;         __builtin_amdgcn_global_load_lds((const unsigned*)((const char*)(gbase) + (UA)[_i]), (LAS unsigned*)(lds + (bufoff) + ldsw + _i * 8192), 16, 0, 0); } while (0)
; #define PG8_LDA(dst, b, h) do { _Pragma("unroll") for (int m = 0; m < 4; ++m) dst[m] = PG8_LD8(lds + PG8_SA(b, h) + aoff + m * 2048); } while (0)
; #define PG8_LDB(dst, b, h) do { _Pragma("unroll") for (int n = 0; n < 2; ++n) dst[n] = PG8_LD8(lds + PG8_SB(b, h) + boff + n * 2048); } while (0)
; #define PG8_WAIT_V(n) asm volatile("s_waitcnt vmcnt(" #n ")" ::: "memory")
; #define PG8_WAIT_L(n) asm volatile("s_waitcnt lgkmcnt(" #n ")" ::: "memory")
; #define PG8_BAR __builtin_amdgcn_s_barrier()
; #define PG8_SCHED __builtin_amdgcn_sched_barrier(0)
; template <class Epi, class Sched, bool GATHER, bool FP8 = false>
; __device__ __forceinline__ void gemm_phase(LAS unsigned char* lds, const Gemm g, const Sched& S, const Epi& E, const int wave_s) {
;     ...
;             PG8_WAIT_V(8); PG8_WAIT_L(0); PG8_BAR; PG8_MMA(1, 0, At, B0); PG8_MMA(1, 1, At, B1); PG8_BAR; PG8_SCHED;
;             PG8_LDB(B0, 1, 0); PG8_LDB(B1, 1, 1); PG8_SCHED; PG8_LDA(At, 1, 0); PG8_STAGE_A(PG8_SA(0, 1), a2, u2[1]);
;             PG8_WAIT_V(8); PG8_WAIT_L(0); PG8_BAR; PG8_MMA(0, 0, At, B0); PG8_MMA(0, 1, At, B1); PG8_BAR; PG8_SCHED;
;             PG8_LDA(At, 1, 1); PG8_STAGE_B(PG8_SB(1, 0), b3); PG8_STAGE_B(PG8_SB(1, 1), b3 + hstepB); PG8_STAGE_A(PG8_SA(1, 0), a3, u2[0]);
;             PG8_WAIT_V(8); PG8_WAIT_L(0); PG8_BAR; PG8_MMA(1, 0, At, B0); PG8_MMA(1, 1, At, B1); PG8_BAR; PG8_SCHED;
	s_setprio 1
	s_waitcnt lgkmcnt(0)
	v_mfma_f32_16x16x32_bf16 v[92:95], v[146:149], v[184:187], v[92:95]
	v_mfma_f32_16x16x32_bf16 v[88:91], v[158:161], v[184:187], v[88:91]
	v_mfma_f32_16x16x32_bf16 v[84:87], v[146:149], v[192:195], v[84:87]
	v_mfma_f32_16x16x32_bf16 v[80:83], v[158:161], v[192:195], v[80:83]
	v_mfma_f32_16x16x32_bf16 v[76:79], v[146:149], v[216:219], v[76:79]
	v_mfma_f32_16x16x32_bf16 v[72:75], v[158:161], v[216:219], v[72:75]
	v_mfma_f32_16x16x32_bf16 v[60:63], v[146:149], v[224:227], v[60:63]
	v_mfma_f32_16x16x32_bf16 v[56:59], v[158:161], v[224:227], v[56:59]
	v_mfma_f32_16x16x32_bf16 v[92:95], v[154:157], v[188:191], v[92:95]
	v_mfma_f32_16x16x32_bf16 v[88:91], v[164:167], v[188:191], v[88:91]
	v_mfma_f32_16x16x32_bf16 v[84:87], v[154:157], v[212:215], v[84:87]
	v_mfma_f32_16x16x32_bf16 v[80:83], v[164:167], v[212:215], v[80:83]
	v_mfma_f32_16x16x32_bf16 v[76:79], v[154:157], v[220:223], v[76:79]
	v_mfma_f32_16x16x32_bf16 v[72:75], v[164:167], v[220:223], v[72:75]
	v_mfma_f32_16x16x32_bf16 v[60:63], v[154:157], v[228:231], v[60:63]
	v_mfma_f32_16x16x32_bf16 v[56:59], v[164:167], v[228:231], v[56:59]
	v_mfma_f32_16x16x32_bf16 v[12:15], v[168:171], v[184:187], v[12:15]
	v_mfma_f32_16x16x32_bf16 v[8:11], v[176:179], v[184:187], v[8:11]
	v_mfma_f32_16x16x32_bf16 v[4:7], v[168:171], v[192:195], v[4:7]
	v_mfma_f32_16x16x32_bf16 v[0:3], v[176:179], v[192:195], v[0:3]
	v_mfma_f32_16x16x32_bf16 v[24:27], v[168:171], v[216:219], v[24:27]
	v_mfma_f32_16x16x32_bf16 v[28:31], v[176:179], v[216:219], v[28:31]
	v_mfma_f32_16x16x32_bf16 v[16:19], v[168:171], v[224:227], v[16:19]
	v_mfma_f32_16x16x32_bf16 v[20:23], v[176:179], v[224:227], v[20:23]
	v_mfma_f32_16x16x32_bf16 v[12:15], v[172:175], v[188:191], v[12:15]
	v_mfma_f32_16x16x32_bf16 v[8:11], v[180:183], v[188:191], v[8:11]
	v_mfma_f32_16x16x32_bf16 v[4:7], v[172:175], v[212:215], v[4:7]
	v_mfma_f32_16x16x32_bf16 v[0:3], v[180:183], v[212:215], v[0:3]
	v_mfma_f32_16x16x32_bf16 v[24:27], v[172:175], v[220:223], v[24:27]
	v_mfma_f32_16x16x32_bf16 v[28:31], v[180:183], v[220:223], v[28:31]
	v_mfma_f32_16x16x32_bf16 v[16:19], v[172:175], v[228:231], v[16:19]
	v_mfma_f32_16x16x32_bf16 v[20:23], v[180:183], v[228:231], v[20:23]
	s_setprio 0
	s_barrier
	v_add_u32_e32 v145, s76, v142
	ds_read_b128 v[146:149], v145
	ds_read_b128 v[154:157], v145 offset:1024
	ds_read_b128 v[158:161], v145 offset:2048
	ds_read_b128 v[164:167], v145 offset:3072
	v_add_u32_e32 v145, s74, v142
	ds_read_b128 v[168:171], v145
	ds_read_b128 v[172:175], v145 offset:1024
	ds_read_b128 v[176:179], v145 offset:2048
	ds_read_b128 v[180:183], v145 offset:3072
	s_mov_b32 m0, s64
	v_lshl_add_u64 v[238:239], s[54:55], 0, v[136:137]
	ds_read_b128 v[184:187], v144 offset:32768
	ds_read_b128 v[188:191], v144 offset:33792
	ds_read_b128 v[192:195], v144 offset:34816
	ds_read_b128 v[212:215], v144 offset:35840
	ds_read_b128 v[216:219], v144 offset:36864
	ds_read_b128 v[220:223], v144 offset:37888
	ds_read_b128 v[224:227], v144 offset:38912
	ds_read_b128 v[228:231], v144 offset:39936
	global_load_lds_dwordx4 v[238:239], off
	v_lshl_add_u64 v[238:239], s[54:55], 0, v[138:139]
	s_mov_b32 m0, s65
	s_nop 0
	global_load_lds_dwordx4 v[238:239], off
	s_waitcnt vmcnt(8)
	s_waitcnt lgkmcnt(0)
	s_barrier
	s_setprio 1
	s_waitcnt lgkmcnt(0)
	v_mfma_f32_16x16x32_bf16 v[124:127], v[146:149], v[184:187], v[124:127]
	v_mfma_f32_16x16x32_bf16 v[120:123], v[158:161], v[184:187], v[120:123]
	v_mfma_f32_16x16x32_bf16 v[116:119], v[146:149], v[192:195], v[116:119]
	v_mfma_f32_16x16x32_bf16 v[112:115], v[158:161], v[192:195], v[112:115]
	v_mfma_f32_16x16x32_bf16 v[108:111], v[146:149], v[216:219], v[108:111]
	v_mfma_f32_16x16x32_bf16 v[104:107], v[158:161], v[216:219], v[104:107]
	v_mfma_f32_16x16x32_bf16 v[100:103], v[146:149], v[224:227], v[100:103]
	v_mfma_f32_16x16x32_bf16 v[96:99], v[158:161], v[224:227], v[96:99]
	v_mfma_f32_16x16x32_bf16 v[124:127], v[154:157], v[188:191], v[124:127]
	v_mfma_f32_16x16x32_bf16 v[120:123], v[164:167], v[188:191], v[120:123]
	v_mfma_f32_16x16x32_bf16 v[116:119], v[154:157], v[212:215], v[116:119]
	v_mfma_f32_16x16x32_bf16 v[112:115], v[164:167], v[212:215], v[112:115]
	v_mfma_f32_16x16x32_bf16 v[108:111], v[154:157], v[220:223], v[108:111]
	v_mfma_f32_16x16x32_bf16 v[104:107], v[164:167], v[220:223], v[104:107]
	v_mfma_f32_16x16x32_bf16 v[100:103], v[154:157], v[228:231], v[100:103]
	v_mfma_f32_16x16x32_bf16 v[96:99], v[164:167], v[228:231], v[96:99]
	v_mfma_f32_16x16x32_bf16 v[68:71], v[168:171], v[184:187], v[68:71]
	v_mfma_f32_16x16x32_bf16 v[64:67], v[176:179], v[184:187], v[64:67]
	v_mfma_f32_16x16x32_bf16 v[52:55], v[168:171], v[192:195], v[52:55]
	v_mfma_f32_16x16x32_bf16 v[48:51], v[176:179], v[192:195], v[48:51]
	v_mfma_f32_16x16x32_bf16 v[44:47], v[168:171], v[216:219], v[44:47]
	v_mfma_f32_16x16x32_bf16 v[40:43], v[176:179], v[216:219], v[40:43]
	v_mfma_f32_16x16x32_bf16 v[36:39], v[168:171], v[224:227], v[36:39]
	v_mfma_f32_16x16x32_bf16 v[32:35], v[176:179], v[224:227], v[32:35]
	v_mfma_f32_16x16x32_bf16 v[68:71], v[172:175], v[188:191], v[68:71]
	v_mfma_f32_16x16x32_bf16 v[64:67], v[180:183], v[188:191], v[64:67]
	v_mfma_f32_16x16x32_bf16 v[52:55], v[172:175], v[212:215], v[52:55]
	v_mfma_f32_16x16x32_bf16 v[48:51], v[180:183], v[212:215], v[48:51]
	v_mfma_f32_16x16x32_bf16 v[44:47], v[172:175], v[220:223], v[44:47]
	v_mfma_f32_16x16x32_bf16 v[40:43], v[180:183], v[220:223], v[40:43]
	v_mfma_f32_16x16x32_bf16 v[36:39], v[172:175], v[228:231], v[36:39]
	v_mfma_f32_16x16x32_bf16 v[32:35], v[180:183], v[228:231], v[32:35]
	s_setprio 0
	s_barrier
; #define PG8_STAGE_B(bufoff, gbase) do { _Pragma("unroll") for (int _i = 0; _i < 2; ++_i) \
;         __builtin_amdgcn_global_load_lds((const unsigned*)((const char*)(gbase) + voffB[_i]), (LAS unsigned*)(lds + (bufoff) + ldsw + _i * 8192), 16, 0, 0); } while (0)
; #define PG8_STAGE_A(bufoff, gbase, UA) do { _Pragma("unroll") for (int _i = 0; _i < 2; ++_i) \
;         __builtin_amdgcn_global_load_lds((const unsigned*)((const char*)(gbase) + (UA)[_i]), (LAS unsigned*)(lds + (bufoff) + ldsw + _i * 8192), 16, 0, 0); } while (0)
; #define PG8_LDA(dst, b, h) do { _Pragma("unroll") for (int m = 0; m < 4; ++m) dst[m] = PG8_LD8(lds + PG8_SA(b, h) + aoff + m * 2048); } while (0)
; #define PG8_WAIT_V(n) asm volatile("s_waitcnt vmcnt(" #n ")" ::: "memory")
; #define PG8_WAIT_L(n) asm volatile("s_waitcnt lgkmcnt(" #n ")" ::: "memory")
; #define PG8_BAR __builtin_amdgcn_s_barrier()
; #define PG8_SCHED __builtin_amdgcn_sched_barrier(0)
; template <class Epi, class Sched, bool GATHER, bool FP8 = false>
; __device__ __forceinline__ void gemm_phase(LAS unsigned char* lds, const Gemm g, const Sched& S, const Epi& E, const int wave_s) {
;     ...
;             PG8_LDA(At, 1, 1); PG8_STAGE_B(PG8_SB(1, 0), b3); PG8_STAGE_B(PG8_SB(1, 1), b3 + hstepB); PG8_STAGE_A(PG8_SA(1, 0), a3, u2[0]);
;             PG8_WAIT_V(8); PG8_WAIT_L(0); PG8_BAR; PG8_MMA(1, 0, At, B0); PG8_MMA(1, 1, At, B1); PG8_BAR; PG8_SCHED;
;         }
;         if (wr == 0) PG8_BAR;
	s_mov_b32 m0, s73
	v_lshl_add_u64 v[150:151], v[150:151], 0, s[96:97]
	ds_read_b128 v[184:187], v144 offset:49152
	ds_read_b128 v[188:191], v144 offset:50176
	ds_read_b128 v[192:195], v144 offset:51200
	ds_read_b128 v[212:215], v144 offset:52224
	ds_read_b128 v[216:219], v144 offset:53248
	ds_read_b128 v[220:223], v144 offset:54272
	ds_read_b128 v[224:227], v144 offset:55296
	ds_read_b128 v[228:231], v144 offset:56320
	global_load_lds_dwordx4 v[150:151], off
	v_lshl_add_u64 v[150:151], v[232:233], 0, s[96:97]
	s_mov_b32 m0, s72
	s_nop 0
	global_load_lds_dwordx4 v[150:151], off
	v_lshl_add_u64 v[150:151], s[50:51], 0, v[130:131]
	s_mov_b32 m0, vcc_hi
	s_nop 0
	global_load_lds_dwordx4 v[150:151], off
	v_lshl_add_u64 v[150:151], s[50:51], 0, v[128:129]
	s_mov_b32 m0, s40
	s_nop 0
	global_load_lds_dwordx4 v[150:151], off
	v_lshl_add_u64 v[150:151], v[234:235], 0, s[96:97]
	s_mov_b32 m0, s67
	s_nop 0
	global_load_lds_dwordx4 v[150:151], off
	v_lshl_add_u64 v[150:151], v[236:237], 0, s[96:97]
	s_mov_b32 m0, s68
	s_nop 0
	global_load_lds_dwordx4 v[150:151], off
	s_waitcnt vmcnt(8)
	s_waitcnt lgkmcnt(0)
	s_barrier
	s_setprio 1
	s_waitcnt lgkmcnt(0)
	v_mfma_f32_16x16x32_bf16 v[92:95], v[146:149], v[184:187], v[92:95]
	v_mfma_f32_16x16x32_bf16 v[88:91], v[158:161], v[184:187], v[88:91]
	v_mfma_f32_16x16x32_bf16 v[84:87], v[146:149], v[192:195], v[84:87]
	v_mfma_f32_16x16x32_bf16 v[80:83], v[158:161], v[192:195], v[80:83]
	v_mfma_f32_16x16x32_bf16 v[76:79], v[146:149], v[216:219], v[76:79]
	v_mfma_f32_16x16x32_bf16 v[72:75], v[158:161], v[216:219], v[72:75]
	v_mfma_f32_16x16x32_bf16 v[60:63], v[146:149], v[224:227], v[60:63]
	v_mfma_f32_16x16x32_bf16 v[56:59], v[158:161], v[224:227], v[56:59]
	v_mfma_f32_16x16x32_bf16 v[92:95], v[154:157], v[188:191], v[92:95]
	v_mfma_f32_16x16x32_bf16 v[88:91], v[164:167], v[188:191], v[88:91]
	v_mfma_f32_16x16x32_bf16 v[84:87], v[154:157], v[212:215], v[84:87]
	v_mfma_f32_16x16x32_bf16 v[80:83], v[164:167], v[212:215], v[80:83]
	v_mfma_f32_16x16x32_bf16 v[76:79], v[154:157], v[220:223], v[76:79]
	v_mfma_f32_16x16x32_bf16 v[72:75], v[164:167], v[220:223], v[72:75]
	v_mfma_f32_16x16x32_bf16 v[60:63], v[154:157], v[228:231], v[60:63]
	v_mfma_f32_16x16x32_bf16 v[56:59], v[164:167], v[228:231], v[56:59]
	v_mfma_f32_16x16x32_bf16 v[12:15], v[168:171], v[184:187], v[12:15]
	v_mfma_f32_16x16x32_bf16 v[8:11], v[176:179], v[184:187], v[8:11]
	v_mfma_f32_16x16x32_bf16 v[4:7], v[168:171], v[192:195], v[4:7]
	v_mfma_f32_16x16x32_bf16 v[0:3], v[176:179], v[192:195], v[0:3]
	v_mfma_f32_16x16x32_bf16 v[24:27], v[168:171], v[216:219], v[24:27]
	v_mfma_f32_16x16x32_bf16 v[28:31], v[176:179], v[216:219], v[28:31]
	v_mfma_f32_16x16x32_bf16 v[16:19], v[168:171], v[224:227], v[16:19]
	v_mfma_f32_16x16x32_bf16 v[20:23], v[176:179], v[224:227], v[20:23]
	v_mfma_f32_16x16x32_bf16 v[12:15], v[172:175], v[188:191], v[12:15]
	v_mfma_f32_16x16x32_bf16 v[8:11], v[180:183], v[188:191], v[8:11]
	v_mfma_f32_16x16x32_bf16 v[4:7], v[172:175], v[212:215], v[4:7]
	v_mfma_f32_16x16x32_bf16 v[0:3], v[180:183], v[212:215], v[0:3]
	v_mfma_f32_16x16x32_bf16 v[24:27], v[172:175], v[220:223], v[24:27]
	v_mfma_f32_16x16x32_bf16 v[28:31], v[180:183], v[220:223], v[28:31]
	v_mfma_f32_16x16x32_bf16 v[16:19], v[172:175], v[228:231], v[16:19]
	v_mfma_f32_16x16x32_bf16 v[20:23], v[180:183], v[228:231], v[20:23]
	s_setprio 0
	s_barrier
	s_andn2_b64 vcc, exec, s[48:49]
	s_mov_b64 s[50:51], -1
	s_mov_b64 s[48:49], 0
	s_mov_b64 s[52:53], 0x100
	s_cbranch_vccz .LBB0_469
	s_and_b64 vcc, exec, s[10:11]
	s_cbranch_vccz .LBB0_472
	s_barrier

; #define PG8_STAGE_B(bufoff, gbase) do { _Pragma("unroll") for (int _i = 0; _i < 2; ++_i) \
;         __builtin_amdgcn_global_load_lds((const unsigned*)((const char*)(gbase) + voffB[_i]), (LAS unsigned*)(lds + (bufoff) + ldsw + _i * 8192), 16, 0, 0); } while (0)
; #define PG8_STAGE_A(bufoff, gbase, UA) do { _Pragma("unroll") for (int _i = 0; _i < 2; ++_i) \
;         __builtin_amdgcn_global_load_lds((const unsigned*)((const char*)(gbase) + (UA)[_i]), (LAS unsigned*)(lds + (bufoff) + ldsw + _i * 8192), 16, 0, 0); } while (0)
; #define PG8_LDA(dst, b, h) do { _Pragma("unroll") for (int m = 0; m < 4; ++m) dst[m] = PG8_LD8(lds + PG8_SA(b, h) + aoff + m * 2048); } while (0)
; #define PG8_LDB(dst, b, h) do { _Pragma("unroll") for (int n = 0; n < 2; ++n) dst[n] = PG8_LD8(lds + PG8_SB(b, h) + boff + n * 2048); } while (0)
; #define PG8_WAIT_V(n) asm volatile("s_waitcnt vmcnt(" #n ")" ::: "memory")
; #define PG8_WAIT_L(n) asm volatile("s_waitcnt lgkmcnt(" #n ")" ::: "memory")
; #define PG8_BAR __builtin_amdgcn_s_barrier()
; #define PG8_SCHED __builtin_amdgcn_sched_barrier(0)
; template <class Epi, class Sched, bool GATHER, bool FP8 = false>
; __device__ __forceinline__ void gemm_phase(LAS unsigned char* lds, const Gemm g, const Sched& S, const Epi& E, const int wave_s) {
;     ...
;         for (int t = 0; t < nt; t += 2) {
;             const bool last = (t == nt - 2);
;             const char* a1 = cA + (size_t)(t + 1) * kstep;
;             const char* a2 = last ? nA : cA + (size_t)(t + 2) * kstep; const char* b2 = last ? nB : cB + (size_t)(t + 2) * kstep;
;             const char* a3 = a2 + kstep; const char* b3 = b2 + kstep;
;             unsigned u2[2][2];
; #pragma unroll
;             for (int h = 0; h < 2; ++h)
; #pragma unroll
;                 for (int i = 0; i < 2; ++i) u2[h][i] = (GATHER && last) ? uAn[h][i] : uAc[h][i];
;             PG8_LDB(B0, 0, 0); PG8_LDB(B1, 0, 1); PG8_SCHED; PG8_LDA(At, 0, 0); PG8_STAGE_A(PG8_SA(1, 1), a1, uAc[1]);
;             PG8_WAIT_V(8); PG8_WAIT_L(0); PG8_BAR; PG8_MMA(0, 0, At, B0); PG8_MMA(0, 1, At, B1); PG8_BAR; PG8_SCHED;
;             PG8_LDA(At, 0, 1); PG8_STAGE_B(PG8_SB(0, 0), b2); PG8_STAGE_B(PG8_SB(0, 1), b2 + hstepB); PG8_STAGE_A(PG8_SA(0, 0), a2, u2[0]);
;             PG8_WAIT_V(8); PG8_WAIT_L(0); PG8_BAR; PG8_MMA(1, 0, At, B0); PG8_MMA(1, 1, At, B1); PG8_BAR; PG8_SCHED;
.LBB0_654:
	s_add_u32 s0, s40, s8
	s_addc_u32 s1, s41, s9
	s_add_u32 s0, s0, 0x5bf00100
	s_addc_u32 s1, s1, 0
	s_add_u32 s2, s42, s8
	s_addc_u32 s3, s43, s9
	s_cmpk_eq_i32 s8, 0x700
	s_cselect_b32 s1, s21, s1
	s_cselect_b32 s0, s20, s0
	s_cselect_b32 s11, s7, s3
	s_cselect_b32 s10, s6, s2
	s_add_i32 s2, 0, 0x10000
	v_add_u32_e32 v155, s2, v146
	s_add_i32 s4, 0, 0x14000
	ds_read_b128 v[148:151], v155
	ds_read_b128 v[156:159], v155 offset:1024
	ds_read_b128 v[164:167], v155 offset:2048
	ds_read_b128 v[168:171], v155 offset:3072
	v_add_u32_e32 v155, s4, v146
	ds_read_b128 v[172:175], v155
	ds_read_b128 v[176:179], v155 offset:1024
	ds_read_b128 v[180:183], v155 offset:2048
	ds_read_b128 v[184:187], v155 offset:3072
	v_lshl_add_u64 v[160:161], v[142:143], 0, s[8:9]
	s_add_i32 m0, s13, 0xc000
	ds_read_b128 v[188:191], v147
	ds_read_b128 v[192:195], v147 offset:1024
	ds_read_b128 v[212:215], v147 offset:2048
	ds_read_b128 v[216:219], v147 offset:3072
	ds_read_b128 v[220:223], v147 offset:4096
	ds_read_b128 v[224:227], v147 offset:5120
	ds_read_b128 v[228:231], v147 offset:6144
	ds_read_b128 v[232:235], v147 offset:7168
	global_load_lds_dwordx4 v[160:161], off
	v_lshl_add_u64 v[160:161], v[140:141], 0, s[8:9]
	s_add_i32 m0, s13, 0xe000
	s_nop 0
	global_load_lds_dwordx4 v[160:161], off
	s_waitcnt vmcnt(8)
	s_waitcnt lgkmcnt(0)
	s_barrier
	s_setprio 1
	s_waitcnt lgkmcnt(0)
	v_mfma_f32_16x16x32_bf16 v[124:127], v[148:151], v[188:191], v[124:127]
	v_mfma_f32_16x16x32_bf16 v[120:123], v[164:167], v[188:191], v[120:123]
	v_mfma_f32_16x16x32_bf16 v[116:119], v[148:151], v[212:215], v[116:119]
	v_mfma_f32_16x16x32_bf16 v[108:111], v[164:167], v[212:215], v[108:111]
	v_mfma_f32_16x16x32_bf16 v[100:103], v[148:151], v[220:223], v[100:103]
	v_mfma_f32_16x16x32_bf16 v[92:95], v[164:167], v[220:223], v[92:95]
	v_mfma_f32_16x16x32_bf16 v[80:83], v[148:151], v[228:231], v[80:83]
	v_mfma_f32_16x16x32_bf16 v[72:75], v[164:167], v[228:231], v[72:75]
	v_mfma_f32_16x16x32_bf16 v[124:127], v[156:159], v[192:195], v[124:127]
	v_mfma_f32_16x16x32_bf16 v[120:123], v[168:171], v[192:195], v[120:123]
	v_mfma_f32_16x16x32_bf16 v[116:119], v[156:159], v[216:219], v[116:119]
	v_mfma_f32_16x16x32_bf16 v[108:111], v[168:171], v[216:219], v[108:111]
	v_mfma_f32_16x16x32_bf16 v[100:103], v[156:159], v[224:227], v[100:103]
	v_mfma_f32_16x16x32_bf16 v[92:95], v[168:171], v[224:227], v[92:95]
	v_mfma_f32_16x16x32_bf16 v[80:83], v[156:159], v[232:235], v[80:83]
	v_mfma_f32_16x16x32_bf16 v[72:75], v[168:171], v[232:235], v[72:75]
	v_mfma_f32_16x16x32_bf16 v[112:115], v[172:175], v[188:191], v[112:115]
	v_mfma_f32_16x16x32_bf16 v[104:107], v[180:183], v[188:191], v[104:107]
	v_mfma_f32_16x16x32_bf16 v[96:99], v[172:175], v[212:215], v[96:99]
	v_mfma_f32_16x16x32_bf16 v[88:91], v[180:183], v[212:215], v[88:91]
	v_mfma_f32_16x16x32_bf16 v[84:87], v[172:175], v[220:223], v[84:87]
	v_mfma_f32_16x16x32_bf16 v[76:79], v[180:183], v[220:223], v[76:79]
	v_mfma_f32_16x16x32_bf16 v[68:71], v[172:175], v[228:231], v[68:71]
	v_mfma_f32_16x16x32_bf16 v[64:67], v[180:183], v[228:231], v[64:67]
	v_mfma_f32_16x16x32_bf16 v[112:115], v[176:179], v[192:195], v[112:115]
	v_mfma_f32_16x16x32_bf16 v[104:107], v[184:187], v[192:195], v[104:107]
	v_mfma_f32_16x16x32_bf16 v[96:99], v[176:179], v[216:219], v[96:99]
	v_mfma_f32_16x16x32_bf16 v[88:91], v[184:187], v[216:219], v[88:91]
	v_mfma_f32_16x16x32_bf16 v[84:87], v[176:179], v[224:227], v[84:87]
	v_mfma_f32_16x16x32_bf16 v[76:79], v[184:187], v[224:227], v[76:79]
	v_mfma_f32_16x16x32_bf16 v[68:71], v[176:179], v[232:235], v[68:71]
	v_mfma_f32_16x16x32_bf16 v[64:67], v[184:187], v[232:235], v[64:67]
	s_setprio 0
	s_barrier
	s_add_i32 s2, s2, s12
	v_lshl_add_u64 v[160:161], s[10:11], 0, v[152:153]
	s_mov_b32 m0, s2
	ds_read_b128 v[188:191], v147 offset:16384
	ds_read_b128 v[192:195], v147 offset:17408
	ds_read_b128 v[212:215], v147 offset:18432
	ds_read_b128 v[216:219], v147 offset:19456
	ds_read_b128 v[220:223], v147 offset:20480
	ds_read_b128 v[224:227], v147 offset:21504
	ds_read_b128 v[228:231], v147 offset:22528
	ds_read_b128 v[232:235], v147 offset:23552
	global_load_lds_dwordx4 v[160:161], off
	s_add_i32 m0, s2, 0x2000
	s_add_u32 s2, s10, 0x40000
	v_lshl_add_u64 v[236:237], s[10:11], 0, v[130:131]
	s_addc_u32 s3, s11, 0
	s_add_i32 s4, s4, s12
	global_load_lds_dwordx4 v[236:237], off
	v_lshl_add_u64 v[238:239], s[2:3], 0, v[152:153]
	s_mov_b32 m0, s4
	v_lshl_add_u64 v[240:241], s[0:1], 0, v[134:135]
	global_load_lds_dwordx4 v[238:239], off
	v_lshl_add_u64 v[238:239], s[2:3], 0, v[130:131]
	s_add_i32 m0, s4, 0x2000
	s_nop 0
	global_load_lds_dwordx4 v[238:239], off
	v_lshl_add_u64 v[238:239], s[0:1], 0, v[132:133]
	s_mov_b32 m0, s13
	s_nop 0
	global_load_lds_dwordx4 v[238:239], off
	s_mov_b32 m0, s14
	s_nop 0
	global_load_lds_dwordx4 v[240:241], off
	s_waitcnt vmcnt(8)
	s_waitcnt lgkmcnt(0)
	s_barrier
; #define PG8_STAGE_A(bufoff, gbase, UA) do { _Pragma("unroll") for (int _i = 0; _i < 2; ++_i) \
;         __builtin_amdgcn_global_load_lds((const unsigned*)((const char*)(gbase) + (UA)[_i]), (LAS unsigned*)(lds + (bufoff) + ldsw + _i * 8192), 16, 0, 0); } while (0)
; #define PG8_LDA(dst, b, h) do { _Pragma("unroll") for (int m = 0; m < 4; ++m) dst[m] = PG8_LD8(lds + PG8_SA(b, h) + aoff + m * 2048); } while (0)
; #define PG8_LDB(dst, b, h) do { _Pragma("unroll") for (int n = 0; n < 2; ++n) dst[n] = PG8_LD8(lds + PG8_SB(b, h) + boff + n * 2048); } while (0)
; #define PG8_WAIT_V(n) asm volatile("s_waitcnt vmcnt(" #n ")" ::: "memory")
; #define PG8_WAIT_L(n) asm volatile("s_waitcnt lgkmcnt(" #n ")" ::: "memory")
; #define PG8_BAR __builtin_amdgcn_s_barrier()
; #define PG8_SCHED __builtin_amdgcn_sched_barrier(0)
; template <class Epi, class Sched, bool GATHER, bool FP8 = false>
; __device__ __forceinline__ void gemm_phase(LAS unsigned char* lds, const Gemm g, const Sched& S, const Epi& E, const int wave_s) {
;     ...
;             PG8_WAIT_V(8); PG8_WAIT_L(0); PG8_BAR; PG8_MMA(1, 0, At, B0); PG8_MMA(1, 1, At, B1); PG8_BAR; PG8_SCHED;
;             PG8_LDB(B0, 1, 0); PG8_LDB(B1, 1, 1); PG8_SCHED; PG8_LDA(At, 1, 0); PG8_STAGE_A(PG8_SA(0, 1), a2, u2[1]);
;             PG8_WAIT_V(8); PG8_WAIT_L(0); PG8_BAR; PG8_MMA(0, 0, At, B0); PG8_MMA(0, 1, At, B1); PG8_BAR; PG8_SCHED;
	s_setprio 1
	s_waitcnt lgkmcnt(0)
	v_mfma_f32_16x16x32_bf16 v[60:63], v[148:151], v[188:191], v[60:63]
	v_mfma_f32_16x16x32_bf16 v[56:59], v[164:167], v[188:191], v[56:59]
	v_mfma_f32_16x16x32_bf16 v[44:47], v[148:151], v[212:215], v[44:47]
	v_mfma_f32_16x16x32_bf16 v[36:39], v[164:167], v[212:215], v[36:39]
	v_mfma_f32_16x16x32_bf16 v[20:23], v[148:151], v[220:223], v[20:23]
	v_mfma_f32_16x16x32_bf16 v[12:15], v[164:167], v[220:223], v[12:15]
	v_mfma_f32_16x16x32_bf16 v[4:7], v[148:151], v[228:231], v[4:7]
	v_mfma_f32_16x16x32_bf16 v[0:3], v[164:167], v[228:231], v[0:3]
	v_mfma_f32_16x16x32_bf16 v[60:63], v[156:159], v[192:195], v[60:63]
	v_mfma_f32_16x16x32_bf16 v[56:59], v[168:171], v[192:195], v[56:59]
	v_mfma_f32_16x16x32_bf16 v[44:47], v[156:159], v[216:219], v[44:47]
	v_mfma_f32_16x16x32_bf16 v[36:39], v[168:171], v[216:219], v[36:39]
	v_mfma_f32_16x16x32_bf16 v[20:23], v[156:159], v[224:227], v[20:23]
	v_mfma_f32_16x16x32_bf16 v[12:15], v[168:171], v[224:227], v[12:15]
	v_mfma_f32_16x16x32_bf16 v[4:7], v[156:159], v[232:235], v[4:7]
	v_mfma_f32_16x16x32_bf16 v[0:3], v[168:171], v[232:235], v[0:3]
	v_mfma_f32_16x16x32_bf16 v[40:43], v[172:175], v[188:191], v[40:43]
	v_mfma_f32_16x16x32_bf16 v[32:35], v[180:183], v[188:191], v[32:35]
	v_mfma_f32_16x16x32_bf16 v[16:19], v[172:175], v[212:215], v[16:19]
	v_mfma_f32_16x16x32_bf16 v[8:11], v[180:183], v[212:215], v[8:11]
	v_mfma_f32_16x16x32_bf16 v[52:55], v[172:175], v[220:223], v[52:55]
	v_mfma_f32_16x16x32_bf16 v[48:51], v[180:183], v[220:223], v[48:51]
	v_mfma_f32_16x16x32_bf16 v[28:31], v[172:175], v[228:231], v[28:31]
	v_mfma_f32_16x16x32_bf16 v[24:27], v[180:183], v[228:231], v[24:27]
	v_mfma_f32_16x16x32_bf16 v[40:43], v[176:179], v[192:195], v[40:43]
	v_mfma_f32_16x16x32_bf16 v[32:35], v[184:187], v[192:195], v[32:35]
	v_mfma_f32_16x16x32_bf16 v[16:19], v[176:179], v[216:219], v[16:19]
	v_mfma_f32_16x16x32_bf16 v[8:11], v[184:187], v[216:219], v[8:11]
	v_mfma_f32_16x16x32_bf16 v[52:55], v[176:179], v[224:227], v[52:55]
	v_mfma_f32_16x16x32_bf16 v[48:51], v[184:187], v[224:227], v[48:51]
	v_mfma_f32_16x16x32_bf16 v[28:31], v[176:179], v[232:235], v[28:31]
	v_mfma_f32_16x16x32_bf16 v[24:27], v[184:187], v[232:235], v[24:27]
	s_setprio 0
	s_barrier
	s_add_i32 s2, 0, 0x18000
	v_add_u32_e32 v155, s2, v146
	s_add_i32 s3, 0, 0x1c000
	ds_read_b128 v[148:151], v155
	ds_read_b128 v[156:159], v155 offset:1024
	ds_read_b128 v[164:167], v155 offset:2048
	ds_read_b128 v[168:171], v155 offset:3072
	v_add_u32_e32 v155, s3, v146
	ds_read_b128 v[172:175], v155
	ds_read_b128 v[176:179], v155 offset:1024
	ds_read_b128 v[180:183], v155 offset:2048
	ds_read_b128 v[184:187], v155 offset:3072
	s_mov_b32 m0, s15
	v_lshl_add_u64 v[242:243], s[0:1], 0, v[136:137]
	ds_read_b128 v[188:191], v147 offset:32768
	ds_read_b128 v[192:195], v147 offset:33792
	ds_read_b128 v[212:215], v147 offset:34816
	ds_read_b128 v[216:219], v147 offset:35840
	ds_read_b128 v[220:223], v147 offset:36864
	ds_read_b128 v[224:227], v147 offset:37888
	ds_read_b128 v[228:231], v147 offset:38912
	ds_read_b128 v[232:235], v147 offset:39936
	global_load_lds_dwordx4 v[242:243], off
	v_lshl_add_u64 v[242:243], s[0:1], 0, v[138:139]
	s_mov_b32 m0, s16
	s_nop 0
	global_load_lds_dwordx4 v[242:243], off
	s_waitcnt vmcnt(8)
	s_waitcnt lgkmcnt(0)
	s_barrier
	s_setprio 1
	s_waitcnt lgkmcnt(0)
	v_mfma_f32_16x16x32_bf16 v[124:127], v[148:151], v[188:191], v[124:127]
	v_mfma_f32_16x16x32_bf16 v[120:123], v[164:167], v[188:191], v[120:123]
	v_mfma_f32_16x16x32_bf16 v[116:119], v[148:151], v[212:215], v[116:119]
	v_mfma_f32_16x16x32_bf16 v[108:111], v[164:167], v[212:215], v[108:111]
	v_mfma_f32_16x16x32_bf16 v[100:103], v[148:151], v[220:223], v[100:103]
	v_mfma_f32_16x16x32_bf16 v[92:95], v[164:167], v[220:223], v[92:95]
	v_mfma_f32_16x16x32_bf16 v[80:83], v[148:151], v[228:231], v[80:83]
	v_mfma_f32_16x16x32_bf16 v[72:75], v[164:167], v[228:231], v[72:75]
	v_mfma_f32_16x16x32_bf16 v[124:127], v[156:159], v[192:195], v[124:127]
	v_mfma_f32_16x16x32_bf16 v[120:123], v[168:171], v[192:195], v[120:123]
	v_mfma_f32_16x16x32_bf16 v[116:119], v[156:159], v[216:219], v[116:119]
	v_mfma_f32_16x16x32_bf16 v[108:111], v[168:171], v[216:219], v[108:111]
	v_mfma_f32_16x16x32_bf16 v[100:103], v[156:159], v[224:227], v[100:103]
	v_mfma_f32_16x16x32_bf16 v[92:95], v[168:171], v[224:227], v[92:95]
	v_mfma_f32_16x16x32_bf16 v[80:83], v[156:159], v[232:235], v[80:83]
	v_mfma_f32_16x16x32_bf16 v[72:75], v[168:171], v[232:235], v[72:75]
	v_mfma_f32_16x16x32_bf16 v[112:115], v[172:175], v[188:191], v[112:115]
	v_mfma_f32_16x16x32_bf16 v[104:107], v[180:183], v[188:191], v[104:107]
	v_mfma_f32_16x16x32_bf16 v[96:99], v[172:175], v[212:215], v[96:99]
	v_mfma_f32_16x16x32_bf16 v[88:91], v[180:183], v[212:215], v[88:91]
	v_mfma_f32_16x16x32_bf16 v[84:87], v[172:175], v[220:223], v[84:87]
	v_mfma_f32_16x16x32_bf16 v[76:79], v[180:183], v[220:223], v[76:79]
	v_mfma_f32_16x16x32_bf16 v[68:71], v[172:175], v[228:231], v[68:71]
	v_mfma_f32_16x16x32_bf16 v[64:67], v[180:183], v[228:231], v[64:67]
	v_mfma_f32_16x16x32_bf16 v[112:115], v[176:179], v[192:195], v[112:115]
	v_mfma_f32_16x16x32_bf16 v[104:107], v[184:187], v[192:195], v[104:107]
	v_mfma_f32_16x16x32_bf16 v[96:99], v[176:179], v[216:219], v[96:99]
	v_mfma_f32_16x16x32_bf16 v[88:91], v[184:187], v[216:219], v[88:91]
	v_mfma_f32_16x16x32_bf16 v[84:87], v[176:179], v[224:227], v[84:87]
	v_mfma_f32_16x16x32_bf16 v[76:79], v[184:187], v[224:227], v[76:79]
	v_mfma_f32_16x16x32_bf16 v[68:71], v[176:179], v[232:235], v[68:71]
	v_mfma_f32_16x16x32_bf16 v[64:67], v[184:187], v[232:235], v[64:67]
	s_setprio 0
	s_barrier
; #define PG8_STAGE_B(bufoff, gbase) do { _Pragma("unroll") for (int _i = 0; _i < 2; ++_i) \
;         __builtin_amdgcn_global_load_lds((const unsigned*)((const char*)(gbase) + voffB[_i]), (LAS unsigned*)(lds + (bufoff) + ldsw + _i * 8192), 16, 0, 0); } while (0)
; #define PG8_STAGE_A(bufoff, gbase, UA) do { _Pragma("unroll") for (int _i = 0; _i < 2; ++_i) \
;         __builtin_amdgcn_global_load_lds((const unsigned*)((const char*)(gbase) + (UA)[_i]), (LAS unsigned*)(lds + (bufoff) + ldsw + _i * 8192), 16, 0, 0); } while (0)
; #define PG8_LDA(dst, b, h) do { _Pragma("unroll") for (int m = 0; m < 4; ++m) dst[m] = PG8_LD8(lds + PG8_SA(b, h) + aoff + m * 2048); } while (0)
; #define PG8_WAIT_V(n) asm volatile("s_waitcnt vmcnt(" #n ")" ::: "memory")
; #define PG8_WAIT_L(n) asm volatile("s_waitcnt lgkmcnt(" #n ")" ::: "memory")
; #define PG8_BAR __builtin_amdgcn_s_barrier()
; #define PG8_SCHED __builtin_amdgcn_sched_barrier(0)
; template <class Epi, class Sched, bool GATHER, bool FP8 = false>
; __device__ __forceinline__ void gemm_phase(LAS unsigned char* lds, const Gemm g, const Sched& S, const Epi& E, const int wave_s) {
;     ...
;             PG8_LDA(At, 1, 1); PG8_STAGE_B(PG8_SB(1, 0), b3); PG8_STAGE_B(PG8_SB(1, 1), b3 + hstepB); PG8_STAGE_A(PG8_SA(1, 0), a3, u2[0]);
;             PG8_WAIT_V(8); PG8_WAIT_L(0); PG8_BAR; PG8_MMA(1, 0, At, B0); PG8_MMA(1, 1, At, B1); PG8_BAR; PG8_SCHED;
;         }
;         if (wr == 0) PG8_BAR;
	s_add_i32 s0, s2, s12
	v_lshl_add_u64 v[160:161], v[160:161], 0, s[96:97]
	s_mov_b32 m0, s0
	ds_read_b128 v[188:191], v147 offset:49152
	ds_read_b128 v[192:195], v147 offset:50176
	ds_read_b128 v[212:215], v147 offset:51200
	ds_read_b128 v[216:219], v147 offset:52224
	ds_read_b128 v[220:223], v147 offset:53248
	ds_read_b128 v[224:227], v147 offset:54272
	ds_read_b128 v[228:231], v147 offset:55296
	ds_read_b128 v[232:235], v147 offset:56320
	global_load_lds_dwordx4 v[160:161], off
	s_add_i32 m0, s0, 0x2000
	s_add_u32 s0, s10, 0x40080
	v_lshl_add_u64 v[160:161], v[236:237], 0, s[96:97]
	s_addc_u32 s1, s11, 0
	s_add_i32 s2, s3, s12
	global_load_lds_dwordx4 v[160:161], off
	v_lshl_add_u64 v[160:161], s[0:1], 0, v[152:153]
	s_mov_b32 m0, s2
	s_nop 0
	global_load_lds_dwordx4 v[160:161], off
	v_lshl_add_u64 v[160:161], s[0:1], 0, v[130:131]
	s_add_i32 m0, s2, 0x2000
	s_nop 0
	global_load_lds_dwordx4 v[160:161], off
	v_lshl_add_u64 v[160:161], v[238:239], 0, s[96:97]
	s_mov_b32 m0, s18
	s_nop 0
	global_load_lds_dwordx4 v[160:161], off
	v_lshl_add_u64 v[160:161], v[240:241], 0, s[96:97]
	s_mov_b32 m0, s19
	s_nop 0
	global_load_lds_dwordx4 v[160:161], off
	s_waitcnt vmcnt(8)
	s_waitcnt lgkmcnt(0)
	s_barrier
	s_setprio 1
	s_waitcnt lgkmcnt(0)
	v_mfma_f32_16x16x32_bf16 v[60:63], v[148:151], v[188:191], v[60:63]
	v_mfma_f32_16x16x32_bf16 v[56:59], v[164:167], v[188:191], v[56:59]
	v_mfma_f32_16x16x32_bf16 v[44:47], v[148:151], v[212:215], v[44:47]
	v_mfma_f32_16x16x32_bf16 v[36:39], v[164:167], v[212:215], v[36:39]
	v_mfma_f32_16x16x32_bf16 v[20:23], v[148:151], v[220:223], v[20:23]
	v_mfma_f32_16x16x32_bf16 v[12:15], v[164:167], v[220:223], v[12:15]
	v_mfma_f32_16x16x32_bf16 v[4:7], v[148:151], v[228:231], v[4:7]
	v_mfma_f32_16x16x32_bf16 v[0:3], v[164:167], v[228:231], v[0:3]
	v_mfma_f32_16x16x32_bf16 v[60:63], v[156:159], v[192:195], v[60:63]
	v_mfma_f32_16x16x32_bf16 v[56:59], v[168:171], v[192:195], v[56:59]
	v_mfma_f32_16x16x32_bf16 v[44:47], v[156:159], v[216:219], v[44:47]
	v_mfma_f32_16x16x32_bf16 v[36:39], v[168:171], v[216:219], v[36:39]
	v_mfma_f32_16x16x32_bf16 v[20:23], v[156:159], v[224:227], v[20:23]
	v_mfma_f32_16x16x32_bf16 v[12:15], v[168:171], v[224:227], v[12:15]
	v_mfma_f32_16x16x32_bf16 v[4:7], v[156:159], v[232:235], v[4:7]
	v_mfma_f32_16x16x32_bf16 v[0:3], v[168:171], v[232:235], v[0:3]
	v_mfma_f32_16x16x32_bf16 v[40:43], v[172:175], v[188:191], v[40:43]
	v_mfma_f32_16x16x32_bf16 v[32:35], v[180:183], v[188:191], v[32:35]
	v_mfma_f32_16x16x32_bf16 v[16:19], v[172:175], v[212:215], v[16:19]
	v_mfma_f32_16x16x32_bf16 v[8:11], v[180:183], v[212:215], v[8:11]
	v_mfma_f32_16x16x32_bf16 v[52:55], v[172:175], v[220:223], v[52:55]
	v_mfma_f32_16x16x32_bf16 v[48:51], v[180:183], v[220:223], v[48:51]
	v_mfma_f32_16x16x32_bf16 v[28:31], v[172:175], v[228:231], v[28:31]
	v_mfma_f32_16x16x32_bf16 v[24:27], v[180:183], v[228:231], v[24:27]
	v_mfma_f32_16x16x32_bf16 v[40:43], v[176:179], v[192:195], v[40:43]
	v_mfma_f32_16x16x32_bf16 v[32:35], v[184:187], v[192:195], v[32:35]
	v_mfma_f32_16x16x32_bf16 v[16:19], v[176:179], v[216:219], v[16:19]
	v_mfma_f32_16x16x32_bf16 v[8:11], v[184:187], v[216:219], v[8:11]
	v_mfma_f32_16x16x32_bf16 v[52:55], v[176:179], v[224:227], v[52:55]
	v_mfma_f32_16x16x32_bf16 v[48:51], v[184:187], v[224:227], v[48:51]
	v_mfma_f32_16x16x32_bf16 v[28:31], v[176:179], v[232:235], v[28:31]
	v_mfma_f32_16x16x32_bf16 v[24:27], v[184:187], v[232:235], v[24:27]
	s_setprio 0
	s_barrier
	s_add_i32 s31, s31, 2
	s_add_u32 s8, s8, 0x100
	s_addc_u32 s9, s9, 0
	s_cmp_gt_u32 s31, 13
	s_cbranch_scc0 .LBB0_654
	s_cmpk_lt_u32 s5, 0x100
	s_cbranch_scc0 .LBB0_657
	s_barrier

; #define PG8_STAGE_B(bufoff, gbase) do { _Pragma("unroll") for (int _i = 0; _i < 2; ++_i) \
;         __builtin_amdgcn_global_load_lds((const unsigned*)((const char*)(gbase) + voffB[_i]), (LAS unsigned*)(lds + (bufoff) + ldsw + _i * 8192), 16, 0, 0); } while (0)
; #define PG8_STAGE_A(bufoff, gbase, UA) do { _Pragma("unroll") for (int _i = 0; _i < 2; ++_i) \
;         __builtin_amdgcn_global_load_lds((const unsigned*)((const char*)(gbase) + (UA)[_i]), (LAS unsigned*)(lds + (bufoff) + ldsw + _i * 8192), 16, 0, 0); } while (0)
; #define PG8_LDA(dst, b, h) do { _Pragma("unroll") for (int m = 0; m < 4; ++m) dst[m] = PG8_LD8(lds + PG8_SA(b, h) + aoff + m * 2048); } while (0)
; #define PG8_LDB(dst, b, h) do { _Pragma("unroll") for (int n = 0; n < 2; ++n) dst[n] = PG8_LD8(lds + PG8_SB(b, h) + boff + n * 2048); } while (0)
; #define PG8_WAIT_V(n) asm volatile("s_waitcnt vmcnt(" #n ")" ::: "memory")
; #define PG8_WAIT_L(n) asm volatile("s_waitcnt lgkmcnt(" #n ")" ::: "memory")
; #define PG8_BAR __builtin_amdgcn_s_barrier()
; #define PG8_SCHED __builtin_amdgcn_sched_barrier(0)
; template <class Epi, class Sched, bool GATHER, bool FP8 = false>
; __device__ __forceinline__ void gemm_phase(LAS unsigned char* lds, const Gemm g, const Sched& S, const Epi& E, const int wave_s) {
;     ...
;             const bool last = (t == nt - 2);
;             const char* a1 = cA + (size_t)(t + 1) * kstep;
;             const char* a2 = last ? nA : cA + (size_t)(t + 2) * kstep; const char* b2 = last ? nB : cB + (size_t)(t + 2) * kstep;
;             const char* a3 = a2 + kstep; const char* b3 = b2 + kstep;
;             unsigned u2[2][2];
; #pragma unroll
;             for (int h = 0; h < 2; ++h)
; #pragma unroll
;                 for (int i = 0; i < 2; ++i) u2[h][i] = (GATHER && last) ? uAn[h][i] : uAc[h][i];
;             PG8_LDB(B0, 0, 0); PG8_LDB(B1, 0, 1); PG8_SCHED; PG8_LDA(At, 0, 0); PG8_STAGE_A(PG8_SA(1, 1), a1, uAc[1]);
;             PG8_WAIT_V(8); PG8_WAIT_L(0); PG8_BAR; PG8_MMA(0, 0, At, B0); PG8_MMA(0, 1, At, B1); PG8_BAR; PG8_SCHED;
;             PG8_LDA(At, 0, 1); PG8_STAGE_B(PG8_SB(0, 0), b2); PG8_STAGE_B(PG8_SB(0, 1), b2 + hstepB); PG8_STAGE_A(PG8_SA(0, 0), a2, u2[0]);
;             PG8_WAIT_V(8); PG8_WAIT_L(0); PG8_BAR; PG8_MMA(1, 0, At, B0); PG8_MMA(1, 1, At, B1); PG8_BAR; PG8_SCHED;
.LBB0_765:
	s_add_u32 s0, s42, 0x80
	s_addc_u32 s1, s43, 0
	s_cmp_eq_u32 s60, 12
	s_cselect_b32 s1, s15, s1
	s_cselect_b32 s0, s57, s0
	s_cselect_b32 s45, s13, s59
	s_cselect_b32 s44, s56, s58
	s_add_i32 s2, 0, 0x10000
	v_add_u32_e32 v142, s2, v145
	s_add_i32 s4, 0, 0x14000
	ds_read_b128 v[148:151], v142
	ds_read_b128 v[154:157], v142 offset:1024
	ds_read_b128 v[158:161], v142 offset:2048
	ds_read_b128 v[164:167], v142 offset:3072
	v_add_u32_e32 v142, s4, v145
	ds_read_b128 v[168:171], v142
	ds_read_b128 v[172:175], v142 offset:1024
	ds_read_b128 v[176:179], v142 offset:2048
	ds_read_b128 v[180:183], v142 offset:3072
	v_lshl_add_u64 v[142:143], s[42:43], 0, v[138:139]
	s_add_i32 m0, s47, 0xc000
	ds_read_b128 v[184:187], v147
	ds_read_b128 v[188:191], v147 offset:1024
	ds_read_b128 v[192:195], v147 offset:2048
	ds_read_b128 v[212:215], v147 offset:3072
	ds_read_b128 v[216:219], v147 offset:4096
	ds_read_b128 v[220:223], v147 offset:5120
	ds_read_b128 v[224:227], v147 offset:6144
	ds_read_b128 v[228:231], v147 offset:7168
	global_load_lds_dwordx4 v[142:143], off
	v_lshl_add_u64 v[142:143], s[42:43], 0, v[140:141]
	s_add_i32 m0, s47, 0xe000
	s_nop 0
	global_load_lds_dwordx4 v[142:143], off
	s_waitcnt vmcnt(8)
	s_waitcnt lgkmcnt(0)
	s_barrier
	s_setprio 1
	s_waitcnt lgkmcnt(0)
	v_mfma_f32_16x16x32_bf16 v[124:127], v[148:151], v[184:187], v[124:127]
	v_mfma_f32_16x16x32_bf16 v[120:123], v[158:161], v[184:187], v[120:123]
	v_mfma_f32_16x16x32_bf16 v[116:119], v[148:151], v[192:195], v[116:119]
	v_mfma_f32_16x16x32_bf16 v[108:111], v[158:161], v[192:195], v[108:111]
	v_mfma_f32_16x16x32_bf16 v[100:103], v[148:151], v[216:219], v[100:103]
	v_mfma_f32_16x16x32_bf16 v[92:95], v[158:161], v[216:219], v[92:95]
	v_mfma_f32_16x16x32_bf16 v[80:83], v[148:151], v[224:227], v[80:83]
	v_mfma_f32_16x16x32_bf16 v[72:75], v[158:161], v[224:227], v[72:75]
	v_mfma_f32_16x16x32_bf16 v[124:127], v[154:157], v[188:191], v[124:127]
	v_mfma_f32_16x16x32_bf16 v[120:123], v[164:167], v[188:191], v[120:123]
	v_mfma_f32_16x16x32_bf16 v[116:119], v[154:157], v[212:215], v[116:119]
	v_mfma_f32_16x16x32_bf16 v[108:111], v[164:167], v[212:215], v[108:111]
	v_mfma_f32_16x16x32_bf16 v[100:103], v[154:157], v[220:223], v[100:103]
	v_mfma_f32_16x16x32_bf16 v[92:95], v[164:167], v[220:223], v[92:95]
	v_mfma_f32_16x16x32_bf16 v[80:83], v[154:157], v[228:231], v[80:83]
	v_mfma_f32_16x16x32_bf16 v[72:75], v[164:167], v[228:231], v[72:75]
	v_mfma_f32_16x16x32_bf16 v[112:115], v[168:171], v[184:187], v[112:115]
	v_mfma_f32_16x16x32_bf16 v[104:107], v[176:179], v[184:187], v[104:107]
	v_mfma_f32_16x16x32_bf16 v[96:99], v[168:171], v[192:195], v[96:99]
	v_mfma_f32_16x16x32_bf16 v[88:91], v[176:179], v[192:195], v[88:91]
	v_mfma_f32_16x16x32_bf16 v[84:87], v[168:171], v[216:219], v[84:87]
	v_mfma_f32_16x16x32_bf16 v[76:79], v[176:179], v[216:219], v[76:79]
	v_mfma_f32_16x16x32_bf16 v[68:71], v[168:171], v[224:227], v[68:71]
	v_mfma_f32_16x16x32_bf16 v[64:67], v[176:179], v[224:227], v[64:67]
	v_mfma_f32_16x16x32_bf16 v[112:115], v[172:175], v[188:191], v[112:115]
	v_mfma_f32_16x16x32_bf16 v[104:107], v[180:183], v[188:191], v[104:107]
	v_mfma_f32_16x16x32_bf16 v[96:99], v[172:175], v[212:215], v[96:99]
	v_mfma_f32_16x16x32_bf16 v[88:91], v[180:183], v[212:215], v[88:91]
	v_mfma_f32_16x16x32_bf16 v[84:87], v[172:175], v[220:223], v[84:87]
	v_mfma_f32_16x16x32_bf16 v[76:79], v[180:183], v[220:223], v[76:79]
	v_mfma_f32_16x16x32_bf16 v[68:71], v[172:175], v[228:231], v[68:71]
	v_mfma_f32_16x16x32_bf16 v[64:67], v[180:183], v[228:231], v[64:67]
	s_setprio 0
	s_barrier
	s_add_i32 s2, s2, s5
	v_lshl_add_u64 v[142:143], s[44:45], 0, v[152:153]
	s_mov_b32 m0, s2
	ds_read_b128 v[184:187], v147 offset:16384
	ds_read_b128 v[188:191], v147 offset:17408
	ds_read_b128 v[192:195], v147 offset:18432
	ds_read_b128 v[212:215], v147 offset:19456
	ds_read_b128 v[216:219], v147 offset:20480
	ds_read_b128 v[220:223], v147 offset:21504
	ds_read_b128 v[224:227], v147 offset:22528
	ds_read_b128 v[228:231], v147 offset:23552
	global_load_lds_dwordx4 v[142:143], off
	s_add_i32 m0, s2, 0x2000
	s_add_u32 s2, s44, 0x40000
	v_lshl_add_u64 v[232:233], s[44:45], 0, v[128:129]
	s_addc_u32 s3, s45, 0
	s_add_i32 s4, s4, s5
	global_load_lds_dwordx4 v[232:233], off
	v_lshl_add_u64 v[234:235], s[2:3], 0, v[152:153]
	s_mov_b32 m0, s4
	v_lshl_add_u64 v[236:237], s[0:1], 0, v[132:133]
	global_load_lds_dwordx4 v[234:235], off
	v_lshl_add_u64 v[234:235], s[2:3], 0, v[128:129]
	s_add_i32 m0, s4, 0x2000
	s_nop 0
	global_load_lds_dwordx4 v[234:235], off
	v_lshl_add_u64 v[234:235], s[0:1], 0, v[130:131]
	s_mov_b32 m0, s47
	s_nop 0
	global_load_lds_dwordx4 v[234:235], off
	s_mov_b32 m0, s48
	s_nop 0
	global_load_lds_dwordx4 v[236:237], off
	s_waitcnt vmcnt(8)
	s_waitcnt lgkmcnt(0)
	s_barrier
; #define PG8_STAGE_A(bufoff, gbase, UA) do { _Pragma("unroll") for (int _i = 0; _i < 2; ++_i) \
;         __builtin_amdgcn_global_load_lds((const unsigned*)((const char*)(gbase) + (UA)[_i]), (LAS unsigned*)(lds + (bufoff) + ldsw + _i * 8192), 16, 0, 0); } while (0)
; #define PG8_LDA(dst, b, h) do { _Pragma("unroll") for (int m = 0; m < 4; ++m) dst[m] = PG8_LD8(lds + PG8_SA(b, h) + aoff + m * 2048); } while (0)
; #define PG8_LDB(dst, b, h) do { _Pragma("unroll") for (int n = 0; n < 2; ++n) dst[n] = PG8_LD8(lds + PG8_SB(b, h) + boff + n * 2048); } while (0)
; #define PG8_WAIT_V(n) asm volatile("s_waitcnt vmcnt(" #n ")" ::: "memory")
; #define PG8_WAIT_L(n) asm volatile("s_waitcnt lgkmcnt(" #n ")" ::: "memory")
; #define PG8_BAR __builtin_amdgcn_s_barrier()
; #define PG8_SCHED __builtin_amdgcn_sched_barrier(0)
; template <class Epi, class Sched, bool GATHER, bool FP8 = false>
; __device__ __forceinline__ void gemm_phase(LAS unsigned char* lds, const Gemm g, const Sched& S, const Epi& E, const int wave_s) {
;     ...
;             PG8_WAIT_V(8); PG8_WAIT_L(0); PG8_BAR; PG8_MMA(1, 0, At, B0); PG8_MMA(1, 1, At, B1); PG8_BAR; PG8_SCHED;
;             PG8_LDB(B0, 1, 0); PG8_LDB(B1, 1, 1); PG8_SCHED; PG8_LDA(At, 1, 0); PG8_STAGE_A(PG8_SA(0, 1), a2, u2[1]);
;             PG8_WAIT_V(8); PG8_WAIT_L(0); PG8_BAR; PG8_MMA(0, 0, At, B0); PG8_MMA(0, 1, At, B1); PG8_BAR; PG8_SCHED;
	s_setprio 1
	s_waitcnt lgkmcnt(0)
	v_mfma_f32_16x16x32_bf16 v[60:63], v[148:151], v[184:187], v[60:63]
	v_mfma_f32_16x16x32_bf16 v[56:59], v[158:161], v[184:187], v[56:59]
	v_mfma_f32_16x16x32_bf16 v[44:47], v[148:151], v[192:195], v[44:47]
	v_mfma_f32_16x16x32_bf16 v[36:39], v[158:161], v[192:195], v[36:39]
	v_mfma_f32_16x16x32_bf16 v[20:23], v[148:151], v[216:219], v[20:23]
	v_mfma_f32_16x16x32_bf16 v[12:15], v[158:161], v[216:219], v[12:15]
	v_mfma_f32_16x16x32_bf16 v[4:7], v[148:151], v[224:227], v[4:7]
	v_mfma_f32_16x16x32_bf16 v[0:3], v[158:161], v[224:227], v[0:3]
	v_mfma_f32_16x16x32_bf16 v[60:63], v[154:157], v[188:191], v[60:63]
	v_mfma_f32_16x16x32_bf16 v[56:59], v[164:167], v[188:191], v[56:59]
	v_mfma_f32_16x16x32_bf16 v[44:47], v[154:157], v[212:215], v[44:47]
	v_mfma_f32_16x16x32_bf16 v[36:39], v[164:167], v[212:215], v[36:39]
	v_mfma_f32_16x16x32_bf16 v[20:23], v[154:157], v[220:223], v[20:23]
	v_mfma_f32_16x16x32_bf16 v[12:15], v[164:167], v[220:223], v[12:15]
	v_mfma_f32_16x16x32_bf16 v[4:7], v[154:157], v[228:231], v[4:7]
	v_mfma_f32_16x16x32_bf16 v[0:3], v[164:167], v[228:231], v[0:3]
	v_mfma_f32_16x16x32_bf16 v[40:43], v[168:171], v[184:187], v[40:43]
	v_mfma_f32_16x16x32_bf16 v[32:35], v[176:179], v[184:187], v[32:35]
	v_mfma_f32_16x16x32_bf16 v[16:19], v[168:171], v[192:195], v[16:19]
	v_mfma_f32_16x16x32_bf16 v[8:11], v[176:179], v[192:195], v[8:11]
	v_mfma_f32_16x16x32_bf16 v[52:55], v[168:171], v[216:219], v[52:55]
	v_mfma_f32_16x16x32_bf16 v[48:51], v[176:179], v[216:219], v[48:51]
	v_mfma_f32_16x16x32_bf16 v[28:31], v[168:171], v[224:227], v[28:31]
	v_mfma_f32_16x16x32_bf16 v[24:27], v[176:179], v[224:227], v[24:27]
	v_mfma_f32_16x16x32_bf16 v[40:43], v[172:175], v[188:191], v[40:43]
	v_mfma_f32_16x16x32_bf16 v[32:35], v[180:183], v[188:191], v[32:35]
	v_mfma_f32_16x16x32_bf16 v[16:19], v[172:175], v[212:215], v[16:19]
	v_mfma_f32_16x16x32_bf16 v[8:11], v[180:183], v[212:215], v[8:11]
	v_mfma_f32_16x16x32_bf16 v[52:55], v[172:175], v[220:223], v[52:55]
	v_mfma_f32_16x16x32_bf16 v[48:51], v[180:183], v[220:223], v[48:51]
	v_mfma_f32_16x16x32_bf16 v[28:31], v[172:175], v[228:231], v[28:31]
	v_mfma_f32_16x16x32_bf16 v[24:27], v[180:183], v[228:231], v[24:27]
	s_setprio 0
	s_barrier
	s_add_i32 s2, 0, 0x18000
	s_add_i32 s3, 0, 0x1c000
	v_add_u32_e32 v164, s2, v145
	v_add_u32_e32 v180, s3, v145
	ds_read_b128 v[148:151], v164
	ds_read_b128 v[154:157], v164 offset:1024
	ds_read_b128 v[158:161], v164 offset:2048
	ds_read_b128 v[164:167], v164 offset:3072
	ds_read_b128 v[168:171], v180
	ds_read_b128 v[172:175], v180 offset:1024
	ds_read_b128 v[176:179], v180 offset:2048
	ds_read_b128 v[180:183], v180 offset:3072
	s_mov_b32 m0, s49
	v_lshl_add_u64 v[238:239], s[0:1], 0, v[134:135]
	ds_read_b128 v[184:187], v147 offset:32768
	ds_read_b128 v[188:191], v147 offset:33792
	ds_read_b128 v[192:195], v147 offset:34816
	ds_read_b128 v[212:215], v147 offset:35840
	ds_read_b128 v[216:219], v147 offset:36864
	ds_read_b128 v[220:223], v147 offset:37888
	ds_read_b128 v[224:227], v147 offset:38912
	ds_read_b128 v[228:231], v147 offset:39936
	global_load_lds_dwordx4 v[238:239], off
	v_lshl_add_u64 v[238:239], s[0:1], 0, v[136:137]
	s_mov_b32 m0, s50
	s_nop 0
	global_load_lds_dwordx4 v[238:239], off
	s_waitcnt vmcnt(8)
	s_waitcnt lgkmcnt(0)
	s_barrier
	s_setprio 1
	s_waitcnt lgkmcnt(0)
	v_mfma_f32_16x16x32_bf16 v[124:127], v[148:151], v[184:187], v[124:127]
	v_mfma_f32_16x16x32_bf16 v[120:123], v[158:161], v[184:187], v[120:123]
	v_mfma_f32_16x16x32_bf16 v[116:119], v[148:151], v[192:195], v[116:119]
	v_mfma_f32_16x16x32_bf16 v[108:111], v[158:161], v[192:195], v[108:111]
	v_mfma_f32_16x16x32_bf16 v[100:103], v[148:151], v[216:219], v[100:103]
	v_mfma_f32_16x16x32_bf16 v[92:95], v[158:161], v[216:219], v[92:95]
	v_mfma_f32_16x16x32_bf16 v[80:83], v[148:151], v[224:227], v[80:83]
	v_mfma_f32_16x16x32_bf16 v[72:75], v[158:161], v[224:227], v[72:75]
	v_mfma_f32_16x16x32_bf16 v[124:127], v[154:157], v[188:191], v[124:127]
	v_mfma_f32_16x16x32_bf16 v[120:123], v[164:167], v[188:191], v[120:123]
	v_mfma_f32_16x16x32_bf16 v[116:119], v[154:157], v[212:215], v[116:119]
	v_mfma_f32_16x16x32_bf16 v[108:111], v[164:167], v[212:215], v[108:111]
	v_mfma_f32_16x16x32_bf16 v[100:103], v[154:157], v[220:223], v[100:103]
	v_mfma_f32_16x16x32_bf16 v[92:95], v[164:167], v[220:223], v[92:95]
	v_mfma_f32_16x16x32_bf16 v[80:83], v[154:157], v[228:231], v[80:83]
	v_mfma_f32_16x16x32_bf16 v[72:75], v[164:167], v[228:231], v[72:75]
	v_mfma_f32_16x16x32_bf16 v[112:115], v[168:171], v[184:187], v[112:115]
	v_mfma_f32_16x16x32_bf16 v[104:107], v[176:179], v[184:187], v[104:107]
	v_mfma_f32_16x16x32_bf16 v[96:99], v[168:171], v[192:195], v[96:99]
	v_mfma_f32_16x16x32_bf16 v[88:91], v[176:179], v[192:195], v[88:91]
	v_mfma_f32_16x16x32_bf16 v[84:87], v[168:171], v[216:219], v[84:87]
	v_mfma_f32_16x16x32_bf16 v[76:79], v[176:179], v[216:219], v[76:79]
	v_mfma_f32_16x16x32_bf16 v[68:71], v[168:171], v[224:227], v[68:71]
	v_mfma_f32_16x16x32_bf16 v[64:67], v[176:179], v[224:227], v[64:67]
	v_mfma_f32_16x16x32_bf16 v[112:115], v[172:175], v[188:191], v[112:115]
	v_mfma_f32_16x16x32_bf16 v[104:107], v[180:183], v[188:191], v[104:107]
	v_mfma_f32_16x16x32_bf16 v[96:99], v[172:175], v[212:215], v[96:99]
	v_mfma_f32_16x16x32_bf16 v[88:91], v[180:183], v[212:215], v[88:91]
	v_mfma_f32_16x16x32_bf16 v[84:87], v[172:175], v[220:223], v[84:87]
	v_mfma_f32_16x16x32_bf16 v[76:79], v[180:183], v[220:223], v[76:79]
	v_mfma_f32_16x16x32_bf16 v[68:71], v[172:175], v[228:231], v[68:71]
	v_mfma_f32_16x16x32_bf16 v[64:67], v[180:183], v[228:231], v[64:67]
	s_setprio 0
	s_barrier
; #define PG8_STAGE_B(bufoff, gbase) do { _Pragma("unroll") for (int _i = 0; _i < 2; ++_i) \
;         __builtin_amdgcn_global_load_lds((const unsigned*)((const char*)(gbase) + voffB[_i]), (LAS unsigned*)(lds + (bufoff) + ldsw + _i * 8192), 16, 0, 0); } while (0)
; #define PG8_STAGE_A(bufoff, gbase, UA) do { _Pragma("unroll") for (int _i = 0; _i < 2; ++_i) \
;         __builtin_amdgcn_global_load_lds((const unsigned*)((const char*)(gbase) + (UA)[_i]), (LAS unsigned*)(lds + (bufoff) + ldsw + _i * 8192), 16, 0, 0); } while (0)
; #define PG8_LDA(dst, b, h) do { _Pragma("unroll") for (int m = 0; m < 4; ++m) dst[m] = PG8_LD8(lds + PG8_SA(b, h) + aoff + m * 2048); } while (0)
; #define PG8_WAIT_V(n) asm volatile("s_waitcnt vmcnt(" #n ")" ::: "memory")
; #define PG8_WAIT_L(n) asm volatile("s_waitcnt lgkmcnt(" #n ")" ::: "memory")
; #define PG8_BAR __builtin_amdgcn_s_barrier()
; #define PG8_SCHED __builtin_amdgcn_sched_barrier(0)
; template <class Epi, class Sched, bool GATHER, bool FP8 = false>
; __device__ __forceinline__ void gemm_phase(LAS unsigned char* lds, const Gemm g, const Sched& S, const Epi& E, const int wave_s) {
;     ...
;             PG8_LDA(At, 1, 1); PG8_STAGE_B(PG8_SB(1, 0), b3); PG8_STAGE_B(PG8_SB(1, 1), b3 + hstepB); PG8_STAGE_A(PG8_SA(1, 0), a3, u2[0]);
;             PG8_WAIT_V(8); PG8_WAIT_L(0); PG8_BAR; PG8_MMA(1, 0, At, B0); PG8_MMA(1, 1, At, B1); PG8_BAR; PG8_SCHED;
;         }
;         if (wr == 0) PG8_BAR;
	s_add_i32 s0, s2, s5
	v_lshl_add_u64 v[142:143], v[142:143], 0, s[96:97]
	s_mov_b32 m0, s0
	ds_read_b128 v[184:187], v147 offset:49152
	ds_read_b128 v[188:191], v147 offset:50176
	ds_read_b128 v[192:195], v147 offset:51200
	ds_read_b128 v[212:215], v147 offset:52224
	ds_read_b128 v[216:219], v147 offset:53248
	ds_read_b128 v[220:223], v147 offset:54272
	ds_read_b128 v[224:227], v147 offset:55296
	ds_read_b128 v[228:231], v147 offset:56320
	global_load_lds_dwordx4 v[142:143], off
	s_add_i32 m0, s0, 0x2000
	s_add_u32 s0, s44, 0x40080
	v_lshl_add_u64 v[142:143], v[232:233], 0, s[96:97]
	s_addc_u32 s1, s45, 0
	s_add_i32 s2, s3, s5
	global_load_lds_dwordx4 v[142:143], off
	v_lshl_add_u64 v[142:143], s[0:1], 0, v[152:153]
	s_mov_b32 m0, s2
	s_nop 0
	global_load_lds_dwordx4 v[142:143], off
	v_lshl_add_u64 v[142:143], s[0:1], 0, v[128:129]
	s_add_i32 m0, s2, 0x2000
	s_nop 0
	global_load_lds_dwordx4 v[142:143], off
	v_lshl_add_u64 v[142:143], v[234:235], 0, s[96:97]
	s_mov_b32 m0, s51
	s_nop 0
	global_load_lds_dwordx4 v[142:143], off
	v_lshl_add_u64 v[142:143], v[236:237], 0, s[96:97]
	s_mov_b32 m0, s52
	s_nop 0
	global_load_lds_dwordx4 v[142:143], off
	s_waitcnt vmcnt(8)
	s_waitcnt lgkmcnt(0)
	s_barrier
	s_setprio 1
	s_waitcnt lgkmcnt(0)
	v_mfma_f32_16x16x32_bf16 v[60:63], v[148:151], v[184:187], v[60:63]
	v_mfma_f32_16x16x32_bf16 v[56:59], v[158:161], v[184:187], v[56:59]
	v_mfma_f32_16x16x32_bf16 v[44:47], v[148:151], v[192:195], v[44:47]
	v_mfma_f32_16x16x32_bf16 v[36:39], v[158:161], v[192:195], v[36:39]
	v_mfma_f32_16x16x32_bf16 v[20:23], v[148:151], v[216:219], v[20:23]
	v_mfma_f32_16x16x32_bf16 v[12:15], v[158:161], v[216:219], v[12:15]
	v_mfma_f32_16x16x32_bf16 v[4:7], v[148:151], v[224:227], v[4:7]
	v_mfma_f32_16x16x32_bf16 v[0:3], v[158:161], v[224:227], v[0:3]
	v_mfma_f32_16x16x32_bf16 v[60:63], v[154:157], v[188:191], v[60:63]
	v_mfma_f32_16x16x32_bf16 v[56:59], v[164:167], v[188:191], v[56:59]
	v_mfma_f32_16x16x32_bf16 v[44:47], v[154:157], v[212:215], v[44:47]
	v_mfma_f32_16x16x32_bf16 v[36:39], v[164:167], v[212:215], v[36:39]
	v_mfma_f32_16x16x32_bf16 v[20:23], v[154:157], v[220:223], v[20:23]
	v_mfma_f32_16x16x32_bf16 v[12:15], v[164:167], v[220:223], v[12:15]
	v_mfma_f32_16x16x32_bf16 v[4:7], v[154:157], v[228:231], v[4:7]
	v_mfma_f32_16x16x32_bf16 v[0:3], v[164:167], v[228:231], v[0:3]
	v_mfma_f32_16x16x32_bf16 v[40:43], v[168:171], v[184:187], v[40:43]
	v_mfma_f32_16x16x32_bf16 v[32:35], v[176:179], v[184:187], v[32:35]
	v_mfma_f32_16x16x32_bf16 v[16:19], v[168:171], v[192:195], v[16:19]
	v_mfma_f32_16x16x32_bf16 v[8:11], v[176:179], v[192:195], v[8:11]
	v_mfma_f32_16x16x32_bf16 v[52:55], v[168:171], v[216:219], v[52:55]
	v_mfma_f32_16x16x32_bf16 v[48:51], v[176:179], v[216:219], v[48:51]
	v_mfma_f32_16x16x32_bf16 v[28:31], v[168:171], v[224:227], v[28:31]
	v_mfma_f32_16x16x32_bf16 v[24:27], v[176:179], v[224:227], v[24:27]
	v_mfma_f32_16x16x32_bf16 v[40:43], v[172:175], v[188:191], v[40:43]
	v_mfma_f32_16x16x32_bf16 v[32:35], v[180:183], v[188:191], v[32:35]
	v_mfma_f32_16x16x32_bf16 v[16:19], v[172:175], v[212:215], v[16:19]
	v_mfma_f32_16x16x32_bf16 v[8:11], v[180:183], v[212:215], v[8:11]
	v_mfma_f32_16x16x32_bf16 v[52:55], v[172:175], v[220:223], v[52:55]
	v_mfma_f32_16x16x32_bf16 v[48:51], v[180:183], v[220:223], v[48:51]
	v_mfma_f32_16x16x32_bf16 v[28:31], v[172:175], v[228:231], v[28:31]
	v_mfma_f32_16x16x32_bf16 v[24:27], v[180:183], v[228:231], v[24:27]
	s_setprio 0
	s_barrier
	s_add_i32 s60, s60, 2
	s_add_u32 s42, s42, 0x100
	s_addc_u32 s43, s43, 0
	s_add_u32 s58, s58, 0x100
	s_addc_u32 s59, s59, 0
	s_cmp_gt_u32 s60, 13
	s_cbranch_scc0 .LBB0_765
	s_and_b64 vcc, exec, s[10:11]
	s_cbranch_vccz .LBB0_768
	s_barrier

; #define PG8_STAGE_B(bufoff, gbase) do { _Pragma("unroll") for (int _i = 0; _i < 2; ++_i) \
;         __builtin_amdgcn_global_load_lds((const unsigned*)((const char*)(gbase) + voffB[_i]), (LAS unsigned*)(lds + (bufoff) + ldsw + _i * 8192), 16, 0, 0); } while (0)
; #define PG8_STAGE_A(bufoff, gbase, UA) do { _Pragma("unroll") for (int _i = 0; _i < 2; ++_i) \
;         __builtin_amdgcn_global_load_lds((const unsigned*)((const char*)(gbase) + (UA)[_i]), (LAS unsigned*)(lds + (bufoff) + ldsw + _i * 8192), 16, 0, 0); } while (0)
; #define PG8_LDA(dst, b, h) do { _Pragma("unroll") for (int m = 0; m < 4; ++m) dst[m] = PG8_LD8(lds + PG8_SA(b, h) + aoff + m * 2048); } while (0)
; #define PG8_LDB(dst, b, h) do { _Pragma("unroll") for (int n = 0; n < 2; ++n) dst[n] = PG8_LD8(lds + PG8_SB(b, h) + boff + n * 2048); } while (0)
; #define PG8_WAIT_V(n) asm volatile("s_waitcnt vmcnt(" #n ")" ::: "memory")
; #define PG8_WAIT_L(n) asm volatile("s_waitcnt lgkmcnt(" #n ")" ::: "memory")
; #define PG8_BAR __builtin_amdgcn_s_barrier()
; #define PG8_SCHED __builtin_amdgcn_sched_barrier(0)
; template <class Epi, class Sched, bool GATHER, bool FP8 = false>
; __device__ __forceinline__ void gemm_phase(LAS unsigned char* lds, const Gemm g, const Sched& S, const Epi& E, const int wave_s) {
;     ...
;             const bool last = (t == nt - 2);
;             const char* a1 = cA + (size_t)(t + 1) * kstep;
;             const char* a2 = last ? nA : cA + (size_t)(t + 2) * kstep; const char* b2 = last ? nB : cB + (size_t)(t + 2) * kstep;
;             const char* a3 = a2 + kstep; const char* b3 = b2 + kstep;
;             unsigned u2[2][2];
; #pragma unroll
;             for (int h = 0; h < 2; ++h)
; #pragma unroll
;                 for (int i = 0; i < 2; ++i) u2[h][i] = (GATHER && last) ? uAn[h][i] : uAc[h][i];
;             PG8_LDB(B0, 0, 0); PG8_LDB(B1, 0, 1); PG8_SCHED; PG8_LDA(At, 0, 0); PG8_STAGE_A(PG8_SA(1, 1), a1, uAc[1]);
;             PG8_WAIT_V(8); PG8_WAIT_L(0); PG8_BAR; PG8_MMA(0, 0, At, B0); PG8_MMA(0, 1, At, B1); PG8_BAR; PG8_SCHED;
;             PG8_LDA(At, 0, 1); PG8_STAGE_B(PG8_SB(0, 0), b2); PG8_STAGE_B(PG8_SB(0, 1), b2 + hstepB); PG8_STAGE_A(PG8_SA(0, 0), a2, u2[0]);
;             PG8_WAIT_V(8); PG8_WAIT_L(0); PG8_BAR; PG8_MMA(1, 0, At, B0); PG8_MMA(1, 1, At, B1); PG8_BAR; PG8_SCHED;
.LBB0_1471:
	s_add_u32 s2, s78, s42
	s_addc_u32 s3, s79, s43
	s_add_u32 s4, s2, 0x72600100
	s_addc_u32 s20, s3, 0
	s_add_u32 s21, s17, s42
	s_addc_u32 s22, s66, s43
	s_cmpk_eq_i32 s42, 0x300
	s_cselect_b64 vcc, -1, 0
	s_and_b64 s[2:3], vcc, exec
	s_cselect_b32 s49, s37, s20
	s_cselect_b32 s48, s36, s4
	s_cselect_b32 s47, s0, s22
	s_cselect_b32 s46, s1, s21
	s_add_i32 s68, 0, 0x10000
	s_add_i32 s69, 0, 0x14000
	v_add_u32_e32 v0, s68, v216
	v_add_u32_e32 v12, s69, v216
	ds_read_b128 v[16:19], v0
	ds_read_b128 v[20:23], v0 offset:1024
	ds_read_b128 v[24:27], v0 offset:2048
	ds_read_b128 v[28:31], v0 offset:3072
	ds_read_b128 v[0:3], v12
	ds_read_b128 v[4:7], v12 offset:1024
	ds_read_b128 v[8:11], v12 offset:2048
	ds_read_b128 v[12:15], v12 offset:3072
	v_cndmask_b32_e32 v152, v176, v218, vcc
	v_cndmask_b32_e32 v188, v178, v219, vcc
	v_cndmask_b32_e32 v183, v180, v220, vcc
	v_cndmask_b32_e32 v181, v182, v221, vcc
	v_lshl_add_u64 v[190:191], v[186:187], 0, s[42:43]
	s_add_i32 m0, s45, 0xc000
	ds_read_b128 v[222:225], v217
	ds_read_b128 v[226:229], v217 offset:1024
	ds_read_b128 v[230:233], v217 offset:2048
	ds_read_b128 v[234:237], v217 offset:3072
	ds_read_b128 v[238:241], v217 offset:4096
	ds_read_b128 v[242:245], v217 offset:5120
	ds_read_b128 v[164:167], v217 offset:6144
	ds_read_b128 v[168:171], v217 offset:7168
	global_load_lds_dwordx4 v[190:191], off
	v_lshl_add_u64 v[190:191], v[184:185], 0, s[42:43]
	s_add_i32 m0, s45, 0xe000
	s_nop 0
	global_load_lds_dwordx4 v[190:191], off
	s_waitcnt vmcnt(8)
	s_waitcnt lgkmcnt(0)
	s_barrier
	s_setprio 1
	s_waitcnt lgkmcnt(0)
	v_mfma_scale_f32_16x16x128_f8f6f4 v[158:161], v[16:23], v[222:229], v[158:161], v163, v196 op_sel_hi:[0,0,0]
	v_mfma_scale_f32_16x16x128_f8f6f4 v[154:157], v[24:31], v[222:229], v[154:157], v163, v196 op_sel_hi:[0,0,0]
	v_mfma_scale_f32_16x16x128_f8f6f4 v[140:143], v[16:23], v[230:237], v[140:143], v163, v196 op_sel_hi:[0,0,0]
	v_mfma_scale_f32_16x16x128_f8f6f4 v[136:139], v[24:31], v[230:237], v[136:139], v163, v196 op_sel_hi:[0,0,0]
	v_mfma_scale_f32_16x16x128_f8f6f4 v[124:127], v[16:23], v[238:245], v[124:127], v163, v196 op_sel_hi:[0,0,0]
	v_mfma_scale_f32_16x16x128_f8f6f4 v[120:123], v[24:31], v[238:245], v[120:123], v163, v196 op_sel_hi:[0,0,0]
	v_mfma_scale_f32_16x16x128_f8f6f4 v[108:111], v[16:23], v[164:171], v[108:111], v163, v196 op_sel_hi:[0,0,0]
	v_mfma_scale_f32_16x16x128_f8f6f4 v[104:107], v[24:31], v[164:171], v[104:107], v163, v196 op_sel_hi:[0,0,0]
	v_mfma_scale_f32_16x16x128_f8f6f4 v[148:151], v[0:7], v[222:229], v[148:151], v163, v196 op_sel_hi:[0,0,0]
	v_mfma_scale_f32_16x16x128_f8f6f4 v[144:147], v[8:15], v[222:229], v[144:147], v163, v196 op_sel_hi:[0,0,0]
	v_mfma_scale_f32_16x16x128_f8f6f4 v[132:135], v[0:7], v[230:237], v[132:135], v163, v196 op_sel_hi:[0,0,0]
	v_mfma_scale_f32_16x16x128_f8f6f4 v[128:131], v[8:15], v[230:237], v[128:131], v163, v196 op_sel_hi:[0,0,0]
	v_mfma_scale_f32_16x16x128_f8f6f4 v[116:119], v[0:7], v[238:245], v[116:119], v163, v196 op_sel_hi:[0,0,0]
	v_mfma_scale_f32_16x16x128_f8f6f4 v[112:115], v[8:15], v[238:245], v[112:115], v163, v196 op_sel_hi:[0,0,0]
	v_mfma_scale_f32_16x16x128_f8f6f4 v[100:103], v[0:7], v[164:171], v[100:103], v163, v196 op_sel_hi:[0,0,0]
	v_mfma_scale_f32_16x16x128_f8f6f4 v[96:99], v[8:15], v[164:171], v[96:99], v163, v196 op_sel_hi:[0,0,0]
	s_setprio 0
	s_barrier
	s_add_i32 s2, s68, s54
	v_lshl_add_u64 v[190:191], s[46:47], 0, v[172:173]
	s_mov_b32 m0, s2
	ds_read_b128 v[164:167], v217 offset:16384
	ds_read_b128 v[168:171], v217 offset:17408
	ds_read_b128 v[222:225], v217 offset:18432
	ds_read_b128 v[226:229], v217 offset:19456
	ds_read_b128 v[230:233], v217 offset:20480
	ds_read_b128 v[234:237], v217 offset:21504
	ds_read_b128 v[238:241], v217 offset:22528
	ds_read_b128 v[242:245], v217 offset:23552
	global_load_lds_dwordx4 v[190:191], off
	s_add_i32 m0, s2, 0x2000
	s_add_u32 s2, s46, 0x20000
	v_lshl_add_u64 v[192:193], s[46:47], 0, v[174:175]
	s_addc_u32 s3, s47, 0
	s_add_i32 s4, s69, s54
	global_load_lds_dwordx4 v[192:193], off
	v_lshl_add_u64 v[194:195], s[2:3], 0, v[172:173]
	s_mov_b32 m0, s4
	v_mov_b32_e32 v189, v153
	global_load_lds_dwordx4 v[194:195], off
	v_lshl_add_u64 v[194:195], s[2:3], 0, v[174:175]
	s_add_i32 m0, s4, 0x2000
	s_nop 0
	global_load_lds_dwordx4 v[194:195], off
	s_mov_b32 m0, s45
	v_lshl_add_u64 v[194:195], s[48:49], 0, v[152:153]
	global_load_lds_dwordx4 v152, s[48:49]
	s_mov_b32 m0, s57
	s_nop 0
	global_load_lds_dwordx4 v188, s[48:49]
	s_waitcnt vmcnt(8)
	s_waitcnt lgkmcnt(0)
	v_lshl_add_u64 v[188:189], s[48:49], 0, v[188:189]
	s_barrier
	s_setprio 1
	s_waitcnt lgkmcnt(0)
	v_mfma_scale_f32_16x16x128_f8f6f4 v[92:95], v[16:23], v[164:171], v[92:95], v163, v196 op_sel_hi:[0,0,0]
	v_mfma_scale_f32_16x16x128_f8f6f4 v[88:91], v[24:31], v[164:171], v[88:91], v163, v196 op_sel_hi:[0,0,0]
	v_mfma_scale_f32_16x16x128_f8f6f4 v[76:79], v[16:23], v[222:229], v[76:79], v163, v196 op_sel_hi:[0,0,0]
	v_mfma_scale_f32_16x16x128_f8f6f4 v[72:75], v[24:31], v[222:229], v[72:75], v163, v196 op_sel_hi:[0,0,0]
	v_mfma_scale_f32_16x16x128_f8f6f4 v[60:63], v[16:23], v[230:237], v[60:63], v163, v196 op_sel_hi:[0,0,0]
	v_mfma_scale_f32_16x16x128_f8f6f4 v[56:59], v[24:31], v[230:237], v[56:59], v163, v196 op_sel_hi:[0,0,0]
	v_mfma_scale_f32_16x16x128_f8f6f4 v[44:47], v[16:23], v[238:245], v[44:47], v163, v196 op_sel_hi:[0,0,0]
	v_mfma_scale_f32_16x16x128_f8f6f4 v[40:43], v[24:31], v[238:245], v[40:43], v163, v196 op_sel_hi:[0,0,0]
	v_mfma_scale_f32_16x16x128_f8f6f4 v[84:87], v[0:7], v[164:171], v[84:87], v163, v196 op_sel_hi:[0,0,0]
	v_mfma_scale_f32_16x16x128_f8f6f4 v[80:83], v[8:15], v[164:171], v[80:83], v163, v196 op_sel_hi:[0,0,0]
	v_mfma_scale_f32_16x16x128_f8f6f4 v[68:71], v[0:7], v[222:229], v[68:71], v163, v196 op_sel_hi:[0,0,0]
	v_mfma_scale_f32_16x16x128_f8f6f4 v[64:67], v[8:15], v[222:229], v[64:67], v163, v196 op_sel_hi:[0,0,0]
	v_mfma_scale_f32_16x16x128_f8f6f4 v[52:55], v[0:7], v[230:237], v[52:55], v163, v196 op_sel_hi:[0,0,0]
	v_mfma_scale_f32_16x16x128_f8f6f4 v[48:51], v[8:15], v[230:237], v[48:51], v163, v196 op_sel_hi:[0,0,0]
	v_mfma_scale_f32_16x16x128_f8f6f4 v[32:35], v[0:7], v[238:245], v[32:35], v163, v196 op_sel_hi:[0,0,0]
	v_mfma_scale_f32_16x16x128_f8f6f4 v[36:39], v[8:15], v[238:245], v[36:39], v163, v196 op_sel_hi:[0,0,0]
	s_setprio 0
	s_barrier
; #define PG8_STAGE_B(bufoff, gbase) do { _Pragma("unroll") for (int _i = 0; _i < 2; ++_i) \
;         __builtin_amdgcn_global_load_lds((const unsigned*)((const char*)(gbase) + voffB[_i]), (LAS unsigned*)(lds + (bufoff) + ldsw + _i * 8192), 16, 0, 0); } while (0)
; #define PG8_STAGE_A(bufoff, gbase, UA) do { _Pragma("unroll") for (int _i = 0; _i < 2; ++_i) \
;         __builtin_amdgcn_global_load_lds((const unsigned*)((const char*)(gbase) + (UA)[_i]), (LAS unsigned*)(lds + (bufoff) + ldsw + _i * 8192), 16, 0, 0); } while (0)
; #define PG8_LDA(dst, b, h) do { _Pragma("unroll") for (int m = 0; m < 4; ++m) dst[m] = PG8_LD8(lds + PG8_SA(b, h) + aoff + m * 2048); } while (0)
; #define PG8_LDB(dst, b, h) do { _Pragma("unroll") for (int n = 0; n < 2; ++n) dst[n] = PG8_LD8(lds + PG8_SB(b, h) + boff + n * 2048); } while (0)
; #define PG8_WAIT_V(n) asm volatile("s_waitcnt vmcnt(" #n ")" ::: "memory")
; #define PG8_WAIT_L(n) asm volatile("s_waitcnt lgkmcnt(" #n ")" ::: "memory")
; #define PG8_BAR __builtin_amdgcn_s_barrier()
; #define PG8_SCHED __builtin_amdgcn_sched_barrier(0)
; template <class Epi, class Sched, bool GATHER, bool FP8 = false>
; __device__ __forceinline__ void gemm_phase(LAS unsigned char* lds, const Gemm g, const Sched& S, const Epi& E, const int wave_s) {
;     ...
;             PG8_LDB(B0, 1, 0); PG8_LDB(B1, 1, 1); PG8_SCHED; PG8_LDA(At, 1, 0); PG8_STAGE_A(PG8_SA(0, 1), a2, u2[1]);
;             PG8_WAIT_V(8); PG8_WAIT_L(0); PG8_BAR; PG8_MMA(0, 0, At, B0); PG8_MMA(0, 1, At, B1); PG8_BAR; PG8_SCHED;
;             PG8_LDA(At, 1, 1); PG8_STAGE_B(PG8_SB(1, 0), b3); PG8_STAGE_B(PG8_SB(1, 1), b3 + hstepB); PG8_STAGE_A(PG8_SA(1, 0), a3, u2[0]);
;             PG8_WAIT_V(8); PG8_WAIT_L(0); PG8_BAR; PG8_MMA(1, 0, At, B0); PG8_MMA(1, 1, At, B1); PG8_BAR; PG8_SCHED;
;         }
;         if (wr == 0) PG8_BAR;
	s_add_i32 s2, 0, 0x18000
	s_add_i32 s4, 0, 0x1c000
	v_add_u32_e32 v12, s2, v216
	v_add_u32_e32 v28, s4, v216
	ds_read_b128 v[0:3], v12
	ds_read_b128 v[4:7], v12 offset:1024
	ds_read_b128 v[8:11], v12 offset:2048
	ds_read_b128 v[12:15], v12 offset:3072
	ds_read_b128 v[16:19], v28
	ds_read_b128 v[20:23], v28 offset:1024
	ds_read_b128 v[24:27], v28 offset:2048
	ds_read_b128 v[28:31], v28 offset:3072
	s_mov_b32 m0, s58
	ds_read_b128 v[164:167], v217 offset:32768
	ds_read_b128 v[168:171], v217 offset:33792
	ds_read_b128 v[222:225], v217 offset:34816
	ds_read_b128 v[226:229], v217 offset:35840
	ds_read_b128 v[230:233], v217 offset:36864
	ds_read_b128 v[234:237], v217 offset:37888
	ds_read_b128 v[238:241], v217 offset:38912
	ds_read_b128 v[242:245], v217 offset:39936
	global_load_lds_dwordx4 v183, s[48:49]
	s_mov_b32 m0, s59
	s_nop 0
	global_load_lds_dwordx4 v181, s[48:49]
	s_waitcnt vmcnt(8)
	s_waitcnt lgkmcnt(0)
	s_barrier
	s_setprio 1
	s_waitcnt lgkmcnt(0)
	v_mfma_scale_f32_16x16x128_f8f6f4 v[158:161], v[0:7], v[164:171], v[158:161], v163, v196 op_sel_hi:[0,0,0]
	v_mfma_scale_f32_16x16x128_f8f6f4 v[154:157], v[8:15], v[164:171], v[154:157], v163, v196 op_sel_hi:[0,0,0]
	v_mfma_scale_f32_16x16x128_f8f6f4 v[140:143], v[0:7], v[222:229], v[140:143], v163, v196 op_sel_hi:[0,0,0]
	v_mfma_scale_f32_16x16x128_f8f6f4 v[136:139], v[8:15], v[222:229], v[136:139], v163, v196 op_sel_hi:[0,0,0]
	v_mfma_scale_f32_16x16x128_f8f6f4 v[124:127], v[0:7], v[230:237], v[124:127], v163, v196 op_sel_hi:[0,0,0]
	v_mfma_scale_f32_16x16x128_f8f6f4 v[120:123], v[8:15], v[230:237], v[120:123], v163, v196 op_sel_hi:[0,0,0]
	v_mfma_scale_f32_16x16x128_f8f6f4 v[108:111], v[0:7], v[238:245], v[108:111], v163, v196 op_sel_hi:[0,0,0]
	v_mfma_scale_f32_16x16x128_f8f6f4 v[104:107], v[8:15], v[238:245], v[104:107], v163, v196 op_sel_hi:[0,0,0]
	v_mfma_scale_f32_16x16x128_f8f6f4 v[148:151], v[16:23], v[164:171], v[148:151], v163, v196 op_sel_hi:[0,0,0]
	v_mfma_scale_f32_16x16x128_f8f6f4 v[144:147], v[24:31], v[164:171], v[144:147], v163, v196 op_sel_hi:[0,0,0]
	v_mfma_scale_f32_16x16x128_f8f6f4 v[132:135], v[16:23], v[222:229], v[132:135], v163, v196 op_sel_hi:[0,0,0]
	v_mfma_scale_f32_16x16x128_f8f6f4 v[128:131], v[24:31], v[222:229], v[128:131], v163, v196 op_sel_hi:[0,0,0]
	v_mfma_scale_f32_16x16x128_f8f6f4 v[116:119], v[16:23], v[230:237], v[116:119], v163, v196 op_sel_hi:[0,0,0]
	v_mfma_scale_f32_16x16x128_f8f6f4 v[112:115], v[24:31], v[230:237], v[112:115], v163, v196 op_sel_hi:[0,0,0]
	v_mfma_scale_f32_16x16x128_f8f6f4 v[100:103], v[16:23], v[238:245], v[100:103], v163, v196 op_sel_hi:[0,0,0]
	v_mfma_scale_f32_16x16x128_f8f6f4 v[96:99], v[24:31], v[238:245], v[96:99], v163, v196 op_sel_hi:[0,0,0]
	s_setprio 0
	s_barrier
	s_add_i32 s2, s2, s54
	v_lshl_add_u64 v[190:191], v[190:191], 0, s[96:97]
	s_mov_b32 m0, s2
	ds_read_b128 v[164:167], v217 offset:49152
	ds_read_b128 v[168:171], v217 offset:50176
	ds_read_b128 v[222:225], v217 offset:51200
	ds_read_b128 v[226:229], v217 offset:52224
	ds_read_b128 v[230:233], v217 offset:53248
	ds_read_b128 v[234:237], v217 offset:54272
	ds_read_b128 v[238:241], v217 offset:55296
	ds_read_b128 v[242:245], v217 offset:56320
	global_load_lds_dwordx4 v[190:191], off
	s_add_i32 m0, s2, 0x2000
	s_add_u32 s2, s46, 0x20080
	v_lshl_add_u64 v[190:191], v[192:193], 0, s[96:97]
	s_addc_u32 s3, s47, 0
	s_add_i32 s4, s4, s54
	global_load_lds_dwordx4 v[190:191], off
	v_lshl_add_u64 v[190:191], s[2:3], 0, v[172:173]
	s_mov_b32 m0, s4
	v_lshl_add_u64 v[188:189], v[188:189], 0, s[96:97]
	global_load_lds_dwordx4 v[190:191], off
	v_lshl_add_u64 v[190:191], s[2:3], 0, v[174:175]
	s_add_i32 m0, s4, 0x2000
	s_nop 0
	global_load_lds_dwordx4 v[190:191], off
	v_lshl_add_u64 v[190:191], v[194:195], 0, s[96:97]
	s_mov_b32 m0, s60
	s_nop 0
	global_load_lds_dwordx4 v[190:191], off
	s_mov_b32 m0, s61
	s_nop 0
	global_load_lds_dwordx4 v[188:189], off
	s_waitcnt vmcnt(8)
	s_waitcnt lgkmcnt(0)
	s_barrier
	s_setprio 1
	s_waitcnt lgkmcnt(0)
	v_mfma_scale_f32_16x16x128_f8f6f4 v[92:95], v[0:7], v[164:171], v[92:95], v163, v196 op_sel_hi:[0,0,0]
	v_mfma_scale_f32_16x16x128_f8f6f4 v[88:91], v[8:15], v[164:171], v[88:91], v163, v196 op_sel_hi:[0,0,0]
	v_mfma_scale_f32_16x16x128_f8f6f4 v[76:79], v[0:7], v[222:229], v[76:79], v163, v196 op_sel_hi:[0,0,0]
	v_mfma_scale_f32_16x16x128_f8f6f4 v[72:75], v[8:15], v[222:229], v[72:75], v163, v196 op_sel_hi:[0,0,0]
	v_mfma_scale_f32_16x16x128_f8f6f4 v[60:63], v[0:7], v[230:237], v[60:63], v163, v196 op_sel_hi:[0,0,0]
	v_mfma_scale_f32_16x16x128_f8f6f4 v[56:59], v[8:15], v[230:237], v[56:59], v163, v196 op_sel_hi:[0,0,0]
	v_mfma_scale_f32_16x16x128_f8f6f4 v[44:47], v[0:7], v[238:245], v[44:47], v163, v196 op_sel_hi:[0,0,0]
	v_mfma_scale_f32_16x16x128_f8f6f4 v[40:43], v[8:15], v[238:245], v[40:43], v163, v196 op_sel_hi:[0,0,0]
	v_mfma_scale_f32_16x16x128_f8f6f4 v[84:87], v[16:23], v[164:171], v[84:87], v163, v196 op_sel_hi:[0,0,0]
	v_mfma_scale_f32_16x16x128_f8f6f4 v[80:83], v[24:31], v[164:171], v[80:83], v163, v196 op_sel_hi:[0,0,0]
	v_mfma_scale_f32_16x16x128_f8f6f4 v[68:71], v[16:23], v[222:229], v[68:71], v163, v196 op_sel_hi:[0,0,0]
	v_mfma_scale_f32_16x16x128_f8f6f4 v[64:67], v[24:31], v[222:229], v[64:67], v163, v196 op_sel_hi:[0,0,0]
	v_mfma_scale_f32_16x16x128_f8f6f4 v[52:55], v[16:23], v[230:237], v[52:55], v163, v196 op_sel_hi:[0,0,0]
	v_mfma_scale_f32_16x16x128_f8f6f4 v[48:51], v[24:31], v[230:237], v[48:51], v163, v196 op_sel_hi:[0,0,0]
	v_mfma_scale_f32_16x16x128_f8f6f4 v[32:35], v[16:23], v[238:245], v[32:35], v163, v196 op_sel_hi:[0,0,0]
	v_mfma_scale_f32_16x16x128_f8f6f4 v[36:39], v[24:31], v[238:245], v[36:39], v163, v196 op_sel_hi:[0,0,0]
	s_setprio 0
	s_barrier
	s_add_i32 s67, s67, 2
	s_add_u32 s42, s42, 0x100
	s_addc_u32 s43, s43, 0
	s_cmp_gt_u32 s67, 5
	s_cbranch_scc0 .LBB0_1471
	s_and_b64 vcc, exec, s[14:15]
	s_cbranch_vccz .LBB0_1474
	s_barrier

; #define PG8_STAGE_B(bufoff, gbase) do { _Pragma("unroll") for (int _i = 0; _i < 2; ++_i) \
;         __builtin_amdgcn_global_load_lds((const unsigned*)((const char*)(gbase) + voffB[_i]), (LAS unsigned*)(lds + (bufoff) + ldsw + _i * 8192), 16, 0, 0); } while (0)
; #define PG8_STAGE_A(bufoff, gbase, UA) do { _Pragma("unroll") for (int _i = 0; _i < 2; ++_i) \
;         __builtin_amdgcn_global_load_lds((const unsigned*)((const char*)(gbase) + (UA)[_i]), (LAS unsigned*)(lds + (bufoff) + ldsw + _i * 8192), 16, 0, 0); } while (0)
; #define PG8_LDA(dst, b, h) do { _Pragma("unroll") for (int m = 0; m < 4; ++m) dst[m] = PG8_LD8(lds + PG8_SA(b, h) + aoff + m * 2048); } while (0)
; #define PG8_LDB(dst, b, h) do { _Pragma("unroll") for (int n = 0; n < 2; ++n) dst[n] = PG8_LD8(lds + PG8_SB(b, h) + boff + n * 2048); } while (0)
; #define PG8_WAIT_V(n) asm volatile("s_waitcnt vmcnt(" #n ")" ::: "memory")
; #define PG8_WAIT_L(n) asm volatile("s_waitcnt lgkmcnt(" #n ")" ::: "memory")
; #define PG8_BAR __builtin_amdgcn_s_barrier()
; #define PG8_SCHED __builtin_amdgcn_sched_barrier(0)
; template <class Epi, class Sched, bool GATHER, bool FP8 = false>
; __device__ __forceinline__ void gemm_phase(LAS unsigned char* lds, const Gemm g, const Sched& S, const Epi& E, const int wave_s) {
;     ...
;             const bool last = (t == nt - 2);
;             const char* a1 = cA + (size_t)(t + 1) * kstep;
;             const char* a2 = last ? nA : cA + (size_t)(t + 2) * kstep; const char* b2 = last ? nB : cB + (size_t)(t + 2) * kstep;
;             const char* a3 = a2 + kstep; const char* b3 = b2 + kstep;
;             unsigned u2[2][2];
; #pragma unroll
;             for (int h = 0; h < 2; ++h)
; #pragma unroll
;                 for (int i = 0; i < 2; ++i) u2[h][i] = (GATHER && last) ? uAn[h][i] : uAc[h][i];
;             PG8_LDB(B0, 0, 0); PG8_LDB(B1, 0, 1); PG8_SCHED; PG8_LDA(At, 0, 0); PG8_STAGE_A(PG8_SA(1, 1), a1, uAc[1]);
;             PG8_WAIT_V(8); PG8_WAIT_L(0); PG8_BAR; PG8_MMA(0, 0, At, B0); PG8_MMA(0, 1, At, B1); PG8_BAR; PG8_SCHED;
;             PG8_LDA(At, 0, 1); PG8_STAGE_B(PG8_SB(0, 0), b2); PG8_STAGE_B(PG8_SB(0, 1), b2 + hstepB); PG8_STAGE_A(PG8_SA(0, 0), a2, u2[0]);
;             PG8_WAIT_V(8); PG8_WAIT_L(0); PG8_BAR; PG8_MMA(1, 0, At, B0); PG8_MMA(1, 1, At, B1); PG8_BAR; PG8_SCHED;
.LBB0_1571:
	s_add_u32 s2, s50, 0x80
	s_addc_u32 s3, s51, 0
	s_cmp_eq_u32 s74, 4
	s_cselect_b32 s55, s17, s3
	s_cselect_b32 s54, s19, s2
	s_cselect_b32 s53, s0, s73
	s_cselect_b32 s52, s1, s72
	s_add_i32 s76, 0, 0x10000
	s_add_i32 s77, 0, 0x14000
	v_add_u32_e32 v0, s76, v212
	v_add_u32_e32 v12, s77, v212
	ds_read_b128 v[16:19], v0
	ds_read_b128 v[20:23], v0 offset:1024
	ds_read_b128 v[24:27], v0 offset:2048
	ds_read_b128 v[28:31], v0 offset:3072
	ds_read_b128 v[0:3], v12
	ds_read_b128 v[4:7], v12 offset:1024
	ds_read_b128 v[8:11], v12 offset:2048
	ds_read_b128 v[12:15], v12 offset:3072
	v_lshl_add_u64 v[232:233], s[50:51], 0, v[186:187]
	s_add_i32 m0, s47, 0xc000
	ds_read_b128 v[164:167], v215
	ds_read_b128 v[168:171], v215 offset:1024
	ds_read_b128 v[188:191], v215 offset:2048
	ds_read_b128 v[192:195], v215 offset:3072
	ds_read_b128 v[216:219], v215 offset:4096
	ds_read_b128 v[220:223], v215 offset:5120
	ds_read_b128 v[224:227], v215 offset:6144
	ds_read_b128 v[228:231], v215 offset:7168
	global_load_lds_dwordx4 v[232:233], off
	v_lshl_add_u64 v[232:233], s[50:51], 0, v[184:185]
	s_add_i32 m0, s47, 0xe000
	s_nop 0
	global_load_lds_dwordx4 v[232:233], off
	s_waitcnt vmcnt(8)
	s_waitcnt lgkmcnt(0)
	s_barrier
	s_setprio 1
	s_waitcnt lgkmcnt(0)
	v_mfma_scale_f32_16x16x128_f8f6f4 v[158:161], v[16:23], v[164:171], v[158:161], v202, v196 op_sel_hi:[0,0,0]
	v_mfma_scale_f32_16x16x128_f8f6f4 v[154:157], v[24:31], v[164:171], v[154:157], v202, v196 op_sel_hi:[0,0,0]
	v_mfma_scale_f32_16x16x128_f8f6f4 v[140:143], v[16:23], v[188:195], v[140:143], v202, v196 op_sel_hi:[0,0,0]
	v_mfma_scale_f32_16x16x128_f8f6f4 v[136:139], v[24:31], v[188:195], v[136:139], v202, v196 op_sel_hi:[0,0,0]
	v_mfma_scale_f32_16x16x128_f8f6f4 v[124:127], v[16:23], v[216:223], v[124:127], v202, v196 op_sel_hi:[0,0,0]
	v_mfma_scale_f32_16x16x128_f8f6f4 v[120:123], v[24:31], v[216:223], v[120:123], v202, v196 op_sel_hi:[0,0,0]
	v_mfma_scale_f32_16x16x128_f8f6f4 v[108:111], v[16:23], v[224:231], v[108:111], v202, v196 op_sel_hi:[0,0,0]
	v_mfma_scale_f32_16x16x128_f8f6f4 v[104:107], v[24:31], v[224:231], v[104:107], v202, v196 op_sel_hi:[0,0,0]
	v_mfma_scale_f32_16x16x128_f8f6f4 v[148:151], v[0:7], v[164:171], v[148:151], v202, v196 op_sel_hi:[0,0,0]
	v_mfma_scale_f32_16x16x128_f8f6f4 v[144:147], v[8:15], v[164:171], v[144:147], v202, v196 op_sel_hi:[0,0,0]
	v_mfma_scale_f32_16x16x128_f8f6f4 v[132:135], v[0:7], v[188:195], v[132:135], v202, v196 op_sel_hi:[0,0,0]
	v_mfma_scale_f32_16x16x128_f8f6f4 v[128:131], v[8:15], v[188:195], v[128:131], v202, v196 op_sel_hi:[0,0,0]
	v_mfma_scale_f32_16x16x128_f8f6f4 v[116:119], v[0:7], v[216:223], v[116:119], v202, v196 op_sel_hi:[0,0,0]
	v_mfma_scale_f32_16x16x128_f8f6f4 v[112:115], v[8:15], v[216:223], v[112:115], v202, v196 op_sel_hi:[0,0,0]
	v_mfma_scale_f32_16x16x128_f8f6f4 v[100:103], v[0:7], v[224:231], v[100:103], v202, v196 op_sel_hi:[0,0,0]
	v_mfma_scale_f32_16x16x128_f8f6f4 v[96:99], v[8:15], v[224:231], v[96:99], v202, v196 op_sel_hi:[0,0,0]
	s_setprio 0
	s_barrier
	s_add_i32 s2, s76, s63
	v_lshl_add_u64 v[188:189], s[52:53], 0, v[172:173]
	s_mov_b32 m0, s2
	ds_read_b128 v[164:167], v215 offset:16384
	ds_read_b128 v[168:171], v215 offset:17408
	ds_read_b128 v[216:219], v215 offset:18432
	ds_read_b128 v[220:223], v215 offset:19456
	ds_read_b128 v[224:227], v215 offset:20480
	ds_read_b128 v[228:231], v215 offset:21504
	ds_read_b128 v[232:235], v215 offset:22528
	ds_read_b128 v[236:239], v215 offset:23552
	global_load_lds_dwordx4 v[188:189], off
	s_add_i32 m0, s2, 0x2000
	s_add_u32 s2, s52, 0x20000
	v_lshl_add_u64 v[190:191], s[52:53], 0, v[174:175]
	s_addc_u32 s3, s53, 0
	s_add_i32 s4, s77, s63
	global_load_lds_dwordx4 v[190:191], off
	v_lshl_add_u64 v[192:193], s[2:3], 0, v[172:173]
	s_mov_b32 m0, s4
	v_lshl_add_u64 v[194:195], s[54:55], 0, v[178:179]
	global_load_lds_dwordx4 v[192:193], off
	v_lshl_add_u64 v[192:193], s[2:3], 0, v[174:175]
	s_add_i32 m0, s4, 0x2000
	s_nop 0
	global_load_lds_dwordx4 v[192:193], off
	v_lshl_add_u64 v[192:193], s[54:55], 0, v[176:177]
	s_mov_b32 m0, s47
	s_nop 0
	global_load_lds_dwordx4 v[192:193], off
	s_mov_b32 m0, s49
	s_nop 0
	global_load_lds_dwordx4 v[194:195], off
	s_waitcnt vmcnt(8)
	s_waitcnt lgkmcnt(0)
	s_barrier
	s_setprio 1
	s_waitcnt lgkmcnt(0)
	v_mfma_scale_f32_16x16x128_f8f6f4 v[92:95], v[16:23], v[164:171], v[92:95], v202, v196 op_sel_hi:[0,0,0]
	v_mfma_scale_f32_16x16x128_f8f6f4 v[88:91], v[24:31], v[164:171], v[88:91], v202, v196 op_sel_hi:[0,0,0]
	v_mfma_scale_f32_16x16x128_f8f6f4 v[76:79], v[16:23], v[216:223], v[76:79], v202, v196 op_sel_hi:[0,0,0]
	v_mfma_scale_f32_16x16x128_f8f6f4 v[72:75], v[24:31], v[216:223], v[72:75], v202, v196 op_sel_hi:[0,0,0]
	v_mfma_scale_f32_16x16x128_f8f6f4 v[52:55], v[16:23], v[224:231], v[52:55], v202, v196 op_sel_hi:[0,0,0]
	v_mfma_scale_f32_16x16x128_f8f6f4 v[48:51], v[24:31], v[224:231], v[48:51], v202, v196 op_sel_hi:[0,0,0]
	v_mfma_scale_f32_16x16x128_f8f6f4 v[36:39], v[16:23], v[232:239], v[36:39], v202, v196 op_sel_hi:[0,0,0]
	v_mfma_scale_f32_16x16x128_f8f6f4 v[32:35], v[24:31], v[232:239], v[32:35], v202, v196 op_sel_hi:[0,0,0]
	v_mfma_scale_f32_16x16x128_f8f6f4 v[84:87], v[0:7], v[164:171], v[84:87], v202, v196 op_sel_hi:[0,0,0]
	v_mfma_scale_f32_16x16x128_f8f6f4 v[80:83], v[8:15], v[164:171], v[80:83], v202, v196 op_sel_hi:[0,0,0]
	v_mfma_scale_f32_16x16x128_f8f6f4 v[68:71], v[0:7], v[216:223], v[68:71], v202, v196 op_sel_hi:[0,0,0]
	v_mfma_scale_f32_16x16x128_f8f6f4 v[60:63], v[8:15], v[216:223], v[60:63], v202, v196 op_sel_hi:[0,0,0]
	v_mfma_scale_f32_16x16x128_f8f6f4 v[64:67], v[0:7], v[224:231], v[64:67], v202, v196 op_sel_hi:[0,0,0]
	v_mfma_scale_f32_16x16x128_f8f6f4 v[56:59], v[8:15], v[224:231], v[56:59], v202, v196 op_sel_hi:[0,0,0]
	v_mfma_scale_f32_16x16x128_f8f6f4 v[44:47], v[0:7], v[232:239], v[44:47], v202, v196 op_sel_hi:[0,0,0]
	v_mfma_scale_f32_16x16x128_f8f6f4 v[40:43], v[8:15], v[232:239], v[40:43], v202, v196 op_sel_hi:[0,0,0]
	s_setprio 0
	s_barrier
; #define PG8_STAGE_B(bufoff, gbase) do { _Pragma("unroll") for (int _i = 0; _i < 2; ++_i) \
;         __builtin_amdgcn_global_load_lds((const unsigned*)((const char*)(gbase) + voffB[_i]), (LAS unsigned*)(lds + (bufoff) + ldsw + _i * 8192), 16, 0, 0); } while (0)
; #define PG8_STAGE_A(bufoff, gbase, UA) do { _Pragma("unroll") for (int _i = 0; _i < 2; ++_i) \
;         __builtin_amdgcn_global_load_lds((const unsigned*)((const char*)(gbase) + (UA)[_i]), (LAS unsigned*)(lds + (bufoff) + ldsw + _i * 8192), 16, 0, 0); } while (0)
; #define PG8_LDA(dst, b, h) do { _Pragma("unroll") for (int m = 0; m < 4; ++m) dst[m] = PG8_LD8(lds + PG8_SA(b, h) + aoff + m * 2048); } while (0)
; #define PG8_LDB(dst, b, h) do { _Pragma("unroll") for (int n = 0; n < 2; ++n) dst[n] = PG8_LD8(lds + PG8_SB(b, h) + boff + n * 2048); } while (0)
; #define PG8_WAIT_V(n) asm volatile("s_waitcnt vmcnt(" #n ")" ::: "memory")
; #define PG8_WAIT_L(n) asm volatile("s_waitcnt lgkmcnt(" #n ")" ::: "memory")
; #define PG8_BAR __builtin_amdgcn_s_barrier()
; #define PG8_SCHED __builtin_amdgcn_sched_barrier(0)
; template <class Epi, class Sched, bool GATHER, bool FP8 = false>
; __device__ __forceinline__ void gemm_phase(LAS unsigned char* lds, const Gemm g, const Sched& S, const Epi& E, const int wave_s) {
;     ...
;             PG8_LDB(B0, 1, 0); PG8_LDB(B1, 1, 1); PG8_SCHED; PG8_LDA(At, 1, 0); PG8_STAGE_A(PG8_SA(0, 1), a2, u2[1]);
;             PG8_WAIT_V(8); PG8_WAIT_L(0); PG8_BAR; PG8_MMA(0, 0, At, B0); PG8_MMA(0, 1, At, B1); PG8_BAR; PG8_SCHED;
;             PG8_LDA(At, 1, 1); PG8_STAGE_B(PG8_SB(1, 0), b3); PG8_STAGE_B(PG8_SB(1, 1), b3 + hstepB); PG8_STAGE_A(PG8_SA(1, 0), a3, u2[0]);
;             PG8_WAIT_V(8); PG8_WAIT_L(0); PG8_BAR; PG8_MMA(1, 0, At, B0); PG8_MMA(1, 1, At, B1); PG8_BAR; PG8_SCHED;
;         }
;         if (wr == 0) PG8_BAR;
	s_add_i32 s2, 0, 0x18000
	s_add_i32 s4, 0, 0x1c000
	v_add_u32_e32 v12, s2, v212
	v_add_u32_e32 v28, s4, v212
	ds_read_b128 v[0:3], v12
	ds_read_b128 v[4:7], v12 offset:1024
	ds_read_b128 v[8:11], v12 offset:2048
	ds_read_b128 v[12:15], v12 offset:3072
	ds_read_b128 v[16:19], v28
	ds_read_b128 v[20:23], v28 offset:1024
	ds_read_b128 v[24:27], v28 offset:2048
	ds_read_b128 v[28:31], v28 offset:3072
	s_mov_b32 m0, s66
	v_lshl_add_u64 v[240:241], s[54:55], 0, v[180:181]
	ds_read_b128 v[164:167], v215 offset:32768
	ds_read_b128 v[168:171], v215 offset:33792
	ds_read_b128 v[216:219], v215 offset:34816
	ds_read_b128 v[220:223], v215 offset:35840
	ds_read_b128 v[224:227], v215 offset:36864
	ds_read_b128 v[228:231], v215 offset:37888
	ds_read_b128 v[232:235], v215 offset:38912
	ds_read_b128 v[236:239], v215 offset:39936
	global_load_lds_dwordx4 v[240:241], off
	v_lshl_add_u64 v[240:241], s[54:55], 0, v[182:183]
	s_mov_b32 m0, s67
	s_nop 0
	global_load_lds_dwordx4 v[240:241], off
	s_waitcnt vmcnt(8)
	s_waitcnt lgkmcnt(0)
	s_barrier
	s_setprio 1
	s_waitcnt lgkmcnt(0)
	v_mfma_scale_f32_16x16x128_f8f6f4 v[158:161], v[0:7], v[164:171], v[158:161], v202, v196 op_sel_hi:[0,0,0]
	v_mfma_scale_f32_16x16x128_f8f6f4 v[154:157], v[8:15], v[164:171], v[154:157], v202, v196 op_sel_hi:[0,0,0]
	v_mfma_scale_f32_16x16x128_f8f6f4 v[140:143], v[0:7], v[216:223], v[140:143], v202, v196 op_sel_hi:[0,0,0]
	v_mfma_scale_f32_16x16x128_f8f6f4 v[136:139], v[8:15], v[216:223], v[136:139], v202, v196 op_sel_hi:[0,0,0]
	v_mfma_scale_f32_16x16x128_f8f6f4 v[124:127], v[0:7], v[224:231], v[124:127], v202, v196 op_sel_hi:[0,0,0]
	v_mfma_scale_f32_16x16x128_f8f6f4 v[120:123], v[8:15], v[224:231], v[120:123], v202, v196 op_sel_hi:[0,0,0]
	v_mfma_scale_f32_16x16x128_f8f6f4 v[108:111], v[0:7], v[232:239], v[108:111], v202, v196 op_sel_hi:[0,0,0]
	v_mfma_scale_f32_16x16x128_f8f6f4 v[104:107], v[8:15], v[232:239], v[104:107], v202, v196 op_sel_hi:[0,0,0]
	v_mfma_scale_f32_16x16x128_f8f6f4 v[148:151], v[16:23], v[164:171], v[148:151], v202, v196 op_sel_hi:[0,0,0]
	v_mfma_scale_f32_16x16x128_f8f6f4 v[144:147], v[24:31], v[164:171], v[144:147], v202, v196 op_sel_hi:[0,0,0]
	v_mfma_scale_f32_16x16x128_f8f6f4 v[132:135], v[16:23], v[216:223], v[132:135], v202, v196 op_sel_hi:[0,0,0]
	v_mfma_scale_f32_16x16x128_f8f6f4 v[128:131], v[24:31], v[216:223], v[128:131], v202, v196 op_sel_hi:[0,0,0]
	v_mfma_scale_f32_16x16x128_f8f6f4 v[116:119], v[16:23], v[224:231], v[116:119], v202, v196 op_sel_hi:[0,0,0]
	v_mfma_scale_f32_16x16x128_f8f6f4 v[112:115], v[24:31], v[224:231], v[112:115], v202, v196 op_sel_hi:[0,0,0]
	v_mfma_scale_f32_16x16x128_f8f6f4 v[100:103], v[16:23], v[232:239], v[100:103], v202, v196 op_sel_hi:[0,0,0]
	v_mfma_scale_f32_16x16x128_f8f6f4 v[96:99], v[24:31], v[232:239], v[96:99], v202, v196 op_sel_hi:[0,0,0]
	s_setprio 0
	s_barrier
	s_add_i32 s2, s2, s63
	v_lshl_add_u64 v[188:189], v[188:189], 0, s[96:97]
	s_mov_b32 m0, s2
	ds_read_b128 v[164:167], v215 offset:49152
	ds_read_b128 v[168:171], v215 offset:50176
	ds_read_b128 v[216:219], v215 offset:51200
	ds_read_b128 v[220:223], v215 offset:52224
	ds_read_b128 v[224:227], v215 offset:53248
	ds_read_b128 v[228:231], v215 offset:54272
	ds_read_b128 v[232:235], v215 offset:55296
	ds_read_b128 v[236:239], v215 offset:56320
	global_load_lds_dwordx4 v[188:189], off
	s_add_i32 m0, s2, 0x2000
	s_add_u32 s2, s52, 0x20080
	v_lshl_add_u64 v[188:189], v[190:191], 0, s[96:97]
	s_addc_u32 s3, s53, 0
	s_add_i32 s4, s4, s63
	global_load_lds_dwordx4 v[188:189], off
	v_lshl_add_u64 v[188:189], s[2:3], 0, v[172:173]
	s_mov_b32 m0, s4
	s_nop 0
	global_load_lds_dwordx4 v[188:189], off
	v_lshl_add_u64 v[188:189], s[2:3], 0, v[174:175]
	s_add_i32 m0, s4, 0x2000
	s_nop 0
	global_load_lds_dwordx4 v[188:189], off
	v_lshl_add_u64 v[188:189], v[192:193], 0, s[96:97]
	s_mov_b32 m0, s68
	s_nop 0
	global_load_lds_dwordx4 v[188:189], off
	v_lshl_add_u64 v[188:189], v[194:195], 0, s[96:97]
	s_mov_b32 m0, s69
	s_nop 0
	global_load_lds_dwordx4 v[188:189], off
	s_waitcnt vmcnt(8)
	s_waitcnt lgkmcnt(0)
	s_barrier
	s_setprio 1
	s_waitcnt lgkmcnt(0)
	v_mfma_scale_f32_16x16x128_f8f6f4 v[92:95], v[0:7], v[164:171], v[92:95], v202, v196 op_sel_hi:[0,0,0]
	v_mfma_scale_f32_16x16x128_f8f6f4 v[88:91], v[8:15], v[164:171], v[88:91], v202, v196 op_sel_hi:[0,0,0]
	v_mfma_scale_f32_16x16x128_f8f6f4 v[76:79], v[0:7], v[216:223], v[76:79], v202, v196 op_sel_hi:[0,0,0]
	v_mfma_scale_f32_16x16x128_f8f6f4 v[72:75], v[8:15], v[216:223], v[72:75], v202, v196 op_sel_hi:[0,0,0]
	v_mfma_scale_f32_16x16x128_f8f6f4 v[52:55], v[0:7], v[224:231], v[52:55], v202, v196 op_sel_hi:[0,0,0]
	v_mfma_scale_f32_16x16x128_f8f6f4 v[48:51], v[8:15], v[224:231], v[48:51], v202, v196 op_sel_hi:[0,0,0]
	v_mfma_scale_f32_16x16x128_f8f6f4 v[36:39], v[0:7], v[232:239], v[36:39], v202, v196 op_sel_hi:[0,0,0]
	v_mfma_scale_f32_16x16x128_f8f6f4 v[32:35], v[8:15], v[232:239], v[32:35], v202, v196 op_sel_hi:[0,0,0]
	v_mfma_scale_f32_16x16x128_f8f6f4 v[84:87], v[16:23], v[164:171], v[84:87], v202, v196 op_sel_hi:[0,0,0]
	v_mfma_scale_f32_16x16x128_f8f6f4 v[80:83], v[24:31], v[164:171], v[80:83], v202, v196 op_sel_hi:[0,0,0]
	v_mfma_scale_f32_16x16x128_f8f6f4 v[68:71], v[16:23], v[216:223], v[68:71], v202, v196 op_sel_hi:[0,0,0]
	v_mfma_scale_f32_16x16x128_f8f6f4 v[60:63], v[24:31], v[216:223], v[60:63], v202, v196 op_sel_hi:[0,0,0]
	v_mfma_scale_f32_16x16x128_f8f6f4 v[64:67], v[16:23], v[224:231], v[64:67], v202, v196 op_sel_hi:[0,0,0]
	v_mfma_scale_f32_16x16x128_f8f6f4 v[56:59], v[24:31], v[224:231], v[56:59], v202, v196 op_sel_hi:[0,0,0]
	v_mfma_scale_f32_16x16x128_f8f6f4 v[44:47], v[16:23], v[232:239], v[44:47], v202, v196 op_sel_hi:[0,0,0]
	v_mfma_scale_f32_16x16x128_f8f6f4 v[40:43], v[24:31], v[232:239], v[40:43], v202, v196 op_sel_hi:[0,0,0]
	s_setprio 0
	s_barrier
	s_add_i32 s74, s74, 2
	s_add_u32 s50, s50, 0x100
	s_addc_u32 s51, s51, 0
	s_add_u32 s72, s72, 0x100
	s_addc_u32 s73, s73, 0
	s_cmp_gt_u32 s74, 5
	s_cbranch_scc0 .LBB0_1571
	v_readlane_b32 s72, v254, 26
	s_and_b64 vcc, exec, s[14:15]
	v_readlane_b32 s73, v254, 27
	s_mov_b32 s20, s84
	s_cbranch_vccz .LBB0_1574
	s_barrier
